# v28: v26 + GEMM K-loops: remaining +kstep LDS-DMA addresses folded into SGPR pairs (no 64-bit VALU adds left in the loop)
# speedup vs baseline: 1.0027x; 1.0027x over previous
; #define PG8_STAGE(bufoff, gbase, voff) do { _Pragma("unroll") for (int _i = 0; _i < 2; ++_i) \
;         __builtin_amdgcn_global_load_lds((const unsigned*)((const char*)(gbase) + (voff)[_i]), (PG8_LAS unsigned*)(lds + (bufoff) + ldsw + _i * 8192), 16, 0, 0); } while (0)
; #define PG8_LDA(dst, b, h) do { _Pragma("unroll") for (int m = 0; m < 4; ++m) _Pragma("unroll") for (int k = 0; k < 2; ++k) dst[m][k] = *(const PG8_LAS bf16x8*)(lds + PG8_SA(b, h) + aoff + m * 2048 + k * 1024); } while (0)
; #define PG8_LDB(dst, b, h) do { _Pragma("unroll") for (int n = 0; n < 2; ++n) _Pragma("unroll") for (int k = 0; k < 2; ++k) dst[n][k] = *(const PG8_LAS bf16x8*)(lds + PG8_SB(b, h) + boff + n * 2048 + k * 1024); } while (0)
; #define PG8_MMA(ai, bj, At, Bt) do { __builtin_amdgcn_s_setprio(1); _Pragma("unroll") for (int m = 0; m < 4; ++m) _Pragma("unroll") for (int n = 0; n < 2; ++n) _Pragma("unroll") for (int k = 0; k < 2; ++k) \
;         acc[ai][bj][m][n] = __builtin_amdgcn_mfma_f32_16x16x32_bf16(Bt[n][k], At[m][k], acc[ai][bj][m][n], 0, 0, 0); __builtin_amdgcn_s_setprio(0); } while (0)
; #define PG8_WAIT_V(n) asm volatile("s_waitcnt vmcnt(" #n ")" ::: "memory")
; #define PG8_WAIT_L(n) asm volatile("s_waitcnt lgkmcnt(" #n ")" ::: "memory")
; template <class Epi, class Sched, bool ALIGN_EPI = false, bool SP2 = false>
; __device__ __forceinline__ void gemm_phase(PG8_LAS unsigned char* lds, const Gemm g, const Sched& S, const Epi& E, const int wid) {
;     ...
;             const bool last = (t == nt - 2);
;             const char* a1 = cA + (size_t)(t + 1) * kstep;
;             const char* a2 = last ? nA : cA + (size_t)(t + 2) * kstep; const char* b2 = last ? nB : cB + (size_t)(t + 2) * kstep;
;             const char* a3 = a2 + kstep; const char* b3 = b2 + kstep;
;             if (last && has_next) S.a_ready(nxt);
;             if constexpr (SP2) {
;             PG8_LDB(B0, 0, 0); PG8_LDB(B1, 0, 1); PG8_SCHED; PG8_LDA(At, 0, 0); PG8_STAGE(PG8_SA(1, 1), a1 + hstepA, voffA);
;             PG8_WAIT_V(8); PG8_WAIT_L(0); PG8_BAR; PG8_MMA(0, 0, At, B0); PG8_MMA(0, 1, At, B1); PG8_BAR; PG8_SCHED;
;             PG8_LDA(At, 0, 1); PG8_STAGE(PG8_SB(0, 0), b2, voffB); PG8_STAGE(PG8_SB(0, 1), b2 + hstepB, voffB); PG8_STAGE(PG8_SA(0, 0), a2, voffA);
;             PG8_WAIT_V(8); PG8_WAIT_L(0); PG8_BAR; PG8_MMA(1, 0, At, B0); PG8_MMA(1, 1, At, B1); PG8_BAR; PG8_SCHED;
.LBB0_349:
	ds_read_b128 v[128:131], v183
	ds_read_b128 v[150:153], v183 offset:1024
	ds_read_b128 v[154:157], v183 offset:2048
	ds_read_b128 v[158:161], v183 offset:3072
	ds_read_b128 v[162:165], v184
	ds_read_b128 v[166:169], v184 offset:1024
	ds_read_b128 v[170:173], v184 offset:2048
	ds_read_b128 v[188:191], v184 offset:3072
	s_add_u32 s36, s8, 0xfffc0080
	s_addc_u32 s37, s9, -1
	s_cmp_eq_u32 s75, 12
	s_cselect_b32 s41, s7, s37
	s_cselect_b32 s40, s27, s36
	s_cselect_b32 s37, s25, s74
	s_cselect_b32 s36, s35, s73
	s_add_i32 m0, s46, 0xc000
	ds_read_b128 v[192:195], v185
	ds_read_b128 v[196:199], v185 offset:1024
	ds_read_b128 v[200:203], v185 offset:2048
	ds_read_b128 v[204:207], v185 offset:3072
	ds_read_b128 v[208:211], v185 offset:4096
	ds_read_b128 v[212:215], v185 offset:5120
	ds_read_b128 v[216:219], v185 offset:6144
	ds_read_b128 v[220:223], v185 offset:7168
	global_load_lds_dwordx4 v142, s[8:9]
	s_add_i32 m0, s46, 0xe000
	s_nop 0
	global_load_lds_dwordx4 v144, s[8:9]
	s_waitcnt vmcnt(8) lgkmcnt(0)
	s_barrier
	s_setprio 1
	v_mfma_f32_16x16x32_bf16 v[124:127], v[128:131], v[192:195], v[124:127]
	v_mfma_f32_16x16x32_bf16 v[120:123], v[154:157], v[192:195], v[120:123]
	v_mfma_f32_16x16x32_bf16 v[108:111], v[128:131], v[200:203], v[108:111]
	v_mfma_f32_16x16x32_bf16 v[104:107], v[154:157], v[200:203], v[104:107]
	v_mfma_f32_16x16x32_bf16 v[92:95], v[128:131], v[208:211], v[92:95]
	v_mfma_f32_16x16x32_bf16 v[88:91], v[154:157], v[208:211], v[88:91]
	v_mfma_f32_16x16x32_bf16 v[76:79], v[128:131], v[216:219], v[76:79]
	v_mfma_f32_16x16x32_bf16 v[72:75], v[154:157], v[216:219], v[72:75]
	v_mfma_f32_16x16x32_bf16 v[124:127], v[150:153], v[196:199], v[124:127]
	v_mfma_f32_16x16x32_bf16 v[120:123], v[158:161], v[196:199], v[120:123]
	v_mfma_f32_16x16x32_bf16 v[108:111], v[150:153], v[204:207], v[108:111]
	v_mfma_f32_16x16x32_bf16 v[104:107], v[158:161], v[204:207], v[104:107]
	v_mfma_f32_16x16x32_bf16 v[92:95], v[150:153], v[212:215], v[92:95]
	v_mfma_f32_16x16x32_bf16 v[88:91], v[158:161], v[212:215], v[88:91]
	v_mfma_f32_16x16x32_bf16 v[76:79], v[150:153], v[220:223], v[76:79]
	v_mfma_f32_16x16x32_bf16 v[72:75], v[158:161], v[220:223], v[72:75]
	s_setprio 0
	s_setprio 1
	v_mfma_f32_16x16x32_bf16 v[116:119], v[162:165], v[192:195], v[116:119]
	v_mfma_f32_16x16x32_bf16 v[112:115], v[170:173], v[192:195], v[112:115]
	v_mfma_f32_16x16x32_bf16 v[100:103], v[162:165], v[200:203], v[100:103]
	v_mfma_f32_16x16x32_bf16 v[96:99], v[170:173], v[200:203], v[96:99]
	v_mfma_f32_16x16x32_bf16 v[84:87], v[162:165], v[208:211], v[84:87]
	v_mfma_f32_16x16x32_bf16 v[80:83], v[170:173], v[208:211], v[80:83]
	v_mfma_f32_16x16x32_bf16 v[68:71], v[162:165], v[216:219], v[68:71]
	v_mfma_f32_16x16x32_bf16 v[64:67], v[170:173], v[216:219], v[64:67]
	v_mfma_f32_16x16x32_bf16 v[116:119], v[166:169], v[196:199], v[116:119]
	v_mfma_f32_16x16x32_bf16 v[112:115], v[188:191], v[196:199], v[112:115]
	v_mfma_f32_16x16x32_bf16 v[100:103], v[166:169], v[204:207], v[100:103]
	v_mfma_f32_16x16x32_bf16 v[96:99], v[188:191], v[204:207], v[96:99]
	v_mfma_f32_16x16x32_bf16 v[84:87], v[166:169], v[212:215], v[84:87]
	v_mfma_f32_16x16x32_bf16 v[80:83], v[188:191], v[212:215], v[80:83]
	v_mfma_f32_16x16x32_bf16 v[68:71], v[166:169], v[220:223], v[68:71]
	v_mfma_f32_16x16x32_bf16 v[64:67], v[188:191], v[220:223], v[64:67]
	s_setprio 0
	s_barrier
	s_add_i32 s76, s69, s45
	s_add_u32 s98, s36, 0x80
	s_addc_u32 s99, s37, 0
	s_mov_b32 m0, s76
	ds_read_b128 v[192:195], v185 offset:16384
	ds_read_b128 v[196:199], v185 offset:17408
	ds_read_b128 v[200:203], v185 offset:18432
	ds_read_b128 v[204:207], v185 offset:19456
	ds_read_b128 v[208:211], v185 offset:20480
	ds_read_b128 v[212:215], v185 offset:21504
	ds_read_b128 v[216:219], v185 offset:22528
	ds_read_b128 v[220:223], v185 offset:23552
	global_load_lds_dwordx4 v134, s[36:37]
	s_add_i32 m0, s76, 0x2000
	s_add_u32 s76, s36, 0x40000
	s_addc_u32 s77, s37, 0
	s_add_i32 s78, s70, s45
	global_load_lds_dwordx4 v138, s[36:37]
	s_mov_b32 m0, s78
	s_add_u32 s100, s40, 0x80
	s_addc_u32 s101, s41, 0
	global_load_lds_dwordx4 v134, s[76:77]
	s_add_i32 m0, s78, 0x2000
	s_nop 0
	global_load_lds_dwordx4 v138, s[76:77]
	s_mov_b32 m0, s46
	s_nop 0
	global_load_lds_dwordx4 v132, s[40:41]
	s_mov_b32 m0, s47
	s_nop 0
	global_load_lds_dwordx4 v136, s[40:41]
	s_waitcnt vmcnt(8) lgkmcnt(0)
	s_barrier
	s_setprio 1
	v_mfma_f32_16x16x32_bf16 v[60:63], v[128:131], v[192:195], v[60:63]
	v_mfma_f32_16x16x32_bf16 v[56:59], v[154:157], v[192:195], v[56:59]
	v_mfma_f32_16x16x32_bf16 v[44:47], v[128:131], v[200:203], v[44:47]
	v_mfma_f32_16x16x32_bf16 v[40:43], v[154:157], v[200:203], v[40:43]
	v_mfma_f32_16x16x32_bf16 v[28:31], v[128:131], v[208:211], v[28:31]
	v_mfma_f32_16x16x32_bf16 v[24:27], v[154:157], v[208:211], v[24:27]
	v_mfma_f32_16x16x32_bf16 v[12:15], v[128:131], v[216:219], v[12:15]
	v_mfma_f32_16x16x32_bf16 v[8:11], v[154:157], v[216:219], v[8:11]
	v_mfma_f32_16x16x32_bf16 v[60:63], v[150:153], v[196:199], v[60:63]
	v_mfma_f32_16x16x32_bf16 v[56:59], v[158:161], v[196:199], v[56:59]
	v_mfma_f32_16x16x32_bf16 v[44:47], v[150:153], v[204:207], v[44:47]
	v_mfma_f32_16x16x32_bf16 v[40:43], v[158:161], v[204:207], v[40:43]
	v_mfma_f32_16x16x32_bf16 v[28:31], v[150:153], v[212:215], v[28:31]
	v_mfma_f32_16x16x32_bf16 v[24:27], v[158:161], v[212:215], v[24:27]
	v_mfma_f32_16x16x32_bf16 v[12:15], v[150:153], v[220:223], v[12:15]
	v_mfma_f32_16x16x32_bf16 v[8:11], v[158:161], v[220:223], v[8:11]
	s_setprio 0
	s_setprio 1
	v_mfma_f32_16x16x32_bf16 v[52:55], v[162:165], v[192:195], v[52:55]
	v_mfma_f32_16x16x32_bf16 v[48:51], v[170:173], v[192:195], v[48:51]
	v_mfma_f32_16x16x32_bf16 v[36:39], v[162:165], v[200:203], v[36:39]
	v_mfma_f32_16x16x32_bf16 v[32:35], v[170:173], v[200:203], v[32:35]
	v_mfma_f32_16x16x32_bf16 v[20:23], v[162:165], v[208:211], v[20:23]
	v_mfma_f32_16x16x32_bf16 v[16:19], v[170:173], v[208:211], v[16:19]
	v_mfma_f32_16x16x32_bf16 v[4:7], v[162:165], v[216:219], v[4:7]
	v_mfma_f32_16x16x32_bf16 v[0:3], v[170:173], v[216:219], v[0:3]
	v_mfma_f32_16x16x32_bf16 v[52:55], v[166:169], v[196:199], v[52:55]
	v_mfma_f32_16x16x32_bf16 v[48:51], v[188:191], v[196:199], v[48:51]
	v_mfma_f32_16x16x32_bf16 v[36:39], v[166:169], v[204:207], v[36:39]
	v_mfma_f32_16x16x32_bf16 v[32:35], v[188:191], v[204:207], v[32:35]
	v_mfma_f32_16x16x32_bf16 v[20:23], v[166:169], v[212:215], v[20:23]
	v_mfma_f32_16x16x32_bf16 v[16:19], v[188:191], v[212:215], v[16:19]
	v_mfma_f32_16x16x32_bf16 v[4:7], v[166:169], v[220:223], v[4:7]
	v_mfma_f32_16x16x32_bf16 v[0:3], v[188:191], v[220:223], v[0:3]
	s_setprio 0
	s_barrier
; #define PG8_STAGE(bufoff, gbase, voff) do { _Pragma("unroll") for (int _i = 0; _i < 2; ++_i) \
;         __builtin_amdgcn_global_load_lds((const unsigned*)((const char*)(gbase) + (voff)[_i]), (PG8_LAS unsigned*)(lds + (bufoff) + ldsw + _i * 8192), 16, 0, 0); } while (0)
; #define PG8_LDA(dst, b, h) do { _Pragma("unroll") for (int m = 0; m < 4; ++m) _Pragma("unroll") for (int k = 0; k < 2; ++k) dst[m][k] = *(const PG8_LAS bf16x8*)(lds + PG8_SA(b, h) + aoff + m * 2048 + k * 1024); } while (0)
; #define PG8_LDB(dst, b, h) do { _Pragma("unroll") for (int n = 0; n < 2; ++n) _Pragma("unroll") for (int k = 0; k < 2; ++k) dst[n][k] = *(const PG8_LAS bf16x8*)(lds + PG8_SB(b, h) + boff + n * 2048 + k * 1024); } while (0)
; #define PG8_MMA(ai, bj, At, Bt) do { __builtin_amdgcn_s_setprio(1); _Pragma("unroll") for (int m = 0; m < 4; ++m) _Pragma("unroll") for (int n = 0; n < 2; ++n) _Pragma("unroll") for (int k = 0; k < 2; ++k) \
;         acc[ai][bj][m][n] = __builtin_amdgcn_mfma_f32_16x16x32_bf16(Bt[n][k], At[m][k], acc[ai][bj][m][n], 0, 0, 0); __builtin_amdgcn_s_setprio(0); } while (0)
; #define PG8_WAIT_V(n) asm volatile("s_waitcnt vmcnt(" #n ")" ::: "memory")
; #define PG8_WAIT_L(n) asm volatile("s_waitcnt lgkmcnt(" #n ")" ::: "memory")
; #define PG8_BAR __builtin_amdgcn_s_barrier()
; #define PG8_SCHED __builtin_amdgcn_sched_barrier(0)
; template <class Epi, class Sched, bool ALIGN_EPI = false, bool SP2 = false>
; __device__ __forceinline__ void gemm_phase(PG8_LAS unsigned char* lds, const Gemm g, const Sched& S, const Epi& E, const int wid) {
;     ...
;             PG8_LDB(B0, 1, 0); PG8_LDB(B1, 1, 1); PG8_SCHED; PG8_LDA(At, 1, 0); PG8_STAGE(PG8_SA(0, 1), a2 + hstepA, voffA);
;             PG8_WAIT_V(8); PG8_WAIT_L(0); PG8_BAR; PG8_MMA(0, 0, At, B0); PG8_MMA(0, 1, At, B1); PG8_BAR; PG8_SCHED;
;             PG8_LDA(At, 1, 1); PG8_STAGE(PG8_SB(1, 0), b3, voffB); PG8_STAGE(PG8_SB(1, 1), b3 + hstepB, voffB); PG8_STAGE(PG8_SA(1, 0), a3, voffA);
;             PG8_WAIT_V(8); PG8_WAIT_L(0); PG8_BAR; PG8_MMA(1, 0, At, B0); PG8_MMA(1, 1, At, B1); PG8_BAR; PG8_SCHED;
;     ...
;         if constexpr (ALIGN_EPI) { if (wr == 0) PG8_BAR; }
	s_add_i32 s76, 0, 0x18000
	s_add_i32 s77, 0, 0x1c000
	v_add_u32_e32 v158, s76, v178
	v_add_u32_e32 v188, s77, v178
	ds_read_b128 v[128:131], v158
	ds_read_b128 v[150:153], v158 offset:1024
	ds_read_b128 v[154:157], v158 offset:2048
	ds_read_b128 v[158:161], v158 offset:3072
	ds_read_b128 v[162:165], v188
	ds_read_b128 v[166:169], v188 offset:1024
	ds_read_b128 v[170:173], v188 offset:2048
	ds_read_b128 v[188:191], v188 offset:3072
	s_add_u32 s40, s40, 0x40000
	s_addc_u32 s41, s41, 0
	s_mov_b32 m0, s48
	ds_read_b128 v[192:195], v185 offset:32768
	ds_read_b128 v[196:199], v185 offset:33792
	ds_read_b128 v[200:203], v185 offset:34816
	ds_read_b128 v[204:207], v185 offset:35840
	ds_read_b128 v[208:211], v185 offset:36864
	ds_read_b128 v[212:215], v185 offset:37888
	ds_read_b128 v[216:219], v185 offset:38912
	ds_read_b128 v[220:223], v185 offset:39936
	global_load_lds_dwordx4 v132, s[40:41]
	s_mov_b32 m0, s49
	s_nop 0
	global_load_lds_dwordx4 v136, s[40:41]
	s_waitcnt vmcnt(8) lgkmcnt(0)
	s_barrier
	s_setprio 1
	v_mfma_f32_16x16x32_bf16 v[124:127], v[128:131], v[192:195], v[124:127]
	v_mfma_f32_16x16x32_bf16 v[120:123], v[154:157], v[192:195], v[120:123]
	v_mfma_f32_16x16x32_bf16 v[108:111], v[128:131], v[200:203], v[108:111]
	v_mfma_f32_16x16x32_bf16 v[104:107], v[154:157], v[200:203], v[104:107]
	v_mfma_f32_16x16x32_bf16 v[92:95], v[128:131], v[208:211], v[92:95]
	v_mfma_f32_16x16x32_bf16 v[88:91], v[154:157], v[208:211], v[88:91]
	v_mfma_f32_16x16x32_bf16 v[76:79], v[128:131], v[216:219], v[76:79]
	v_mfma_f32_16x16x32_bf16 v[72:75], v[154:157], v[216:219], v[72:75]
	v_mfma_f32_16x16x32_bf16 v[124:127], v[150:153], v[196:199], v[124:127]
	v_mfma_f32_16x16x32_bf16 v[120:123], v[158:161], v[196:199], v[120:123]
	v_mfma_f32_16x16x32_bf16 v[108:111], v[150:153], v[204:207], v[108:111]
	v_mfma_f32_16x16x32_bf16 v[104:107], v[158:161], v[204:207], v[104:107]
	v_mfma_f32_16x16x32_bf16 v[92:95], v[150:153], v[212:215], v[92:95]
	v_mfma_f32_16x16x32_bf16 v[88:91], v[158:161], v[212:215], v[88:91]
	v_mfma_f32_16x16x32_bf16 v[76:79], v[150:153], v[220:223], v[76:79]
	v_mfma_f32_16x16x32_bf16 v[72:75], v[158:161], v[220:223], v[72:75]
	s_setprio 0
	s_setprio 1
	v_mfma_f32_16x16x32_bf16 v[116:119], v[162:165], v[192:195], v[116:119]
	v_mfma_f32_16x16x32_bf16 v[112:115], v[170:173], v[192:195], v[112:115]
	v_mfma_f32_16x16x32_bf16 v[100:103], v[162:165], v[200:203], v[100:103]
	v_mfma_f32_16x16x32_bf16 v[96:99], v[170:173], v[200:203], v[96:99]
	v_mfma_f32_16x16x32_bf16 v[84:87], v[162:165], v[208:211], v[84:87]
	v_mfma_f32_16x16x32_bf16 v[80:83], v[170:173], v[208:211], v[80:83]
	v_mfma_f32_16x16x32_bf16 v[68:71], v[162:165], v[216:219], v[68:71]
	v_mfma_f32_16x16x32_bf16 v[64:67], v[170:173], v[216:219], v[64:67]
	v_mfma_f32_16x16x32_bf16 v[116:119], v[166:169], v[196:199], v[116:119]
	v_mfma_f32_16x16x32_bf16 v[112:115], v[188:191], v[196:199], v[112:115]
	v_mfma_f32_16x16x32_bf16 v[100:103], v[166:169], v[204:207], v[100:103]
	v_mfma_f32_16x16x32_bf16 v[96:99], v[188:191], v[204:207], v[96:99]
	v_mfma_f32_16x16x32_bf16 v[84:87], v[166:169], v[212:215], v[84:87]
	v_mfma_f32_16x16x32_bf16 v[80:83], v[188:191], v[212:215], v[80:83]
	v_mfma_f32_16x16x32_bf16 v[68:71], v[166:169], v[220:223], v[68:71]
	v_mfma_f32_16x16x32_bf16 v[64:67], v[188:191], v[220:223], v[64:67]
	s_setprio 0
	s_barrier
	s_add_i32 s40, s76, s45
	s_mov_b32 m0, s40
	ds_read_b128 v[192:195], v185 offset:49152
	ds_read_b128 v[196:199], v185 offset:50176
	ds_read_b128 v[200:203], v185 offset:51200
	ds_read_b128 v[204:207], v185 offset:52224
	ds_read_b128 v[208:211], v185 offset:53248
	ds_read_b128 v[212:215], v185 offset:54272
	ds_read_b128 v[216:219], v185 offset:55296
	ds_read_b128 v[220:223], v185 offset:56320
	global_load_lds_dwordx4 v134, s[98:99]
	s_add_i32 m0, s40, 0x2000
	s_add_u32 s36, s36, 0x40080
	s_addc_u32 s37, s37, 0
	s_add_i32 s40, s77, s45
	global_load_lds_dwordx4 v138, s[98:99]
	s_mov_b32 m0, s40
	s_nop 0
	global_load_lds_dwordx4 v134, s[36:37]
	s_add_i32 m0, s40, 0x2000
	s_nop 0
	global_load_lds_dwordx4 v138, s[36:37]
	s_mov_b32 m0, s64
	s_nop 0
	global_load_lds_dwordx4 v132, s[100:101]
	s_mov_b32 m0, s65
	s_nop 0
	global_load_lds_dwordx4 v136, s[100:101]
	s_waitcnt vmcnt(8) lgkmcnt(0)
	s_barrier
	s_setprio 1
	v_mfma_f32_16x16x32_bf16 v[60:63], v[128:131], v[192:195], v[60:63]
	v_mfma_f32_16x16x32_bf16 v[56:59], v[154:157], v[192:195], v[56:59]
	v_mfma_f32_16x16x32_bf16 v[44:47], v[128:131], v[200:203], v[44:47]
	v_mfma_f32_16x16x32_bf16 v[40:43], v[154:157], v[200:203], v[40:43]
	v_mfma_f32_16x16x32_bf16 v[28:31], v[128:131], v[208:211], v[28:31]
	v_mfma_f32_16x16x32_bf16 v[24:27], v[154:157], v[208:211], v[24:27]
	v_mfma_f32_16x16x32_bf16 v[12:15], v[128:131], v[216:219], v[12:15]
	v_mfma_f32_16x16x32_bf16 v[8:11], v[154:157], v[216:219], v[8:11]
	v_mfma_f32_16x16x32_bf16 v[60:63], v[150:153], v[196:199], v[60:63]
	v_mfma_f32_16x16x32_bf16 v[56:59], v[158:161], v[196:199], v[56:59]
	v_mfma_f32_16x16x32_bf16 v[44:47], v[150:153], v[204:207], v[44:47]
	v_mfma_f32_16x16x32_bf16 v[40:43], v[158:161], v[204:207], v[40:43]
	v_mfma_f32_16x16x32_bf16 v[28:31], v[150:153], v[212:215], v[28:31]
	v_mfma_f32_16x16x32_bf16 v[24:27], v[158:161], v[212:215], v[24:27]
	v_mfma_f32_16x16x32_bf16 v[12:15], v[150:153], v[220:223], v[12:15]
	v_mfma_f32_16x16x32_bf16 v[8:11], v[158:161], v[220:223], v[8:11]
	s_setprio 0
	s_setprio 1
	v_mfma_f32_16x16x32_bf16 v[52:55], v[162:165], v[192:195], v[52:55]
	v_mfma_f32_16x16x32_bf16 v[48:51], v[170:173], v[192:195], v[48:51]
	v_mfma_f32_16x16x32_bf16 v[36:39], v[162:165], v[200:203], v[36:39]
	v_mfma_f32_16x16x32_bf16 v[32:35], v[170:173], v[200:203], v[32:35]
	v_mfma_f32_16x16x32_bf16 v[20:23], v[162:165], v[208:211], v[20:23]
	v_mfma_f32_16x16x32_bf16 v[16:19], v[170:173], v[208:211], v[16:19]
	v_mfma_f32_16x16x32_bf16 v[4:7], v[162:165], v[216:219], v[4:7]
	v_mfma_f32_16x16x32_bf16 v[0:3], v[170:173], v[216:219], v[0:3]
	v_mfma_f32_16x16x32_bf16 v[52:55], v[166:169], v[196:199], v[52:55]
	v_mfma_f32_16x16x32_bf16 v[48:51], v[188:191], v[196:199], v[48:51]
	v_mfma_f32_16x16x32_bf16 v[36:39], v[166:169], v[204:207], v[36:39]
	v_mfma_f32_16x16x32_bf16 v[32:35], v[188:191], v[204:207], v[32:35]
	v_mfma_f32_16x16x32_bf16 v[20:23], v[166:169], v[212:215], v[20:23]
	v_mfma_f32_16x16x32_bf16 v[16:19], v[188:191], v[212:215], v[16:19]
	v_mfma_f32_16x16x32_bf16 v[4:7], v[166:169], v[220:223], v[4:7]
	v_mfma_f32_16x16x32_bf16 v[0:3], v[188:191], v[220:223], v[0:3]
	s_setprio 0
	s_barrier
	s_add_i32 s75, s75, 2
	s_add_u32 s8, s8, 0x100
	s_addc_u32 s9, s9, 0
	s_add_u32 s73, s73, 0x100
	s_addc_u32 s74, s74, 0
	s_cmp_gt_u32 s75, 13
	s_cbranch_scc0 .LBB0_349
	s_and_b64 vcc, exec, s[20:21]
	s_cbranch_vccz .LBB0_352
	s_barrier

; #define PG8_STAGE(bufoff, gbase, voff) do { _Pragma("unroll") for (int _i = 0; _i < 2; ++_i) \
;         __builtin_amdgcn_global_load_lds((const unsigned*)((const char*)(gbase) + (voff)[_i]), (PG8_LAS unsigned*)(lds + (bufoff) + ldsw + _i * 8192), 16, 0, 0); } while (0)
; #define PG8_LDA(dst, b, h) do { _Pragma("unroll") for (int m = 0; m < 4; ++m) _Pragma("unroll") for (int k = 0; k < 2; ++k) dst[m][k] = *(const PG8_LAS bf16x8*)(lds + PG8_SA(b, h) + aoff + m * 2048 + k * 1024); } while (0)
; #define PG8_LDB(dst, b, h) do { _Pragma("unroll") for (int n = 0; n < 2; ++n) _Pragma("unroll") for (int k = 0; k < 2; ++k) dst[n][k] = *(const PG8_LAS bf16x8*)(lds + PG8_SB(b, h) + boff + n * 2048 + k * 1024); } while (0)
; #define PG8_MMA(ai, bj, At, Bt) do { __builtin_amdgcn_s_setprio(1); _Pragma("unroll") for (int m = 0; m < 4; ++m) _Pragma("unroll") for (int n = 0; n < 2; ++n) _Pragma("unroll") for (int k = 0; k < 2; ++k) \
;         acc[ai][bj][m][n] = __builtin_amdgcn_mfma_f32_16x16x32_bf16(Bt[n][k], At[m][k], acc[ai][bj][m][n], 0, 0, 0); __builtin_amdgcn_s_setprio(0); } while (0)
; #define PG8_WAIT_V(n) asm volatile("s_waitcnt vmcnt(" #n ")" ::: "memory")
; #define PG8_WAIT_L(n) asm volatile("s_waitcnt lgkmcnt(" #n ")" ::: "memory")
; template <class Epi, class Sched, bool ALIGN_EPI = false, bool SP2 = false>
; __device__ __forceinline__ void gemm_phase(PG8_LAS unsigned char* lds, const Gemm g, const Sched& S, const Epi& E, const int wid) {
;     ...
;             const bool last = (t == nt - 2);
;             const char* a1 = cA + (size_t)(t + 1) * kstep;
;             const char* a2 = last ? nA : cA + (size_t)(t + 2) * kstep; const char* b2 = last ? nB : cB + (size_t)(t + 2) * kstep;
;             const char* a3 = a2 + kstep; const char* b3 = b2 + kstep;
;             if (last && has_next) S.a_ready(nxt);
;             if constexpr (SP2) {
;             PG8_LDB(B0, 0, 0); PG8_LDB(B1, 0, 1); PG8_SCHED; PG8_LDA(At, 0, 0); PG8_STAGE(PG8_SA(1, 1), a1 + hstepA, voffA);
;             PG8_WAIT_V(8); PG8_WAIT_L(0); PG8_BAR; PG8_MMA(0, 0, At, B0); PG8_MMA(0, 1, At, B1); PG8_BAR; PG8_SCHED;
;             PG8_LDA(At, 0, 1); PG8_STAGE(PG8_SB(0, 0), b2, voffB); PG8_STAGE(PG8_SB(0, 1), b2 + hstepB, voffB); PG8_STAGE(PG8_SA(0, 0), a2, voffA);
;             PG8_WAIT_V(8); PG8_WAIT_L(0); PG8_BAR; PG8_MMA(1, 0, At, B0); PG8_MMA(1, 1, At, B1); PG8_BAR; PG8_SCHED;
.LBB0_1780:
	ds_read_b128 v[128:131], v190
	ds_read_b128 v[132:135], v190 offset:1024
	ds_read_b128 v[136:139], v190 offset:2048
	ds_read_b128 v[140:143], v190 offset:3072
	ds_read_b128 v[144:147], v191
	ds_read_b128 v[148:151], v191 offset:1024
	ds_read_b128 v[172:175], v191 offset:2048
	ds_read_b128 v[176:179], v191 offset:3072
	s_add_u32 s34, s30, 0xfffc0080
	s_addc_u32 s35, s31, -1
	s_cmp_eq_u32 s70, 12
	s_cselect_b32 s37, s21, s35
	s_cselect_b32 s36, s27, s34
	s_cselect_b32 s35, s19, s69
	s_cselect_b32 s34, s29, s68
	s_add_i32 m0, s40, 0xc000
	ds_read_b128 v[180:183], v192
	ds_read_b128 v[184:187], v192 offset:1024
	ds_read_b128 v[194:197], v192 offset:2048
	ds_read_b128 v[198:201], v192 offset:3072
	ds_read_b128 v[202:205], v192 offset:4096
	ds_read_b128 v[206:209], v192 offset:5120
	ds_read_b128 v[210:213], v192 offset:6144
	ds_read_b128 v[214:217], v192 offset:7168
	global_load_lds_dwordx4 v164, s[30:31]
	s_add_i32 m0, s40, 0xe000
	s_nop 0
	global_load_lds_dwordx4 v166, s[30:31]
	s_waitcnt vmcnt(8) lgkmcnt(0)
	s_barrier
	s_setprio 1
	v_mfma_f32_16x16x32_bf16 v[124:127], v[128:131], v[180:183], v[124:127]
	v_mfma_f32_16x16x32_bf16 v[120:123], v[136:139], v[180:183], v[120:123]
	v_mfma_f32_16x16x32_bf16 v[108:111], v[128:131], v[194:197], v[108:111]
	v_mfma_f32_16x16x32_bf16 v[104:107], v[136:139], v[194:197], v[104:107]
	v_mfma_f32_16x16x32_bf16 v[92:95], v[128:131], v[202:205], v[92:95]
	v_mfma_f32_16x16x32_bf16 v[88:91], v[136:139], v[202:205], v[88:91]
	v_mfma_f32_16x16x32_bf16 v[76:79], v[128:131], v[210:213], v[76:79]
	v_mfma_f32_16x16x32_bf16 v[72:75], v[136:139], v[210:213], v[72:75]
	v_mfma_f32_16x16x32_bf16 v[124:127], v[132:135], v[184:187], v[124:127]
	v_mfma_f32_16x16x32_bf16 v[120:123], v[140:143], v[184:187], v[120:123]
	v_mfma_f32_16x16x32_bf16 v[108:111], v[132:135], v[198:201], v[108:111]
	v_mfma_f32_16x16x32_bf16 v[104:107], v[140:143], v[198:201], v[104:107]
	v_mfma_f32_16x16x32_bf16 v[92:95], v[132:135], v[206:209], v[92:95]
	v_mfma_f32_16x16x32_bf16 v[88:91], v[140:143], v[206:209], v[88:91]
	v_mfma_f32_16x16x32_bf16 v[76:79], v[132:135], v[214:217], v[76:79]
	v_mfma_f32_16x16x32_bf16 v[72:75], v[140:143], v[214:217], v[72:75]
	s_setprio 0
	s_setprio 1
	v_mfma_f32_16x16x32_bf16 v[116:119], v[144:147], v[180:183], v[116:119]
	v_mfma_f32_16x16x32_bf16 v[112:115], v[172:175], v[180:183], v[112:115]
	v_mfma_f32_16x16x32_bf16 v[100:103], v[144:147], v[194:197], v[100:103]
	v_mfma_f32_16x16x32_bf16 v[96:99], v[172:175], v[194:197], v[96:99]
	v_mfma_f32_16x16x32_bf16 v[84:87], v[144:147], v[202:205], v[84:87]
	v_mfma_f32_16x16x32_bf16 v[80:83], v[172:175], v[202:205], v[80:83]
	v_mfma_f32_16x16x32_bf16 v[68:71], v[144:147], v[210:213], v[68:71]
	v_mfma_f32_16x16x32_bf16 v[64:67], v[172:175], v[210:213], v[64:67]
	v_mfma_f32_16x16x32_bf16 v[116:119], v[148:151], v[184:187], v[116:119]
	v_mfma_f32_16x16x32_bf16 v[112:115], v[176:179], v[184:187], v[112:115]
	v_mfma_f32_16x16x32_bf16 v[100:103], v[148:151], v[198:201], v[100:103]
	v_mfma_f32_16x16x32_bf16 v[96:99], v[176:179], v[198:201], v[96:99]
	v_mfma_f32_16x16x32_bf16 v[84:87], v[148:151], v[206:209], v[84:87]
	v_mfma_f32_16x16x32_bf16 v[80:83], v[176:179], v[206:209], v[80:83]
	v_mfma_f32_16x16x32_bf16 v[68:71], v[148:151], v[214:217], v[68:71]
	v_mfma_f32_16x16x32_bf16 v[64:67], v[176:179], v[214:217], v[64:67]
	s_setprio 0
	s_barrier
	s_add_i32 s71, s65, s39
	s_add_u32 s98, s34, 0x80
	s_addc_u32 s99, s35, 0
	s_mov_b32 m0, s71
	ds_read_b128 v[180:183], v192 offset:16384
	ds_read_b128 v[184:187], v192 offset:17408
	ds_read_b128 v[194:197], v192 offset:18432
	ds_read_b128 v[198:201], v192 offset:19456
	ds_read_b128 v[202:205], v192 offset:20480
	ds_read_b128 v[206:209], v192 offset:21504
	ds_read_b128 v[210:213], v192 offset:22528
	ds_read_b128 v[214:217], v192 offset:23552
	global_load_lds_dwordx4 v154, s[34:35]
	s_add_i32 m0, s71, 0x2000
	s_add_u32 s72, s34, 0x40000
	s_addc_u32 s73, s35, 0
	s_add_i32 s71, s66, s39
	global_load_lds_dwordx4 v158, s[34:35]
	s_mov_b32 m0, s71
	s_add_u32 s100, s36, 0x80
	s_addc_u32 s101, s37, 0
	global_load_lds_dwordx4 v154, s[72:73]
	s_add_i32 m0, s71, 0x2000
	s_nop 0
	global_load_lds_dwordx4 v158, s[72:73]
	s_mov_b32 m0, s40
	s_nop 0
	global_load_lds_dwordx4 v152, s[36:37]
	s_mov_b32 m0, s41
	s_nop 0
	global_load_lds_dwordx4 v156, s[36:37]
	s_waitcnt vmcnt(8) lgkmcnt(0)
	s_barrier
	s_setprio 1
	v_mfma_f32_16x16x32_bf16 v[60:63], v[128:131], v[180:183], v[60:63]
	v_mfma_f32_16x16x32_bf16 v[56:59], v[136:139], v[180:183], v[56:59]
	v_mfma_f32_16x16x32_bf16 v[44:47], v[128:131], v[194:197], v[44:47]
	v_mfma_f32_16x16x32_bf16 v[40:43], v[136:139], v[194:197], v[40:43]
	v_mfma_f32_16x16x32_bf16 v[28:31], v[128:131], v[202:205], v[28:31]
	v_mfma_f32_16x16x32_bf16 v[24:27], v[136:139], v[202:205], v[24:27]
	v_mfma_f32_16x16x32_bf16 v[12:15], v[128:131], v[210:213], v[12:15]
	v_mfma_f32_16x16x32_bf16 v[8:11], v[136:139], v[210:213], v[8:11]
	v_mfma_f32_16x16x32_bf16 v[60:63], v[132:135], v[184:187], v[60:63]
	v_mfma_f32_16x16x32_bf16 v[56:59], v[140:143], v[184:187], v[56:59]
	v_mfma_f32_16x16x32_bf16 v[44:47], v[132:135], v[198:201], v[44:47]
	v_mfma_f32_16x16x32_bf16 v[40:43], v[140:143], v[198:201], v[40:43]
	v_mfma_f32_16x16x32_bf16 v[28:31], v[132:135], v[206:209], v[28:31]
	v_mfma_f32_16x16x32_bf16 v[24:27], v[140:143], v[206:209], v[24:27]
	v_mfma_f32_16x16x32_bf16 v[12:15], v[132:135], v[214:217], v[12:15]
	v_mfma_f32_16x16x32_bf16 v[8:11], v[140:143], v[214:217], v[8:11]
	s_setprio 0
	s_setprio 1
	v_mfma_f32_16x16x32_bf16 v[52:55], v[144:147], v[180:183], v[52:55]
	v_mfma_f32_16x16x32_bf16 v[48:51], v[172:175], v[180:183], v[48:51]
	v_mfma_f32_16x16x32_bf16 v[36:39], v[144:147], v[194:197], v[36:39]
	v_mfma_f32_16x16x32_bf16 v[32:35], v[172:175], v[194:197], v[32:35]
	v_mfma_f32_16x16x32_bf16 v[20:23], v[144:147], v[202:205], v[20:23]
	v_mfma_f32_16x16x32_bf16 v[16:19], v[172:175], v[202:205], v[16:19]
	v_mfma_f32_16x16x32_bf16 v[4:7], v[144:147], v[210:213], v[4:7]
	v_mfma_f32_16x16x32_bf16 v[0:3], v[172:175], v[210:213], v[0:3]
	v_mfma_f32_16x16x32_bf16 v[52:55], v[148:151], v[184:187], v[52:55]
	v_mfma_f32_16x16x32_bf16 v[48:51], v[176:179], v[184:187], v[48:51]
	v_mfma_f32_16x16x32_bf16 v[36:39], v[148:151], v[198:201], v[36:39]
	v_mfma_f32_16x16x32_bf16 v[32:35], v[176:179], v[198:201], v[32:35]
	v_mfma_f32_16x16x32_bf16 v[20:23], v[148:151], v[206:209], v[20:23]
	v_mfma_f32_16x16x32_bf16 v[16:19], v[176:179], v[206:209], v[16:19]
	v_mfma_f32_16x16x32_bf16 v[4:7], v[148:151], v[214:217], v[4:7]
	v_mfma_f32_16x16x32_bf16 v[0:3], v[176:179], v[214:217], v[0:3]
	s_setprio 0
	s_barrier
; #define PG8_STAGE(bufoff, gbase, voff) do { _Pragma("unroll") for (int _i = 0; _i < 2; ++_i) \
;         __builtin_amdgcn_global_load_lds((const unsigned*)((const char*)(gbase) + (voff)[_i]), (PG8_LAS unsigned*)(lds + (bufoff) + ldsw + _i * 8192), 16, 0, 0); } while (0)
; #define PG8_LDA(dst, b, h) do { _Pragma("unroll") for (int m = 0; m < 4; ++m) _Pragma("unroll") for (int k = 0; k < 2; ++k) dst[m][k] = *(const PG8_LAS bf16x8*)(lds + PG8_SA(b, h) + aoff + m * 2048 + k * 1024); } while (0)
; #define PG8_WAIT_V(n) asm volatile("s_waitcnt vmcnt(" #n ")" ::: "memory")
; #define PG8_WAIT_L(n) asm volatile("s_waitcnt lgkmcnt(" #n ")" ::: "memory")
; #define PG8_BAR __builtin_amdgcn_s_barrier()
; template <class Epi, class Sched, bool ALIGN_EPI = false, bool SP2 = false>
; __device__ __forceinline__ void gemm_phase(PG8_LAS unsigned char* lds, const Gemm g, const Sched& S, const Epi& E, const int wid) {
;     ...
;         for (int t = 0; t < nt; t += 2) {
;             const bool last = (t == nt - 2);
;             const char* a1 = cA + (size_t)(t + 1) * kstep;
;             const char* a2 = last ? nA : cA + (size_t)(t + 2) * kstep; const char* b2 = last ? nB : cB + (size_t)(t + 2) * kstep;
;             const char* a3 = a2 + kstep; const char* b3 = b2 + kstep;
;             if (last && has_next) S.a_ready(nxt);
;             if constexpr (SP2) {
;             PG8_LDB(B0, 0, 0); PG8_LDB(B1, 0, 1); PG8_SCHED; PG8_LDA(At, 0, 0); PG8_STAGE(PG8_SA(1, 1), a1 + hstepA, voffA);
;             PG8_WAIT_V(8); PG8_WAIT_L(0); PG8_BAR; PG8_MMA(0, 0, At, B0); PG8_MMA(0, 1, At, B1); PG8_BAR; PG8_SCHED;
;             PG8_LDA(At, 0, 1); PG8_STAGE(PG8_SB(0, 0), b2, voffB); PG8_STAGE(PG8_SB(0, 1), b2 + hstepB, voffB); PG8_STAGE(PG8_SA(0, 0), a2, voffA);
;             PG8_WAIT_V(8); PG8_WAIT_L(0); PG8_BAR; PG8_MMA(1, 0, At, B0); PG8_MMA(1, 1, At, B1); PG8_BAR; PG8_SCHED;
;             PG8_LDB(B0, 1, 0); PG8_LDB(B1, 1, 1); PG8_SCHED; PG8_LDA(At, 1, 0); PG8_STAGE(PG8_SA(0, 1), a2 + hstepA, voffA);
;             PG8_WAIT_V(8); PG8_WAIT_L(0); PG8_BAR; PG8_MMA(0, 0, At, B0); PG8_MMA(0, 1, At, B1); PG8_BAR; PG8_SCHED;
;             PG8_LDA(At, 1, 1); PG8_STAGE(PG8_SB(1, 0), b3, voffB); PG8_STAGE(PG8_SB(1, 1), b3 + hstepB, voffB); PG8_STAGE(PG8_SA(1, 0), a3, voffA);
;             PG8_WAIT_V(8); PG8_WAIT_L(0); PG8_BAR; PG8_MMA(1, 0, At, B0); PG8_MMA(1, 1, At, B1); PG8_BAR; PG8_SCHED;
	s_add_i32 s71, 0, 0x18000
	s_add_i32 s72, 0, 0x1c000
	v_add_u32_e32 v140, s71, v189
	v_add_u32_e32 v176, s72, v189
	ds_read_b128 v[128:131], v140
	ds_read_b128 v[132:135], v140 offset:1024
	ds_read_b128 v[136:139], v140 offset:2048
	ds_read_b128 v[140:143], v140 offset:3072
	ds_read_b128 v[144:147], v176
	ds_read_b128 v[148:151], v176 offset:1024
	ds_read_b128 v[172:175], v176 offset:2048
	ds_read_b128 v[176:179], v176 offset:3072
	s_add_u32 s36, s36, 0x40000
	s_addc_u32 s37, s37, 0
	s_mov_b32 m0, s44
	ds_read_b128 v[180:183], v192 offset:32768
	ds_read_b128 v[184:187], v192 offset:33792
	ds_read_b128 v[194:197], v192 offset:34816
	ds_read_b128 v[198:201], v192 offset:35840
	ds_read_b128 v[202:205], v192 offset:36864
	ds_read_b128 v[206:209], v192 offset:37888
	ds_read_b128 v[210:213], v192 offset:38912
	ds_read_b128 v[214:217], v192 offset:39936
	global_load_lds_dwordx4 v152, s[36:37]
	s_mov_b32 m0, s45
	s_nop 0
	global_load_lds_dwordx4 v156, s[36:37]
	s_waitcnt vmcnt(8) lgkmcnt(0)
	s_barrier
	s_setprio 1
	v_mfma_f32_16x16x32_bf16 v[124:127], v[128:131], v[180:183], v[124:127]
	v_mfma_f32_16x16x32_bf16 v[120:123], v[136:139], v[180:183], v[120:123]
	v_mfma_f32_16x16x32_bf16 v[108:111], v[128:131], v[194:197], v[108:111]
	v_mfma_f32_16x16x32_bf16 v[104:107], v[136:139], v[194:197], v[104:107]
	v_mfma_f32_16x16x32_bf16 v[92:95], v[128:131], v[202:205], v[92:95]
	v_mfma_f32_16x16x32_bf16 v[88:91], v[136:139], v[202:205], v[88:91]
	v_mfma_f32_16x16x32_bf16 v[76:79], v[128:131], v[210:213], v[76:79]
	v_mfma_f32_16x16x32_bf16 v[72:75], v[136:139], v[210:213], v[72:75]
	v_mfma_f32_16x16x32_bf16 v[124:127], v[132:135], v[184:187], v[124:127]
	v_mfma_f32_16x16x32_bf16 v[120:123], v[140:143], v[184:187], v[120:123]
	v_mfma_f32_16x16x32_bf16 v[108:111], v[132:135], v[198:201], v[108:111]
	v_mfma_f32_16x16x32_bf16 v[104:107], v[140:143], v[198:201], v[104:107]
	v_mfma_f32_16x16x32_bf16 v[92:95], v[132:135], v[206:209], v[92:95]
	v_mfma_f32_16x16x32_bf16 v[88:91], v[140:143], v[206:209], v[88:91]
	v_mfma_f32_16x16x32_bf16 v[76:79], v[132:135], v[214:217], v[76:79]
	v_mfma_f32_16x16x32_bf16 v[72:75], v[140:143], v[214:217], v[72:75]
	s_setprio 0
	s_setprio 1
	v_mfma_f32_16x16x32_bf16 v[116:119], v[144:147], v[180:183], v[116:119]
	v_mfma_f32_16x16x32_bf16 v[112:115], v[172:175], v[180:183], v[112:115]
	v_mfma_f32_16x16x32_bf16 v[100:103], v[144:147], v[194:197], v[100:103]
	v_mfma_f32_16x16x32_bf16 v[96:99], v[172:175], v[194:197], v[96:99]
	v_mfma_f32_16x16x32_bf16 v[84:87], v[144:147], v[202:205], v[84:87]
	v_mfma_f32_16x16x32_bf16 v[80:83], v[172:175], v[202:205], v[80:83]
	v_mfma_f32_16x16x32_bf16 v[68:71], v[144:147], v[210:213], v[68:71]
	v_mfma_f32_16x16x32_bf16 v[64:67], v[172:175], v[210:213], v[64:67]
	v_mfma_f32_16x16x32_bf16 v[116:119], v[148:151], v[184:187], v[116:119]
	v_mfma_f32_16x16x32_bf16 v[112:115], v[176:179], v[184:187], v[112:115]
	v_mfma_f32_16x16x32_bf16 v[100:103], v[148:151], v[198:201], v[100:103]
	v_mfma_f32_16x16x32_bf16 v[96:99], v[176:179], v[198:201], v[96:99]
	v_mfma_f32_16x16x32_bf16 v[84:87], v[148:151], v[206:209], v[84:87]
	v_mfma_f32_16x16x32_bf16 v[80:83], v[176:179], v[206:209], v[80:83]
	v_mfma_f32_16x16x32_bf16 v[68:71], v[148:151], v[214:217], v[68:71]
	v_mfma_f32_16x16x32_bf16 v[64:67], v[176:179], v[214:217], v[64:67]
	s_setprio 0
	s_barrier
	s_add_i32 s36, s71, s39
	s_mov_b32 m0, s36
	ds_read_b128 v[180:183], v192 offset:49152
	ds_read_b128 v[184:187], v192 offset:50176
	ds_read_b128 v[194:197], v192 offset:51200
	ds_read_b128 v[198:201], v192 offset:52224
	ds_read_b128 v[202:205], v192 offset:53248
	ds_read_b128 v[206:209], v192 offset:54272
	ds_read_b128 v[210:213], v192 offset:55296
	ds_read_b128 v[214:217], v192 offset:56320
	global_load_lds_dwordx4 v154, s[98:99]
	s_add_i32 m0, s36, 0x2000
	s_add_u32 s34, s34, 0x40080
	s_addc_u32 s35, s35, 0
	s_add_i32 s36, s72, s39
	global_load_lds_dwordx4 v158, s[98:99]
	s_mov_b32 m0, s36
	s_nop 0
	global_load_lds_dwordx4 v154, s[34:35]
	s_add_i32 m0, s36, 0x2000
	s_nop 0
	global_load_lds_dwordx4 v158, s[34:35]
	s_mov_b32 m0, s47
	s_nop 0
	global_load_lds_dwordx4 v152, s[100:101]
	s_mov_b32 m0, s48
	s_nop 0
	global_load_lds_dwordx4 v156, s[100:101]
	s_waitcnt vmcnt(8) lgkmcnt(0)
	s_barrier
	s_setprio 1
	v_mfma_f32_16x16x32_bf16 v[60:63], v[128:131], v[180:183], v[60:63]
	v_mfma_f32_16x16x32_bf16 v[56:59], v[136:139], v[180:183], v[56:59]
	v_mfma_f32_16x16x32_bf16 v[44:47], v[128:131], v[194:197], v[44:47]
	v_mfma_f32_16x16x32_bf16 v[40:43], v[136:139], v[194:197], v[40:43]
	v_mfma_f32_16x16x32_bf16 v[28:31], v[128:131], v[202:205], v[28:31]
	v_mfma_f32_16x16x32_bf16 v[24:27], v[136:139], v[202:205], v[24:27]
	v_mfma_f32_16x16x32_bf16 v[12:15], v[128:131], v[210:213], v[12:15]
	v_mfma_f32_16x16x32_bf16 v[8:11], v[136:139], v[210:213], v[8:11]
	v_mfma_f32_16x16x32_bf16 v[60:63], v[132:135], v[184:187], v[60:63]
	v_mfma_f32_16x16x32_bf16 v[56:59], v[140:143], v[184:187], v[56:59]
	v_mfma_f32_16x16x32_bf16 v[44:47], v[132:135], v[198:201], v[44:47]
	v_mfma_f32_16x16x32_bf16 v[40:43], v[140:143], v[198:201], v[40:43]
	v_mfma_f32_16x16x32_bf16 v[28:31], v[132:135], v[206:209], v[28:31]
	v_mfma_f32_16x16x32_bf16 v[24:27], v[140:143], v[206:209], v[24:27]
	v_mfma_f32_16x16x32_bf16 v[12:15], v[132:135], v[214:217], v[12:15]
	v_mfma_f32_16x16x32_bf16 v[8:11], v[140:143], v[214:217], v[8:11]
	s_setprio 0
	s_setprio 1
	v_mfma_f32_16x16x32_bf16 v[52:55], v[144:147], v[180:183], v[52:55]
	v_mfma_f32_16x16x32_bf16 v[48:51], v[172:175], v[180:183], v[48:51]
	v_mfma_f32_16x16x32_bf16 v[36:39], v[144:147], v[194:197], v[36:39]
	v_mfma_f32_16x16x32_bf16 v[32:35], v[172:175], v[194:197], v[32:35]
	v_mfma_f32_16x16x32_bf16 v[20:23], v[144:147], v[202:205], v[20:23]
	v_mfma_f32_16x16x32_bf16 v[16:19], v[172:175], v[202:205], v[16:19]
	v_mfma_f32_16x16x32_bf16 v[4:7], v[144:147], v[210:213], v[4:7]
	v_mfma_f32_16x16x32_bf16 v[0:3], v[172:175], v[210:213], v[0:3]
	v_mfma_f32_16x16x32_bf16 v[52:55], v[148:151], v[184:187], v[52:55]
	v_mfma_f32_16x16x32_bf16 v[48:51], v[176:179], v[184:187], v[48:51]
	v_mfma_f32_16x16x32_bf16 v[36:39], v[148:151], v[198:201], v[36:39]
	v_mfma_f32_16x16x32_bf16 v[32:35], v[176:179], v[198:201], v[32:35]
	v_mfma_f32_16x16x32_bf16 v[20:23], v[148:151], v[206:209], v[20:23]
	v_mfma_f32_16x16x32_bf16 v[16:19], v[176:179], v[206:209], v[16:19]
	v_mfma_f32_16x16x32_bf16 v[4:7], v[148:151], v[214:217], v[4:7]
	v_mfma_f32_16x16x32_bf16 v[0:3], v[176:179], v[214:217], v[0:3]
	s_setprio 0
	s_barrier
	s_add_i32 s70, s70, 2
	s_add_u32 s30, s30, 0x100
	s_addc_u32 s31, s31, 0
	s_add_u32 s68, s68, 0x100
	s_addc_u32 s69, s69, 0
	s_cmp_gt_u32 s70, 13
	s_cbranch_scc0 .LBB0_1780
	s_and_b64 vcc, exec, s[16:17]
	s_cbranch_vccz .LBB0_1783
	s_barrier

; #define PG8_STAGE(bufoff, gbase, voff) do { _Pragma("unroll") for (int _i = 0; _i < 2; ++_i) \
;         __builtin_amdgcn_global_load_lds((const unsigned*)((const char*)(gbase) + (voff)[_i]), (PG8_LAS unsigned*)(lds + (bufoff) + ldsw + _i * 8192), 16, 0, 0); } while (0)
; #define PG8_LDA(dst, b, h) do { _Pragma("unroll") for (int m = 0; m < 4; ++m) _Pragma("unroll") for (int k = 0; k < 2; ++k) dst[m][k] = *(const PG8_LAS bf16x8*)(lds + PG8_SA(b, h) + aoff + m * 2048 + k * 1024); } while (0)
; #define PG8_LDB(dst, b, h) do { _Pragma("unroll") for (int n = 0; n < 2; ++n) _Pragma("unroll") for (int k = 0; k < 2; ++k) dst[n][k] = *(const PG8_LAS bf16x8*)(lds + PG8_SB(b, h) + boff + n * 2048 + k * 1024); } while (0)
; #define PG8_WAIT_V(n) asm volatile("s_waitcnt vmcnt(" #n ")" ::: "memory")
; #define PG8_WAIT_L(n) asm volatile("s_waitcnt lgkmcnt(" #n ")" ::: "memory")
; #define PG8_BAR __builtin_amdgcn_s_barrier()
; #define PG8_SCHED __builtin_amdgcn_sched_barrier(0)
; template <class Epi, class Sched, bool ALIGN_EPI = false, bool SP2 = false>
; __device__ __forceinline__ void gemm_phase(PG8_LAS unsigned char* lds, const Gemm g, const Sched& S, const Epi& E, const int wid) {
;     ...
;         const bool has_next = S.next(ui + 1, nxt);
;         const char* nA = has_next ? (const char*)g.A + (size_t)nxt.pm * tstepA : cA; const char* nB = has_next ? (const char*)g.Bt + (size_t)nxt.pn * tstepB : cB;
;         for (int t = 0; t < nt; t += 2) {
;             const bool last = (t == nt - 2);
;             const char* a1 = cA + (size_t)(t + 1) * kstep;
;             const char* a2 = last ? nA : cA + (size_t)(t + 2) * kstep; const char* b2 = last ? nB : cB + (size_t)(t + 2) * kstep;
;             const char* a3 = a2 + kstep; const char* b3 = b2 + kstep;
;             if (last && has_next) S.a_ready(nxt);
;             if constexpr (SP2) {
;             PG8_LDB(B0, 0, 0); PG8_LDB(B1, 0, 1); PG8_SCHED; PG8_LDA(At, 0, 0); PG8_STAGE(PG8_SA(1, 1), a1 + hstepA, voffA);
;             PG8_WAIT_V(8); PG8_WAIT_L(0); PG8_BAR; PG8_MMA(0, 0, At, B0); PG8_MMA(0, 1, At, B1); PG8_BAR; PG8_SCHED;
;             PG8_LDA(At, 0, 1); PG8_STAGE(PG8_SB(0, 0), b2, voffB); PG8_STAGE(PG8_SB(0, 1), b2 + hstepB, voffB); PG8_STAGE(PG8_SA(0, 0), a2, voffA);
;             PG8_WAIT_V(8); PG8_WAIT_L(0); PG8_BAR; PG8_MMA(1, 0, At, B0); PG8_MMA(1, 1, At, B1); PG8_BAR; PG8_SCHED;
.LBB0_1867:
	ds_read_b128 v[148:151], v166
	ds_read_b128 v[152:155], v166 offset:1024
	ds_read_b128 v[156:159], v166 offset:2048
	ds_read_b128 v[160:163], v166 offset:3072
	ds_read_b128 v[172:175], v167
	ds_read_b128 v[176:179], v167 offset:1024
	ds_read_b128 v[180:183], v167 offset:2048
	ds_read_b128 v[184:187], v167 offset:3072
	s_add_u32 s26, s24, 0xfffc0080
	s_addc_u32 s27, s25, -1
	s_cmp_eq_u32 s67, 12
	s_cselect_b32 s29, s17, s27
	s_cselect_b32 s28, s49, s26
	s_cselect_b32 s27, s15, s66
	s_cselect_b32 s26, s64, s65
	s_add_i32 m0, s36, 0xc000
	ds_read_b128 v[188:191], v168
	ds_read_b128 v[192:195], v168 offset:1024
	ds_read_b128 v[196:199], v168 offset:2048
	ds_read_b128 v[200:203], v168 offset:3072
	ds_read_b128 v[204:207], v168 offset:4096
	ds_read_b128 v[208:211], v168 offset:5120
	ds_read_b128 v[212:215], v168 offset:6144
	ds_read_b128 v[216:219], v168 offset:7168
	global_load_lds_dwordx4 v140, s[24:25]
	s_add_i32 m0, s36, 0xe000
	s_nop 0
	global_load_lds_dwordx4 v142, s[24:25]
	s_waitcnt vmcnt(8) lgkmcnt(0)
	s_barrier
	s_setprio 1
	v_mfma_f32_16x16x32_bf16 v[124:127], v[148:151], v[188:191], v[124:127]
	v_mfma_f32_16x16x32_bf16 v[116:119], v[156:159], v[188:191], v[116:119]
	v_mfma_f32_16x16x32_bf16 v[108:111], v[148:151], v[196:199], v[108:111]
	v_mfma_f32_16x16x32_bf16 v[100:103], v[156:159], v[196:199], v[100:103]
	v_mfma_f32_16x16x32_bf16 v[92:95], v[148:151], v[204:207], v[92:95]
	v_mfma_f32_16x16x32_bf16 v[84:87], v[156:159], v[204:207], v[84:87]
	v_mfma_f32_16x16x32_bf16 v[76:79], v[148:151], v[212:215], v[76:79]
	v_mfma_f32_16x16x32_bf16 v[68:71], v[156:159], v[212:215], v[68:71]
	v_mfma_f32_16x16x32_bf16 v[124:127], v[152:155], v[192:195], v[124:127]
	v_mfma_f32_16x16x32_bf16 v[116:119], v[160:163], v[192:195], v[116:119]
	v_mfma_f32_16x16x32_bf16 v[108:111], v[152:155], v[200:203], v[108:111]
	v_mfma_f32_16x16x32_bf16 v[100:103], v[160:163], v[200:203], v[100:103]
	v_mfma_f32_16x16x32_bf16 v[92:95], v[152:155], v[208:211], v[92:95]
	v_mfma_f32_16x16x32_bf16 v[84:87], v[160:163], v[208:211], v[84:87]
	v_mfma_f32_16x16x32_bf16 v[76:79], v[152:155], v[216:219], v[76:79]
	v_mfma_f32_16x16x32_bf16 v[68:71], v[160:163], v[216:219], v[68:71]
	s_setprio 0
	s_setprio 1
	v_mfma_f32_16x16x32_bf16 v[120:123], v[172:175], v[188:191], v[120:123]
	v_mfma_f32_16x16x32_bf16 v[112:115], v[180:183], v[188:191], v[112:115]
	v_mfma_f32_16x16x32_bf16 v[104:107], v[172:175], v[196:199], v[104:107]
	v_mfma_f32_16x16x32_bf16 v[96:99], v[180:183], v[196:199], v[96:99]
	v_mfma_f32_16x16x32_bf16 v[88:91], v[172:175], v[204:207], v[88:91]
	v_mfma_f32_16x16x32_bf16 v[80:83], v[180:183], v[204:207], v[80:83]
	v_mfma_f32_16x16x32_bf16 v[72:75], v[172:175], v[212:215], v[72:75]
	v_mfma_f32_16x16x32_bf16 v[64:67], v[180:183], v[212:215], v[64:67]
	v_mfma_f32_16x16x32_bf16 v[120:123], v[176:179], v[192:195], v[120:123]
	v_mfma_f32_16x16x32_bf16 v[112:115], v[184:187], v[192:195], v[112:115]
	v_mfma_f32_16x16x32_bf16 v[104:107], v[176:179], v[200:203], v[104:107]
	v_mfma_f32_16x16x32_bf16 v[96:99], v[184:187], v[200:203], v[96:99]
	v_mfma_f32_16x16x32_bf16 v[88:91], v[176:179], v[208:211], v[88:91]
	v_mfma_f32_16x16x32_bf16 v[80:83], v[184:187], v[208:211], v[80:83]
	v_mfma_f32_16x16x32_bf16 v[72:75], v[176:179], v[216:219], v[72:75]
	v_mfma_f32_16x16x32_bf16 v[64:67], v[184:187], v[216:219], v[64:67]
	s_setprio 0
	s_barrier
	s_add_i32 s68, s45, s33
	s_add_u32 s98, s26, 0x80
	s_addc_u32 s99, s27, 0
	s_mov_b32 m0, s68
	ds_read_b128 v[188:191], v168 offset:16384
	ds_read_b128 v[192:195], v168 offset:17408
	ds_read_b128 v[196:199], v168 offset:18432
	ds_read_b128 v[200:203], v168 offset:19456
	ds_read_b128 v[204:207], v168 offset:20480
	ds_read_b128 v[208:211], v168 offset:21504
	ds_read_b128 v[212:215], v168 offset:22528
	ds_read_b128 v[216:219], v168 offset:23552
	global_load_lds_dwordx4 v132, s[26:27]
	s_add_i32 m0, s68, 0x2000
	s_add_u32 s68, s26, 0x40000
	s_addc_u32 s69, s27, 0
	s_add_i32 s70, s46, s33
	global_load_lds_dwordx4 v128, s[26:27]
	s_mov_b32 m0, s70
	s_add_u32 s100, s28, 0x80
	s_addc_u32 s101, s29, 0
	global_load_lds_dwordx4 v132, s[68:69]
	s_add_i32 m0, s70, 0x2000
	s_nop 0
	global_load_lds_dwordx4 v128, s[68:69]
	s_mov_b32 m0, s36
	s_nop 0
	global_load_lds_dwordx4 v134, s[28:29]
	s_mov_b32 m0, s37
	s_nop 0
	global_load_lds_dwordx4 v130, s[28:29]
	s_waitcnt vmcnt(8) lgkmcnt(0)
	s_barrier
	s_setprio 1
	v_mfma_f32_16x16x32_bf16 v[60:63], v[148:151], v[188:191], v[60:63]
	v_mfma_f32_16x16x32_bf16 v[52:55], v[156:159], v[188:191], v[52:55]
	v_mfma_f32_16x16x32_bf16 v[44:47], v[148:151], v[196:199], v[44:47]
	v_mfma_f32_16x16x32_bf16 v[36:39], v[156:159], v[196:199], v[36:39]
	v_mfma_f32_16x16x32_bf16 v[28:31], v[148:151], v[204:207], v[28:31]
	v_mfma_f32_16x16x32_bf16 v[20:23], v[156:159], v[204:207], v[20:23]
	v_mfma_f32_16x16x32_bf16 v[12:15], v[148:151], v[212:215], v[12:15]
	v_mfma_f32_16x16x32_bf16 v[4:7], v[156:159], v[212:215], v[4:7]
	v_mfma_f32_16x16x32_bf16 v[60:63], v[152:155], v[192:195], v[60:63]
	v_mfma_f32_16x16x32_bf16 v[52:55], v[160:163], v[192:195], v[52:55]
	v_mfma_f32_16x16x32_bf16 v[44:47], v[152:155], v[200:203], v[44:47]
	v_mfma_f32_16x16x32_bf16 v[36:39], v[160:163], v[200:203], v[36:39]
	v_mfma_f32_16x16x32_bf16 v[28:31], v[152:155], v[208:211], v[28:31]
	v_mfma_f32_16x16x32_bf16 v[20:23], v[160:163], v[208:211], v[20:23]
	v_mfma_f32_16x16x32_bf16 v[12:15], v[152:155], v[216:219], v[12:15]
	v_mfma_f32_16x16x32_bf16 v[4:7], v[160:163], v[216:219], v[4:7]
	s_setprio 0
	s_setprio 1
	v_mfma_f32_16x16x32_bf16 v[56:59], v[172:175], v[188:191], v[56:59]
	v_mfma_f32_16x16x32_bf16 v[48:51], v[180:183], v[188:191], v[48:51]
	v_mfma_f32_16x16x32_bf16 v[40:43], v[172:175], v[196:199], v[40:43]
	v_mfma_f32_16x16x32_bf16 v[32:35], v[180:183], v[196:199], v[32:35]
	v_mfma_f32_16x16x32_bf16 v[24:27], v[172:175], v[204:207], v[24:27]
	v_mfma_f32_16x16x32_bf16 v[16:19], v[180:183], v[204:207], v[16:19]
	v_mfma_f32_16x16x32_bf16 v[8:11], v[172:175], v[212:215], v[8:11]
	v_mfma_f32_16x16x32_bf16 v[0:3], v[180:183], v[212:215], v[0:3]
	v_mfma_f32_16x16x32_bf16 v[56:59], v[176:179], v[192:195], v[56:59]
	v_mfma_f32_16x16x32_bf16 v[48:51], v[184:187], v[192:195], v[48:51]
	v_mfma_f32_16x16x32_bf16 v[40:43], v[176:179], v[200:203], v[40:43]
	v_mfma_f32_16x16x32_bf16 v[32:35], v[184:187], v[200:203], v[32:35]
	v_mfma_f32_16x16x32_bf16 v[24:27], v[176:179], v[208:211], v[24:27]
	v_mfma_f32_16x16x32_bf16 v[16:19], v[184:187], v[208:211], v[16:19]
	v_mfma_f32_16x16x32_bf16 v[8:11], v[176:179], v[216:219], v[8:11]
	v_mfma_f32_16x16x32_bf16 v[0:3], v[184:187], v[216:219], v[0:3]
	s_setprio 0
	s_barrier
; #define PG8_STAGE(bufoff, gbase, voff) do { _Pragma("unroll") for (int _i = 0; _i < 2; ++_i) \
;         __builtin_amdgcn_global_load_lds((const unsigned*)((const char*)(gbase) + (voff)[_i]), (PG8_LAS unsigned*)(lds + (bufoff) + ldsw + _i * 8192), 16, 0, 0); } while (0)
; #define PG8_LDA(dst, b, h) do { _Pragma("unroll") for (int m = 0; m < 4; ++m) _Pragma("unroll") for (int k = 0; k < 2; ++k) dst[m][k] = *(const PG8_LAS bf16x8*)(lds + PG8_SA(b, h) + aoff + m * 2048 + k * 1024); } while (0)
; #define PG8_WAIT_V(n) asm volatile("s_waitcnt vmcnt(" #n ")" ::: "memory")
; #define PG8_WAIT_L(n) asm volatile("s_waitcnt lgkmcnt(" #n ")" ::: "memory")
; #define PG8_BAR __builtin_amdgcn_s_barrier()
; template <class Epi, class Sched, bool ALIGN_EPI = false, bool SP2 = false>
; __device__ __forceinline__ void gemm_phase(PG8_LAS unsigned char* lds, const Gemm g, const Sched& S, const Epi& E, const int wid) {
;     ...
;         for (int t = 0; t < nt; t += 2) {
;             const bool last = (t == nt - 2);
;             const char* a1 = cA + (size_t)(t + 1) * kstep;
;             const char* a2 = last ? nA : cA + (size_t)(t + 2) * kstep; const char* b2 = last ? nB : cB + (size_t)(t + 2) * kstep;
;             const char* a3 = a2 + kstep; const char* b3 = b2 + kstep;
;             if (last && has_next) S.a_ready(nxt);
;             if constexpr (SP2) {
;             PG8_LDB(B0, 0, 0); PG8_LDB(B1, 0, 1); PG8_SCHED; PG8_LDA(At, 0, 0); PG8_STAGE(PG8_SA(1, 1), a1 + hstepA, voffA);
;             PG8_WAIT_V(8); PG8_WAIT_L(0); PG8_BAR; PG8_MMA(0, 0, At, B0); PG8_MMA(0, 1, At, B1); PG8_BAR; PG8_SCHED;
;             PG8_LDA(At, 0, 1); PG8_STAGE(PG8_SB(0, 0), b2, voffB); PG8_STAGE(PG8_SB(0, 1), b2 + hstepB, voffB); PG8_STAGE(PG8_SA(0, 0), a2, voffA);
;             PG8_WAIT_V(8); PG8_WAIT_L(0); PG8_BAR; PG8_MMA(1, 0, At, B0); PG8_MMA(1, 1, At, B1); PG8_BAR; PG8_SCHED;
;             PG8_LDB(B0, 1, 0); PG8_LDB(B1, 1, 1); PG8_SCHED; PG8_LDA(At, 1, 0); PG8_STAGE(PG8_SA(0, 1), a2 + hstepA, voffA);
;             PG8_WAIT_V(8); PG8_WAIT_L(0); PG8_BAR; PG8_MMA(0, 0, At, B0); PG8_MMA(0, 1, At, B1); PG8_BAR; PG8_SCHED;
;             PG8_LDA(At, 1, 1); PG8_STAGE(PG8_SB(1, 0), b3, voffB); PG8_STAGE(PG8_SB(1, 1), b3 + hstepB, voffB); PG8_STAGE(PG8_SA(1, 0), a3, voffA);
;             PG8_WAIT_V(8); PG8_WAIT_L(0); PG8_BAR; PG8_MMA(1, 0, At, B0); PG8_MMA(1, 1, At, B1); PG8_BAR; PG8_SCHED;
	s_add_i32 s68, 0, 0x18000
	s_add_i32 s69, 0, 0x1c000
	v_add_u32_e32 v160, s68, v165
	v_add_u32_e32 v171, s69, v165
	ds_read_b128 v[148:151], v160
	ds_read_b128 v[152:155], v160 offset:1024
	ds_read_b128 v[156:159], v160 offset:2048
	ds_read_b128 v[160:163], v160 offset:3072
	ds_read_b128 v[172:175], v171
	ds_read_b128 v[176:179], v171 offset:1024
	ds_read_b128 v[180:183], v171 offset:2048
	ds_read_b128 v[184:187], v171 offset:3072
	s_add_u32 s28, s28, 0x40000
	s_addc_u32 s29, s29, 0
	s_mov_b32 m0, s38
	ds_read_b128 v[188:191], v168 offset:32768
	ds_read_b128 v[192:195], v168 offset:33792
	ds_read_b128 v[196:199], v168 offset:34816
	ds_read_b128 v[200:203], v168 offset:35840
	ds_read_b128 v[204:207], v168 offset:36864
	ds_read_b128 v[208:211], v168 offset:37888
	ds_read_b128 v[212:215], v168 offset:38912
	ds_read_b128 v[216:219], v168 offset:39936
	global_load_lds_dwordx4 v134, s[28:29]
	s_mov_b32 m0, s39
	s_nop 0
	global_load_lds_dwordx4 v130, s[28:29]
	s_waitcnt vmcnt(8) lgkmcnt(0)
	s_barrier
	s_setprio 1
	v_mfma_f32_16x16x32_bf16 v[124:127], v[148:151], v[188:191], v[124:127]
	v_mfma_f32_16x16x32_bf16 v[116:119], v[156:159], v[188:191], v[116:119]
	v_mfma_f32_16x16x32_bf16 v[108:111], v[148:151], v[196:199], v[108:111]
	v_mfma_f32_16x16x32_bf16 v[100:103], v[156:159], v[196:199], v[100:103]
	v_mfma_f32_16x16x32_bf16 v[92:95], v[148:151], v[204:207], v[92:95]
	v_mfma_f32_16x16x32_bf16 v[84:87], v[156:159], v[204:207], v[84:87]
	v_mfma_f32_16x16x32_bf16 v[76:79], v[148:151], v[212:215], v[76:79]
	v_mfma_f32_16x16x32_bf16 v[68:71], v[156:159], v[212:215], v[68:71]
	v_mfma_f32_16x16x32_bf16 v[124:127], v[152:155], v[192:195], v[124:127]
	v_mfma_f32_16x16x32_bf16 v[116:119], v[160:163], v[192:195], v[116:119]
	v_mfma_f32_16x16x32_bf16 v[108:111], v[152:155], v[200:203], v[108:111]
	v_mfma_f32_16x16x32_bf16 v[100:103], v[160:163], v[200:203], v[100:103]
	v_mfma_f32_16x16x32_bf16 v[92:95], v[152:155], v[208:211], v[92:95]
	v_mfma_f32_16x16x32_bf16 v[84:87], v[160:163], v[208:211], v[84:87]
	v_mfma_f32_16x16x32_bf16 v[76:79], v[152:155], v[216:219], v[76:79]
	v_mfma_f32_16x16x32_bf16 v[68:71], v[160:163], v[216:219], v[68:71]
	s_setprio 0
	s_setprio 1
	v_mfma_f32_16x16x32_bf16 v[120:123], v[172:175], v[188:191], v[120:123]
	v_mfma_f32_16x16x32_bf16 v[112:115], v[180:183], v[188:191], v[112:115]
	v_mfma_f32_16x16x32_bf16 v[104:107], v[172:175], v[196:199], v[104:107]
	v_mfma_f32_16x16x32_bf16 v[96:99], v[180:183], v[196:199], v[96:99]
	v_mfma_f32_16x16x32_bf16 v[88:91], v[172:175], v[204:207], v[88:91]
	v_mfma_f32_16x16x32_bf16 v[80:83], v[180:183], v[204:207], v[80:83]
	v_mfma_f32_16x16x32_bf16 v[72:75], v[172:175], v[212:215], v[72:75]
	v_mfma_f32_16x16x32_bf16 v[64:67], v[180:183], v[212:215], v[64:67]
	v_mfma_f32_16x16x32_bf16 v[120:123], v[176:179], v[192:195], v[120:123]
	v_mfma_f32_16x16x32_bf16 v[112:115], v[184:187], v[192:195], v[112:115]
	v_mfma_f32_16x16x32_bf16 v[104:107], v[176:179], v[200:203], v[104:107]
	v_mfma_f32_16x16x32_bf16 v[96:99], v[184:187], v[200:203], v[96:99]
	v_mfma_f32_16x16x32_bf16 v[88:91], v[176:179], v[208:211], v[88:91]
	v_mfma_f32_16x16x32_bf16 v[80:83], v[184:187], v[208:211], v[80:83]
	v_mfma_f32_16x16x32_bf16 v[72:75], v[176:179], v[216:219], v[72:75]
	v_mfma_f32_16x16x32_bf16 v[64:67], v[184:187], v[216:219], v[64:67]
	s_setprio 0
	s_barrier
	s_add_i32 s28, s68, s33
	s_mov_b32 m0, s28
	ds_read_b128 v[188:191], v168 offset:49152
	ds_read_b128 v[192:195], v168 offset:50176
	ds_read_b128 v[196:199], v168 offset:51200
	ds_read_b128 v[200:203], v168 offset:52224
	ds_read_b128 v[204:207], v168 offset:53248
	ds_read_b128 v[208:211], v168 offset:54272
	ds_read_b128 v[212:215], v168 offset:55296
	ds_read_b128 v[216:219], v168 offset:56320
	global_load_lds_dwordx4 v132, s[98:99]
	s_add_i32 m0, s28, 0x2000
	s_add_u32 s26, s26, 0x40080
	s_addc_u32 s27, s27, 0
	s_add_i32 s28, s69, s33
	global_load_lds_dwordx4 v128, s[98:99]
	s_mov_b32 m0, s28
	s_nop 0
	global_load_lds_dwordx4 v132, s[26:27]
	s_add_i32 m0, s28, 0x2000
	s_nop 0
	global_load_lds_dwordx4 v128, s[26:27]
	s_mov_b32 m0, s40
	s_nop 0
	global_load_lds_dwordx4 v134, s[100:101]
	s_mov_b32 m0, s41
	s_nop 0
	global_load_lds_dwordx4 v130, s[100:101]
	s_waitcnt vmcnt(8) lgkmcnt(0)
	s_barrier
	s_setprio 1
	v_mfma_f32_16x16x32_bf16 v[60:63], v[148:151], v[188:191], v[60:63]
	v_mfma_f32_16x16x32_bf16 v[52:55], v[156:159], v[188:191], v[52:55]
	v_mfma_f32_16x16x32_bf16 v[44:47], v[148:151], v[196:199], v[44:47]
	v_mfma_f32_16x16x32_bf16 v[36:39], v[156:159], v[196:199], v[36:39]
	v_mfma_f32_16x16x32_bf16 v[28:31], v[148:151], v[204:207], v[28:31]
	v_mfma_f32_16x16x32_bf16 v[20:23], v[156:159], v[204:207], v[20:23]
	v_mfma_f32_16x16x32_bf16 v[12:15], v[148:151], v[212:215], v[12:15]
	v_mfma_f32_16x16x32_bf16 v[4:7], v[156:159], v[212:215], v[4:7]
	v_mfma_f32_16x16x32_bf16 v[60:63], v[152:155], v[192:195], v[60:63]
	v_mfma_f32_16x16x32_bf16 v[52:55], v[160:163], v[192:195], v[52:55]
	v_mfma_f32_16x16x32_bf16 v[44:47], v[152:155], v[200:203], v[44:47]
	v_mfma_f32_16x16x32_bf16 v[36:39], v[160:163], v[200:203], v[36:39]
	v_mfma_f32_16x16x32_bf16 v[28:31], v[152:155], v[208:211], v[28:31]
	v_mfma_f32_16x16x32_bf16 v[20:23], v[160:163], v[208:211], v[20:23]
	v_mfma_f32_16x16x32_bf16 v[12:15], v[152:155], v[216:219], v[12:15]
	v_mfma_f32_16x16x32_bf16 v[4:7], v[160:163], v[216:219], v[4:7]
	s_setprio 0
	s_setprio 1
	v_mfma_f32_16x16x32_bf16 v[56:59], v[172:175], v[188:191], v[56:59]
	v_mfma_f32_16x16x32_bf16 v[48:51], v[180:183], v[188:191], v[48:51]
	v_mfma_f32_16x16x32_bf16 v[40:43], v[172:175], v[196:199], v[40:43]
	v_mfma_f32_16x16x32_bf16 v[32:35], v[180:183], v[196:199], v[32:35]
	v_mfma_f32_16x16x32_bf16 v[24:27], v[172:175], v[204:207], v[24:27]
	v_mfma_f32_16x16x32_bf16 v[16:19], v[180:183], v[204:207], v[16:19]
	v_mfma_f32_16x16x32_bf16 v[8:11], v[172:175], v[212:215], v[8:11]
	v_mfma_f32_16x16x32_bf16 v[0:3], v[180:183], v[212:215], v[0:3]
	v_mfma_f32_16x16x32_bf16 v[56:59], v[176:179], v[192:195], v[56:59]
	v_mfma_f32_16x16x32_bf16 v[48:51], v[184:187], v[192:195], v[48:51]
	v_mfma_f32_16x16x32_bf16 v[40:43], v[176:179], v[200:203], v[40:43]
	v_mfma_f32_16x16x32_bf16 v[32:35], v[184:187], v[200:203], v[32:35]
	v_mfma_f32_16x16x32_bf16 v[24:27], v[176:179], v[208:211], v[24:27]
	v_mfma_f32_16x16x32_bf16 v[16:19], v[184:187], v[208:211], v[16:19]
	v_mfma_f32_16x16x32_bf16 v[8:11], v[176:179], v[216:219], v[8:11]
	v_mfma_f32_16x16x32_bf16 v[0:3], v[184:187], v[216:219], v[0:3]
	s_setprio 0
	s_barrier
	s_add_i32 s67, s67, 2
	s_add_u32 s24, s24, 0x100
	s_addc_u32 s25, s25, 0
	s_add_u32 s65, s65, 0x100
	s_addc_u32 s66, s66, 0
	s_cmp_gt_u32 s67, 13
	s_cbranch_scc0 .LBB0_1867
	s_and_b64 vcc, exec, s[12:13]
	s_cbranch_vccz .LBB0_1870
	s_barrier

; #define PG8_STAGE(bufoff, gbase, voff) do { _Pragma("unroll") for (int _i = 0; _i < 2; ++_i) \
;         __builtin_amdgcn_global_load_lds((const unsigned*)((const char*)(gbase) + (voff)[_i]), (PG8_LAS unsigned*)(lds + (bufoff) + ldsw + _i * 8192), 16, 0, 0); } while (0)
; #define PG8_LDA(dst, b, h) do { _Pragma("unroll") for (int m = 0; m < 4; ++m) _Pragma("unroll") for (int k = 0; k < 2; ++k) dst[m][k] = *(const PG8_LAS bf16x8*)(lds + PG8_SA(b, h) + aoff + m * 2048 + k * 1024); } while (0)
; #define PG8_LDB(dst, b, h) do { _Pragma("unroll") for (int n = 0; n < 2; ++n) _Pragma("unroll") for (int k = 0; k < 2; ++k) dst[n][k] = *(const PG8_LAS bf16x8*)(lds + PG8_SB(b, h) + boff + n * 2048 + k * 1024); } while (0)
; #define PG8_WAIT_V(n) asm volatile("s_waitcnt vmcnt(" #n ")" ::: "memory")
; #define PG8_WAIT_L(n) asm volatile("s_waitcnt lgkmcnt(" #n ")" ::: "memory")
; #define PG8_BAR __builtin_amdgcn_s_barrier()
; #define PG8_SCHED __builtin_amdgcn_sched_barrier(0)
; template <class Epi, class Sched, bool ALIGN_EPI = false, bool SP2 = false>
; __device__ __forceinline__ void gemm_phase(PG8_LAS unsigned char* lds, const Gemm g, const Sched& S, const Epi& E, const int wid) {
;     ...
;         const bool has_next = S.next(ui + 1, nxt);
;         const char* nA = has_next ? (const char*)g.A + (size_t)nxt.pm * tstepA : cA; const char* nB = has_next ? (const char*)g.Bt + (size_t)nxt.pn * tstepB : cB;
;         for (int t = 0; t < nt; t += 2) {
;             const bool last = (t == nt - 2);
;             const char* a1 = cA + (size_t)(t + 1) * kstep;
;             const char* a2 = last ? nA : cA + (size_t)(t + 2) * kstep; const char* b2 = last ? nB : cB + (size_t)(t + 2) * kstep;
;             const char* a3 = a2 + kstep; const char* b3 = b2 + kstep;
;             if (last && has_next) S.a_ready(nxt);
;             if constexpr (SP2) {
;             PG8_LDB(B0, 0, 0); PG8_LDB(B1, 0, 1); PG8_SCHED; PG8_LDA(At, 0, 0); PG8_STAGE(PG8_SA(1, 1), a1 + hstepA, voffA);
;             PG8_WAIT_V(8); PG8_WAIT_L(0); PG8_BAR; PG8_MMA(0, 0, At, B0); PG8_MMA(0, 1, At, B1); PG8_BAR; PG8_SCHED;
;             PG8_LDA(At, 0, 1); PG8_STAGE(PG8_SB(0, 0), b2, voffB); PG8_STAGE(PG8_SB(0, 1), b2 + hstepB, voffB); PG8_STAGE(PG8_SA(0, 0), a2, voffA);
;             PG8_WAIT_V(8); PG8_WAIT_L(0); PG8_BAR; PG8_MMA(1, 0, At, B0); PG8_MMA(1, 1, At, B1); PG8_BAR; PG8_SCHED;
.LBB0_1952:
	ds_read_b128 v[128:131], v190
	ds_read_b128 v[132:135], v190 offset:1024
	ds_read_b128 v[136:139], v190 offset:2048
	ds_read_b128 v[140:143], v190 offset:3072
	ds_read_b128 v[144:147], v191
	ds_read_b128 v[148:151], v191 offset:1024
	ds_read_b128 v[172:175], v191 offset:2048
	ds_read_b128 v[176:179], v191 offset:3072
	s_add_u32 s24, s22, 0x100
	s_addc_u32 s25, s23, 0
	s_cmp_eq_u32 s68, 40
	s_cselect_b32 s29, s7, s25
	s_cselect_b32 s28, s6, s24
	s_cselect_b32 s27, s21, s67
	s_cselect_b32 s26, s20, s66
	s_add_i32 m0, s34, 0xc000
	ds_read_b128 v[180:183], v192
	ds_read_b128 v[184:187], v192 offset:1024
	ds_read_b128 v[194:197], v192 offset:2048
	ds_read_b128 v[198:201], v192 offset:3072
	ds_read_b128 v[202:205], v192 offset:4096
	ds_read_b128 v[206:209], v192 offset:5120
	ds_read_b128 v[210:213], v192 offset:6144
	ds_read_b128 v[214:217], v192 offset:7168
	global_load_lds_dwordx4 v164, s[22:23]
	s_add_i32 m0, s34, 0xe000
	s_nop 0
	global_load_lds_dwordx4 v166, s[22:23]
	s_waitcnt vmcnt(8) lgkmcnt(0)
	s_barrier
	s_setprio 1
	v_mfma_f32_16x16x32_bf16 v[124:127], v[128:131], v[180:183], v[124:127]
	v_mfma_f32_16x16x32_bf16 v[120:123], v[136:139], v[180:183], v[120:123]
	v_mfma_f32_16x16x32_bf16 v[108:111], v[128:131], v[194:197], v[108:111]
	v_mfma_f32_16x16x32_bf16 v[104:107], v[136:139], v[194:197], v[104:107]
	v_mfma_f32_16x16x32_bf16 v[92:95], v[128:131], v[202:205], v[92:95]
	v_mfma_f32_16x16x32_bf16 v[88:91], v[136:139], v[202:205], v[88:91]
	v_mfma_f32_16x16x32_bf16 v[76:79], v[128:131], v[210:213], v[76:79]
	v_mfma_f32_16x16x32_bf16 v[72:75], v[136:139], v[210:213], v[72:75]
	v_mfma_f32_16x16x32_bf16 v[124:127], v[132:135], v[184:187], v[124:127]
	v_mfma_f32_16x16x32_bf16 v[120:123], v[140:143], v[184:187], v[120:123]
	v_mfma_f32_16x16x32_bf16 v[108:111], v[132:135], v[198:201], v[108:111]
	v_mfma_f32_16x16x32_bf16 v[104:107], v[140:143], v[198:201], v[104:107]
	v_mfma_f32_16x16x32_bf16 v[92:95], v[132:135], v[206:209], v[92:95]
	v_mfma_f32_16x16x32_bf16 v[88:91], v[140:143], v[206:209], v[88:91]
	v_mfma_f32_16x16x32_bf16 v[76:79], v[132:135], v[214:217], v[76:79]
	v_mfma_f32_16x16x32_bf16 v[72:75], v[140:143], v[214:217], v[72:75]
	s_setprio 0
	s_setprio 1
	v_mfma_f32_16x16x32_bf16 v[116:119], v[144:147], v[180:183], v[116:119]
	v_mfma_f32_16x16x32_bf16 v[112:115], v[172:175], v[180:183], v[112:115]
	v_mfma_f32_16x16x32_bf16 v[100:103], v[144:147], v[194:197], v[100:103]
	v_mfma_f32_16x16x32_bf16 v[96:99], v[172:175], v[194:197], v[96:99]
	v_mfma_f32_16x16x32_bf16 v[84:87], v[144:147], v[202:205], v[84:87]
	v_mfma_f32_16x16x32_bf16 v[80:83], v[172:175], v[202:205], v[80:83]
	v_mfma_f32_16x16x32_bf16 v[68:71], v[144:147], v[210:213], v[68:71]
	v_mfma_f32_16x16x32_bf16 v[64:67], v[172:175], v[210:213], v[64:67]
	v_mfma_f32_16x16x32_bf16 v[116:119], v[148:151], v[184:187], v[116:119]
	v_mfma_f32_16x16x32_bf16 v[112:115], v[176:179], v[184:187], v[112:115]
	v_mfma_f32_16x16x32_bf16 v[100:103], v[148:151], v[198:201], v[100:103]
	v_mfma_f32_16x16x32_bf16 v[96:99], v[176:179], v[198:201], v[96:99]
	v_mfma_f32_16x16x32_bf16 v[84:87], v[148:151], v[206:209], v[84:87]
	v_mfma_f32_16x16x32_bf16 v[80:83], v[176:179], v[206:209], v[80:83]
	v_mfma_f32_16x16x32_bf16 v[68:71], v[148:151], v[214:217], v[68:71]
	v_mfma_f32_16x16x32_bf16 v[64:67], v[176:179], v[214:217], v[64:67]
	s_setprio 0
	s_barrier
	s_add_i32 s22, s45, s33
	s_add_u32 s98, s26, 0x80
	s_addc_u32 s99, s27, 0
	s_mov_b32 m0, s22
	ds_read_b128 v[180:183], v192 offset:16384
	ds_read_b128 v[184:187], v192 offset:17408
	ds_read_b128 v[194:197], v192 offset:18432
	ds_read_b128 v[198:201], v192 offset:19456
	ds_read_b128 v[202:205], v192 offset:20480
	ds_read_b128 v[206:209], v192 offset:21504
	ds_read_b128 v[210:213], v192 offset:22528
	ds_read_b128 v[214:217], v192 offset:23552
	global_load_lds_dwordx4 v154, s[26:27]
	s_add_i32 m0, s22, 0x2000
	s_add_u32 s22, s26, 0xb0000
	s_addc_u32 s23, s27, 0
	s_add_i32 s69, s46, s33
	global_load_lds_dwordx4 v158, s[26:27]
	s_mov_b32 m0, s69
	s_add_u32 s100, s28, 0x80
	s_addc_u32 s101, s29, 0
	global_load_lds_dwordx4 v154, s[22:23]
	s_add_i32 m0, s69, 0x2000
	s_nop 0
	global_load_lds_dwordx4 v158, s[22:23]
	s_mov_b32 m0, s34
	s_nop 0
	global_load_lds_dwordx4 v152, s[28:29]
	s_mov_b32 m0, s35
	s_nop 0
	global_load_lds_dwordx4 v156, s[28:29]
	s_waitcnt vmcnt(8) lgkmcnt(0)
	s_barrier
	s_setprio 1
	v_mfma_f32_16x16x32_bf16 v[60:63], v[128:131], v[180:183], v[60:63]
	v_mfma_f32_16x16x32_bf16 v[56:59], v[136:139], v[180:183], v[56:59]
	v_mfma_f32_16x16x32_bf16 v[44:47], v[128:131], v[194:197], v[44:47]
	v_mfma_f32_16x16x32_bf16 v[40:43], v[136:139], v[194:197], v[40:43]
	v_mfma_f32_16x16x32_bf16 v[28:31], v[128:131], v[202:205], v[28:31]
	v_mfma_f32_16x16x32_bf16 v[24:27], v[136:139], v[202:205], v[24:27]
	v_mfma_f32_16x16x32_bf16 v[12:15], v[128:131], v[210:213], v[12:15]
	v_mfma_f32_16x16x32_bf16 v[8:11], v[136:139], v[210:213], v[8:11]
	v_mfma_f32_16x16x32_bf16 v[60:63], v[132:135], v[184:187], v[60:63]
	v_mfma_f32_16x16x32_bf16 v[56:59], v[140:143], v[184:187], v[56:59]
	v_mfma_f32_16x16x32_bf16 v[44:47], v[132:135], v[198:201], v[44:47]
	v_mfma_f32_16x16x32_bf16 v[40:43], v[140:143], v[198:201], v[40:43]
	v_mfma_f32_16x16x32_bf16 v[28:31], v[132:135], v[206:209], v[28:31]
	v_mfma_f32_16x16x32_bf16 v[24:27], v[140:143], v[206:209], v[24:27]
	v_mfma_f32_16x16x32_bf16 v[12:15], v[132:135], v[214:217], v[12:15]
	v_mfma_f32_16x16x32_bf16 v[8:11], v[140:143], v[214:217], v[8:11]
	s_setprio 0
	s_setprio 1
	v_mfma_f32_16x16x32_bf16 v[52:55], v[144:147], v[180:183], v[52:55]
	v_mfma_f32_16x16x32_bf16 v[48:51], v[172:175], v[180:183], v[48:51]
	v_mfma_f32_16x16x32_bf16 v[36:39], v[144:147], v[194:197], v[36:39]
	v_mfma_f32_16x16x32_bf16 v[32:35], v[172:175], v[194:197], v[32:35]
	v_mfma_f32_16x16x32_bf16 v[20:23], v[144:147], v[202:205], v[20:23]
	v_mfma_f32_16x16x32_bf16 v[16:19], v[172:175], v[202:205], v[16:19]
	v_mfma_f32_16x16x32_bf16 v[4:7], v[144:147], v[210:213], v[4:7]
	v_mfma_f32_16x16x32_bf16 v[0:3], v[172:175], v[210:213], v[0:3]
	v_mfma_f32_16x16x32_bf16 v[52:55], v[148:151], v[184:187], v[52:55]
	v_mfma_f32_16x16x32_bf16 v[48:51], v[176:179], v[184:187], v[48:51]
	v_mfma_f32_16x16x32_bf16 v[36:39], v[148:151], v[198:201], v[36:39]
	v_mfma_f32_16x16x32_bf16 v[32:35], v[176:179], v[198:201], v[32:35]
	v_mfma_f32_16x16x32_bf16 v[20:23], v[148:151], v[206:209], v[20:23]
	v_mfma_f32_16x16x32_bf16 v[16:19], v[176:179], v[206:209], v[16:19]
	v_mfma_f32_16x16x32_bf16 v[4:7], v[148:151], v[214:217], v[4:7]
	v_mfma_f32_16x16x32_bf16 v[0:3], v[176:179], v[214:217], v[0:3]
	s_setprio 0
	s_barrier
; #define PG8_STAGE(bufoff, gbase, voff) do { _Pragma("unroll") for (int _i = 0; _i < 2; ++_i) \
;         __builtin_amdgcn_global_load_lds((const unsigned*)((const char*)(gbase) + (voff)[_i]), (PG8_LAS unsigned*)(lds + (bufoff) + ldsw + _i * 8192), 16, 0, 0); } while (0)
; #define PG8_LDA(dst, b, h) do { _Pragma("unroll") for (int m = 0; m < 4; ++m) _Pragma("unroll") for (int k = 0; k < 2; ++k) dst[m][k] = *(const PG8_LAS bf16x8*)(lds + PG8_SA(b, h) + aoff + m * 2048 + k * 1024); } while (0)
; #define PG8_WAIT_V(n) asm volatile("s_waitcnt vmcnt(" #n ")" ::: "memory")
; #define PG8_WAIT_L(n) asm volatile("s_waitcnt lgkmcnt(" #n ")" ::: "memory")
; #define PG8_BAR __builtin_amdgcn_s_barrier()
; template <class Epi, class Sched, bool ALIGN_EPI = false, bool SP2 = false>
; __device__ __forceinline__ void gemm_phase(PG8_LAS unsigned char* lds, const Gemm g, const Sched& S, const Epi& E, const int wid) {
;     ...
;         for (int t = 0; t < nt; t += 2) {
;             const bool last = (t == nt - 2);
;             const char* a1 = cA + (size_t)(t + 1) * kstep;
;             const char* a2 = last ? nA : cA + (size_t)(t + 2) * kstep; const char* b2 = last ? nB : cB + (size_t)(t + 2) * kstep;
;             const char* a3 = a2 + kstep; const char* b3 = b2 + kstep;
;             if (last && has_next) S.a_ready(nxt);
;             if constexpr (SP2) {
;             PG8_LDB(B0, 0, 0); PG8_LDB(B1, 0, 1); PG8_SCHED; PG8_LDA(At, 0, 0); PG8_STAGE(PG8_SA(1, 1), a1 + hstepA, voffA);
;             PG8_WAIT_V(8); PG8_WAIT_L(0); PG8_BAR; PG8_MMA(0, 0, At, B0); PG8_MMA(0, 1, At, B1); PG8_BAR; PG8_SCHED;
;             PG8_LDA(At, 0, 1); PG8_STAGE(PG8_SB(0, 0), b2, voffB); PG8_STAGE(PG8_SB(0, 1), b2 + hstepB, voffB); PG8_STAGE(PG8_SA(0, 0), a2, voffA);
;             PG8_WAIT_V(8); PG8_WAIT_L(0); PG8_BAR; PG8_MMA(1, 0, At, B0); PG8_MMA(1, 1, At, B1); PG8_BAR; PG8_SCHED;
;             PG8_LDB(B0, 1, 0); PG8_LDB(B1, 1, 1); PG8_SCHED; PG8_LDA(At, 1, 0); PG8_STAGE(PG8_SA(0, 1), a2 + hstepA, voffA);
;             PG8_WAIT_V(8); PG8_WAIT_L(0); PG8_BAR; PG8_MMA(0, 0, At, B0); PG8_MMA(0, 1, At, B1); PG8_BAR; PG8_SCHED;
;             PG8_LDA(At, 1, 1); PG8_STAGE(PG8_SB(1, 0), b3, voffB); PG8_STAGE(PG8_SB(1, 1), b3 + hstepB, voffB); PG8_STAGE(PG8_SA(1, 0), a3, voffA);
;             PG8_WAIT_V(8); PG8_WAIT_L(0); PG8_BAR; PG8_MMA(1, 0, At, B0); PG8_MMA(1, 1, At, B1); PG8_BAR; PG8_SCHED;
	s_add_i32 s69, 0, 0x18000
	s_add_i32 s70, 0, 0x1c000
	v_add_u32_e32 v140, s69, v189
	v_add_u32_e32 v176, s70, v189
	ds_read_b128 v[128:131], v140
	ds_read_b128 v[132:135], v140 offset:1024
	ds_read_b128 v[136:139], v140 offset:2048
	ds_read_b128 v[140:143], v140 offset:3072
	ds_read_b128 v[144:147], v176
	ds_read_b128 v[148:151], v176 offset:1024
	ds_read_b128 v[172:175], v176 offset:2048
	ds_read_b128 v[176:179], v176 offset:3072
	s_add_u32 s22, s28, 0xb0000
	s_addc_u32 s23, s29, 0
	s_mov_b32 m0, s36
	ds_read_b128 v[180:183], v192 offset:32768
	ds_read_b128 v[184:187], v192 offset:33792
	ds_read_b128 v[194:197], v192 offset:34816
	ds_read_b128 v[198:201], v192 offset:35840
	ds_read_b128 v[202:205], v192 offset:36864
	ds_read_b128 v[206:209], v192 offset:37888
	ds_read_b128 v[210:213], v192 offset:38912
	ds_read_b128 v[214:217], v192 offset:39936
	global_load_lds_dwordx4 v152, s[22:23]
	s_mov_b32 m0, s37
	s_nop 0
	global_load_lds_dwordx4 v156, s[22:23]
	s_waitcnt vmcnt(8) lgkmcnt(0)
	s_barrier
	s_setprio 1
	v_mfma_f32_16x16x32_bf16 v[124:127], v[128:131], v[180:183], v[124:127]
	v_mfma_f32_16x16x32_bf16 v[120:123], v[136:139], v[180:183], v[120:123]
	v_mfma_f32_16x16x32_bf16 v[108:111], v[128:131], v[194:197], v[108:111]
	v_mfma_f32_16x16x32_bf16 v[104:107], v[136:139], v[194:197], v[104:107]
	v_mfma_f32_16x16x32_bf16 v[92:95], v[128:131], v[202:205], v[92:95]
	v_mfma_f32_16x16x32_bf16 v[88:91], v[136:139], v[202:205], v[88:91]
	v_mfma_f32_16x16x32_bf16 v[76:79], v[128:131], v[210:213], v[76:79]
	v_mfma_f32_16x16x32_bf16 v[72:75], v[136:139], v[210:213], v[72:75]
	v_mfma_f32_16x16x32_bf16 v[124:127], v[132:135], v[184:187], v[124:127]
	v_mfma_f32_16x16x32_bf16 v[120:123], v[140:143], v[184:187], v[120:123]
	v_mfma_f32_16x16x32_bf16 v[108:111], v[132:135], v[198:201], v[108:111]
	v_mfma_f32_16x16x32_bf16 v[104:107], v[140:143], v[198:201], v[104:107]
	v_mfma_f32_16x16x32_bf16 v[92:95], v[132:135], v[206:209], v[92:95]
	v_mfma_f32_16x16x32_bf16 v[88:91], v[140:143], v[206:209], v[88:91]
	v_mfma_f32_16x16x32_bf16 v[76:79], v[132:135], v[214:217], v[76:79]
	v_mfma_f32_16x16x32_bf16 v[72:75], v[140:143], v[214:217], v[72:75]
	s_setprio 0
	s_setprio 1
	v_mfma_f32_16x16x32_bf16 v[116:119], v[144:147], v[180:183], v[116:119]
	v_mfma_f32_16x16x32_bf16 v[112:115], v[172:175], v[180:183], v[112:115]
	v_mfma_f32_16x16x32_bf16 v[100:103], v[144:147], v[194:197], v[100:103]
	v_mfma_f32_16x16x32_bf16 v[96:99], v[172:175], v[194:197], v[96:99]
	v_mfma_f32_16x16x32_bf16 v[84:87], v[144:147], v[202:205], v[84:87]
	v_mfma_f32_16x16x32_bf16 v[80:83], v[172:175], v[202:205], v[80:83]
	v_mfma_f32_16x16x32_bf16 v[68:71], v[144:147], v[210:213], v[68:71]
	v_mfma_f32_16x16x32_bf16 v[64:67], v[172:175], v[210:213], v[64:67]
	v_mfma_f32_16x16x32_bf16 v[116:119], v[148:151], v[184:187], v[116:119]
	v_mfma_f32_16x16x32_bf16 v[112:115], v[176:179], v[184:187], v[112:115]
	v_mfma_f32_16x16x32_bf16 v[100:103], v[148:151], v[198:201], v[100:103]
	v_mfma_f32_16x16x32_bf16 v[96:99], v[176:179], v[198:201], v[96:99]
	v_mfma_f32_16x16x32_bf16 v[84:87], v[148:151], v[206:209], v[84:87]
	v_mfma_f32_16x16x32_bf16 v[80:83], v[176:179], v[206:209], v[80:83]
	v_mfma_f32_16x16x32_bf16 v[68:71], v[148:151], v[214:217], v[68:71]
	v_mfma_f32_16x16x32_bf16 v[64:67], v[176:179], v[214:217], v[64:67]
	s_setprio 0
	s_barrier
	s_add_i32 s22, s69, s33
	s_mov_b32 m0, s22
	ds_read_b128 v[180:183], v192 offset:49152
	ds_read_b128 v[184:187], v192 offset:50176
	ds_read_b128 v[194:197], v192 offset:51200
	ds_read_b128 v[198:201], v192 offset:52224
	ds_read_b128 v[202:205], v192 offset:53248
	ds_read_b128 v[206:209], v192 offset:54272
	ds_read_b128 v[210:213], v192 offset:55296
	ds_read_b128 v[214:217], v192 offset:56320
	global_load_lds_dwordx4 v154, s[98:99]
	s_add_i32 m0, s22, 0x2000
	s_add_u32 s22, s26, 0xb0080
	s_addc_u32 s23, s27, 0
	s_add_i32 s26, s70, s33
	global_load_lds_dwordx4 v158, s[98:99]
	s_mov_b32 m0, s26
	s_nop 0
	global_load_lds_dwordx4 v154, s[22:23]
	s_add_i32 m0, s26, 0x2000
	s_nop 0
	global_load_lds_dwordx4 v158, s[22:23]
	s_mov_b32 m0, s39
	s_nop 0
	global_load_lds_dwordx4 v152, s[100:101]
	s_mov_b32 m0, s40
	s_nop 0
	global_load_lds_dwordx4 v156, s[100:101]
	s_waitcnt vmcnt(8) lgkmcnt(0)
	s_barrier
	s_setprio 1
	v_mfma_f32_16x16x32_bf16 v[60:63], v[128:131], v[180:183], v[60:63]
	v_mfma_f32_16x16x32_bf16 v[56:59], v[136:139], v[180:183], v[56:59]
	v_mfma_f32_16x16x32_bf16 v[44:47], v[128:131], v[194:197], v[44:47]
	v_mfma_f32_16x16x32_bf16 v[40:43], v[136:139], v[194:197], v[40:43]
	v_mfma_f32_16x16x32_bf16 v[28:31], v[128:131], v[202:205], v[28:31]
	v_mfma_f32_16x16x32_bf16 v[24:27], v[136:139], v[202:205], v[24:27]
	v_mfma_f32_16x16x32_bf16 v[12:15], v[128:131], v[210:213], v[12:15]
	v_mfma_f32_16x16x32_bf16 v[8:11], v[136:139], v[210:213], v[8:11]
	v_mfma_f32_16x16x32_bf16 v[60:63], v[132:135], v[184:187], v[60:63]
	v_mfma_f32_16x16x32_bf16 v[56:59], v[140:143], v[184:187], v[56:59]
	v_mfma_f32_16x16x32_bf16 v[44:47], v[132:135], v[198:201], v[44:47]
	v_mfma_f32_16x16x32_bf16 v[40:43], v[140:143], v[198:201], v[40:43]
	v_mfma_f32_16x16x32_bf16 v[28:31], v[132:135], v[206:209], v[28:31]
	v_mfma_f32_16x16x32_bf16 v[24:27], v[140:143], v[206:209], v[24:27]
	v_mfma_f32_16x16x32_bf16 v[12:15], v[132:135], v[214:217], v[12:15]
	v_mfma_f32_16x16x32_bf16 v[8:11], v[140:143], v[214:217], v[8:11]
	s_setprio 0
	s_setprio 1
	v_mfma_f32_16x16x32_bf16 v[52:55], v[144:147], v[180:183], v[52:55]
	v_mfma_f32_16x16x32_bf16 v[48:51], v[172:175], v[180:183], v[48:51]
	v_mfma_f32_16x16x32_bf16 v[36:39], v[144:147], v[194:197], v[36:39]
	v_mfma_f32_16x16x32_bf16 v[32:35], v[172:175], v[194:197], v[32:35]
	v_mfma_f32_16x16x32_bf16 v[20:23], v[144:147], v[202:205], v[20:23]
	v_mfma_f32_16x16x32_bf16 v[16:19], v[172:175], v[202:205], v[16:19]
	v_mfma_f32_16x16x32_bf16 v[4:7], v[144:147], v[210:213], v[4:7]
	v_mfma_f32_16x16x32_bf16 v[0:3], v[172:175], v[210:213], v[0:3]
	v_mfma_f32_16x16x32_bf16 v[52:55], v[148:151], v[184:187], v[52:55]
	v_mfma_f32_16x16x32_bf16 v[48:51], v[176:179], v[184:187], v[48:51]
	v_mfma_f32_16x16x32_bf16 v[36:39], v[148:151], v[198:201], v[36:39]
	v_mfma_f32_16x16x32_bf16 v[32:35], v[176:179], v[198:201], v[32:35]
	v_mfma_f32_16x16x32_bf16 v[20:23], v[148:151], v[206:209], v[20:23]
	v_mfma_f32_16x16x32_bf16 v[16:19], v[176:179], v[206:209], v[16:19]
	v_mfma_f32_16x16x32_bf16 v[4:7], v[148:151], v[214:217], v[4:7]
	v_mfma_f32_16x16x32_bf16 v[0:3], v[176:179], v[214:217], v[0:3]
	s_setprio 0
	s_barrier
	s_add_i32 s68, s68, 2
	s_add_u32 s66, s66, 0x100
	s_addc_u32 s67, s67, 0
	s_cmp_gt_u32 s68, 41
	s_mov_b64 s[22:23], s[24:25]
	s_cbranch_scc0 .LBB0_1952
	s_and_b64 vcc, exec, s[18:19]
	s_cbranch_vccz .LBB0_1955
	s_barrier

; #define PG8_STAGE(bufoff, gbase, voff) do { _Pragma("unroll") for (int _i = 0; _i < 2; ++_i) \
;         __builtin_amdgcn_global_load_lds((const unsigned*)((const char*)(gbase) + (voff)[_i]), (PG8_LAS unsigned*)(lds + (bufoff) + ldsw + _i * 8192), 16, 0, 0); } while (0)
; #define PG8_LDA(dst, b, h) do { _Pragma("unroll") for (int m = 0; m < 4; ++m) _Pragma("unroll") for (int k = 0; k < 2; ++k) dst[m][k] = *(const PG8_LAS bf16x8*)(lds + PG8_SA(b, h) + aoff + m * 2048 + k * 1024); } while (0)
; #define PG8_LDB(dst, b, h) do { _Pragma("unroll") for (int n = 0; n < 2; ++n) _Pragma("unroll") for (int k = 0; k < 2; ++k) dst[n][k] = *(const PG8_LAS bf16x8*)(lds + PG8_SB(b, h) + boff + n * 2048 + k * 1024); } while (0)
; #define PG8_WAIT_V(n) asm volatile("s_waitcnt vmcnt(" #n ")" ::: "memory")
; #define PG8_WAIT_L(n) asm volatile("s_waitcnt lgkmcnt(" #n ")" ::: "memory")
; #define PG8_BAR __builtin_amdgcn_s_barrier()
; #define PG8_SCHED __builtin_amdgcn_sched_barrier(0)
; template <class Epi, class Sched, bool ALIGN_EPI = false, bool SP2 = false>
; __device__ __forceinline__ void gemm_phase(PG8_LAS unsigned char* lds, const Gemm g, const Sched& S, const Epi& E, const int wid) {
;     ...
;         const bool has_next = S.next(ui + 1, nxt);
;         const char* nA = has_next ? (const char*)g.A + (size_t)nxt.pm * tstepA : cA; const char* nB = has_next ? (const char*)g.Bt + (size_t)nxt.pn * tstepB : cB;
;         for (int t = 0; t < nt; t += 2) {
;             const bool last = (t == nt - 2);
;             const char* a1 = cA + (size_t)(t + 1) * kstep;
;             const char* a2 = last ? nA : cA + (size_t)(t + 2) * kstep; const char* b2 = last ? nB : cB + (size_t)(t + 2) * kstep;
;             const char* a3 = a2 + kstep; const char* b3 = b2 + kstep;
;             if (last && has_next) S.a_ready(nxt);
;             if constexpr (SP2) {
;             PG8_LDB(B0, 0, 0); PG8_LDB(B1, 0, 1); PG8_SCHED; PG8_LDA(At, 0, 0); PG8_STAGE(PG8_SA(1, 1), a1 + hstepA, voffA);
;             PG8_WAIT_V(8); PG8_WAIT_L(0); PG8_BAR; PG8_MMA(0, 0, At, B0); PG8_MMA(0, 1, At, B1); PG8_BAR; PG8_SCHED;
;             PG8_LDA(At, 0, 1); PG8_STAGE(PG8_SB(0, 0), b2, voffB); PG8_STAGE(PG8_SB(0, 1), b2 + hstepB, voffB); PG8_STAGE(PG8_SA(0, 0), a2, voffA);
;             PG8_WAIT_V(8); PG8_WAIT_L(0); PG8_BAR; PG8_MMA(1, 0, At, B0); PG8_MMA(1, 1, At, B1); PG8_BAR; PG8_SCHED;
.LBB0_2049:
	ds_read_b128 v[146:149], v179
	ds_read_b128 v[150:153], v179 offset:1024
	ds_read_b128 v[154:157], v179 offset:2048
	ds_read_b128 v[158:161], v179 offset:3072
	ds_read_b128 v[162:165], v180
	ds_read_b128 v[166:169], v180 offset:1024
	ds_read_b128 v[184:187], v180 offset:2048
	ds_read_b128 v[188:191], v180 offset:3072
	s_add_u32 s12, s8, 0xfffc0080
	s_addc_u32 s13, s9, -1
	s_cmp_eq_u32 s71, 12
	s_cselect_b32 s39, s7, s13
	s_cselect_b32 s38, s11, s12
	s_cselect_b32 s13, s29, s41
	s_cselect_b32 s12, s31, s40
	s_add_i32 m0, s46, 0xc000
	ds_read_b128 v[192:195], v181
	ds_read_b128 v[196:199], v181 offset:1024
	ds_read_b128 v[200:203], v181 offset:2048
	ds_read_b128 v[204:207], v181 offset:3072
	ds_read_b128 v[208:211], v181 offset:4096
	ds_read_b128 v[212:215], v181 offset:5120
	ds_read_b128 v[216:219], v181 offset:6144
	ds_read_b128 v[220:223], v181 offset:7168
	global_load_lds_dwordx4 v138, s[8:9]
	s_add_i32 m0, s46, 0xe000
	s_nop 0
	global_load_lds_dwordx4 v140, s[8:9]
	s_waitcnt vmcnt(8) lgkmcnt(0)
	s_barrier
	s_setprio 1
	v_mfma_f32_16x16x32_bf16 v[124:127], v[146:149], v[192:195], v[124:127]
	v_mfma_f32_16x16x32_bf16 v[120:123], v[154:157], v[192:195], v[120:123]
	v_mfma_f32_16x16x32_bf16 v[108:111], v[146:149], v[200:203], v[108:111]
	v_mfma_f32_16x16x32_bf16 v[104:107], v[154:157], v[200:203], v[104:107]
	v_mfma_f32_16x16x32_bf16 v[92:95], v[146:149], v[208:211], v[92:95]
	v_mfma_f32_16x16x32_bf16 v[88:91], v[154:157], v[208:211], v[88:91]
	v_mfma_f32_16x16x32_bf16 v[76:79], v[146:149], v[216:219], v[76:79]
	v_mfma_f32_16x16x32_bf16 v[72:75], v[154:157], v[216:219], v[72:75]
	v_mfma_f32_16x16x32_bf16 v[124:127], v[150:153], v[196:199], v[124:127]
	v_mfma_f32_16x16x32_bf16 v[120:123], v[158:161], v[196:199], v[120:123]
	v_mfma_f32_16x16x32_bf16 v[108:111], v[150:153], v[204:207], v[108:111]
	v_mfma_f32_16x16x32_bf16 v[104:107], v[158:161], v[204:207], v[104:107]
	v_mfma_f32_16x16x32_bf16 v[92:95], v[150:153], v[212:215], v[92:95]
	v_mfma_f32_16x16x32_bf16 v[88:91], v[158:161], v[212:215], v[88:91]
	v_mfma_f32_16x16x32_bf16 v[76:79], v[150:153], v[220:223], v[76:79]
	v_mfma_f32_16x16x32_bf16 v[72:75], v[158:161], v[220:223], v[72:75]
	s_setprio 0
	s_setprio 1
	v_mfma_f32_16x16x32_bf16 v[116:119], v[162:165], v[192:195], v[116:119]
	v_mfma_f32_16x16x32_bf16 v[112:115], v[184:187], v[192:195], v[112:115]
	v_mfma_f32_16x16x32_bf16 v[100:103], v[162:165], v[200:203], v[100:103]
	v_mfma_f32_16x16x32_bf16 v[96:99], v[184:187], v[200:203], v[96:99]
	v_mfma_f32_16x16x32_bf16 v[84:87], v[162:165], v[208:211], v[84:87]
	v_mfma_f32_16x16x32_bf16 v[80:83], v[184:187], v[208:211], v[80:83]
	v_mfma_f32_16x16x32_bf16 v[68:71], v[162:165], v[216:219], v[68:71]
	v_mfma_f32_16x16x32_bf16 v[64:67], v[184:187], v[216:219], v[64:67]
	v_mfma_f32_16x16x32_bf16 v[116:119], v[166:169], v[196:199], v[116:119]
	v_mfma_f32_16x16x32_bf16 v[112:115], v[188:191], v[196:199], v[112:115]
	v_mfma_f32_16x16x32_bf16 v[100:103], v[166:169], v[204:207], v[100:103]
	v_mfma_f32_16x16x32_bf16 v[96:99], v[188:191], v[204:207], v[96:99]
	v_mfma_f32_16x16x32_bf16 v[84:87], v[166:169], v[212:215], v[84:87]
	v_mfma_f32_16x16x32_bf16 v[80:83], v[188:191], v[212:215], v[80:83]
	v_mfma_f32_16x16x32_bf16 v[68:71], v[166:169], v[220:223], v[68:71]
	v_mfma_f32_16x16x32_bf16 v[64:67], v[188:191], v[220:223], v[64:67]
	s_setprio 0
	s_barrier
	s_add_i32 s72, s69, s45
	s_add_u32 s98, s12, 0x80
	s_addc_u32 s99, s13, 0
	s_mov_b32 m0, s72
	ds_read_b128 v[192:195], v181 offset:16384
	ds_read_b128 v[196:199], v181 offset:17408
	ds_read_b128 v[200:203], v181 offset:18432
	ds_read_b128 v[204:207], v181 offset:19456
	ds_read_b128 v[208:211], v181 offset:20480
	ds_read_b128 v[212:215], v181 offset:21504
	ds_read_b128 v[216:219], v181 offset:22528
	ds_read_b128 v[220:223], v181 offset:23552
	global_load_lds_dwordx4 v130, s[12:13]
	s_add_i32 m0, s72, 0x2000
	s_add_u32 s72, s12, 0x40000
	s_addc_u32 s73, s13, 0
	s_add_i32 s74, s70, s45
	global_load_lds_dwordx4 v134, s[12:13]
	s_mov_b32 m0, s74
	s_add_u32 s100, s38, 0x80
	s_addc_u32 s101, s39, 0
	global_load_lds_dwordx4 v130, s[72:73]
	s_add_i32 m0, s74, 0x2000
	s_nop 0
	global_load_lds_dwordx4 v134, s[72:73]
	s_mov_b32 m0, s46
	s_nop 0
	global_load_lds_dwordx4 v128, s[38:39]
	s_mov_b32 m0, s47
	s_nop 0
	global_load_lds_dwordx4 v132, s[38:39]
	s_waitcnt vmcnt(8) lgkmcnt(0)
	s_barrier
	s_setprio 1
	v_mfma_f32_16x16x32_bf16 v[60:63], v[146:149], v[192:195], v[60:63]
	v_mfma_f32_16x16x32_bf16 v[56:59], v[154:157], v[192:195], v[56:59]
	v_mfma_f32_16x16x32_bf16 v[44:47], v[146:149], v[200:203], v[44:47]
	v_mfma_f32_16x16x32_bf16 v[40:43], v[154:157], v[200:203], v[40:43]
	v_mfma_f32_16x16x32_bf16 v[28:31], v[146:149], v[208:211], v[28:31]
	v_mfma_f32_16x16x32_bf16 v[24:27], v[154:157], v[208:211], v[24:27]
	v_mfma_f32_16x16x32_bf16 v[12:15], v[146:149], v[216:219], v[12:15]
	v_mfma_f32_16x16x32_bf16 v[8:11], v[154:157], v[216:219], v[8:11]
	v_mfma_f32_16x16x32_bf16 v[60:63], v[150:153], v[196:199], v[60:63]
	v_mfma_f32_16x16x32_bf16 v[56:59], v[158:161], v[196:199], v[56:59]
	v_mfma_f32_16x16x32_bf16 v[44:47], v[150:153], v[204:207], v[44:47]
	v_mfma_f32_16x16x32_bf16 v[40:43], v[158:161], v[204:207], v[40:43]
	v_mfma_f32_16x16x32_bf16 v[28:31], v[150:153], v[212:215], v[28:31]
	v_mfma_f32_16x16x32_bf16 v[24:27], v[158:161], v[212:215], v[24:27]
	v_mfma_f32_16x16x32_bf16 v[12:15], v[150:153], v[220:223], v[12:15]
	v_mfma_f32_16x16x32_bf16 v[8:11], v[158:161], v[220:223], v[8:11]
	s_setprio 0
	s_setprio 1
	v_mfma_f32_16x16x32_bf16 v[52:55], v[162:165], v[192:195], v[52:55]
	v_mfma_f32_16x16x32_bf16 v[48:51], v[184:187], v[192:195], v[48:51]
	v_mfma_f32_16x16x32_bf16 v[36:39], v[162:165], v[200:203], v[36:39]
	v_mfma_f32_16x16x32_bf16 v[32:35], v[184:187], v[200:203], v[32:35]
	v_mfma_f32_16x16x32_bf16 v[20:23], v[162:165], v[208:211], v[20:23]
	v_mfma_f32_16x16x32_bf16 v[16:19], v[184:187], v[208:211], v[16:19]
	v_mfma_f32_16x16x32_bf16 v[4:7], v[162:165], v[216:219], v[4:7]
	v_mfma_f32_16x16x32_bf16 v[0:3], v[184:187], v[216:219], v[0:3]
	v_mfma_f32_16x16x32_bf16 v[52:55], v[166:169], v[196:199], v[52:55]
	v_mfma_f32_16x16x32_bf16 v[48:51], v[188:191], v[196:199], v[48:51]
	v_mfma_f32_16x16x32_bf16 v[36:39], v[166:169], v[204:207], v[36:39]
	v_mfma_f32_16x16x32_bf16 v[32:35], v[188:191], v[204:207], v[32:35]
	v_mfma_f32_16x16x32_bf16 v[20:23], v[166:169], v[212:215], v[20:23]
	v_mfma_f32_16x16x32_bf16 v[16:19], v[188:191], v[212:215], v[16:19]
	v_mfma_f32_16x16x32_bf16 v[4:7], v[166:169], v[220:223], v[4:7]
	v_mfma_f32_16x16x32_bf16 v[0:3], v[188:191], v[220:223], v[0:3]
	s_setprio 0
	s_barrier
; #define PG8_STAGE(bufoff, gbase, voff) do { _Pragma("unroll") for (int _i = 0; _i < 2; ++_i) \
;         __builtin_amdgcn_global_load_lds((const unsigned*)((const char*)(gbase) + (voff)[_i]), (PG8_LAS unsigned*)(lds + (bufoff) + ldsw + _i * 8192), 16, 0, 0); } while (0)
; #define PG8_LDA(dst, b, h) do { _Pragma("unroll") for (int m = 0; m < 4; ++m) _Pragma("unroll") for (int k = 0; k < 2; ++k) dst[m][k] = *(const PG8_LAS bf16x8*)(lds + PG8_SA(b, h) + aoff + m * 2048 + k * 1024); } while (0)
; #define PG8_WAIT_V(n) asm volatile("s_waitcnt vmcnt(" #n ")" ::: "memory")
; #define PG8_WAIT_L(n) asm volatile("s_waitcnt lgkmcnt(" #n ")" ::: "memory")
; #define PG8_BAR __builtin_amdgcn_s_barrier()
; template <class Epi, class Sched, bool ALIGN_EPI = false, bool SP2 = false>
; __device__ __forceinline__ void gemm_phase(PG8_LAS unsigned char* lds, const Gemm g, const Sched& S, const Epi& E, const int wid) {
;     ...
;         for (int t = 0; t < nt; t += 2) {
;             const bool last = (t == nt - 2);
;             const char* a1 = cA + (size_t)(t + 1) * kstep;
;             const char* a2 = last ? nA : cA + (size_t)(t + 2) * kstep; const char* b2 = last ? nB : cB + (size_t)(t + 2) * kstep;
;             const char* a3 = a2 + kstep; const char* b3 = b2 + kstep;
;             if (last && has_next) S.a_ready(nxt);
;             if constexpr (SP2) {
;             PG8_LDB(B0, 0, 0); PG8_LDB(B1, 0, 1); PG8_SCHED; PG8_LDA(At, 0, 0); PG8_STAGE(PG8_SA(1, 1), a1 + hstepA, voffA);
;             PG8_WAIT_V(8); PG8_WAIT_L(0); PG8_BAR; PG8_MMA(0, 0, At, B0); PG8_MMA(0, 1, At, B1); PG8_BAR; PG8_SCHED;
;             PG8_LDA(At, 0, 1); PG8_STAGE(PG8_SB(0, 0), b2, voffB); PG8_STAGE(PG8_SB(0, 1), b2 + hstepB, voffB); PG8_STAGE(PG8_SA(0, 0), a2, voffA);
;             PG8_WAIT_V(8); PG8_WAIT_L(0); PG8_BAR; PG8_MMA(1, 0, At, B0); PG8_MMA(1, 1, At, B1); PG8_BAR; PG8_SCHED;
;             PG8_LDB(B0, 1, 0); PG8_LDB(B1, 1, 1); PG8_SCHED; PG8_LDA(At, 1, 0); PG8_STAGE(PG8_SA(0, 1), a2 + hstepA, voffA);
;             PG8_WAIT_V(8); PG8_WAIT_L(0); PG8_BAR; PG8_MMA(0, 0, At, B0); PG8_MMA(0, 1, At, B1); PG8_BAR; PG8_SCHED;
;             PG8_LDA(At, 1, 1); PG8_STAGE(PG8_SB(1, 0), b3, voffB); PG8_STAGE(PG8_SB(1, 1), b3 + hstepB, voffB); PG8_STAGE(PG8_SA(1, 0), a3, voffA);
;             PG8_WAIT_V(8); PG8_WAIT_L(0); PG8_BAR; PG8_MMA(1, 0, At, B0); PG8_MMA(1, 1, At, B1); PG8_BAR; PG8_SCHED;
	s_add_i32 s72, 0, 0x18000
	s_add_i32 s73, 0, 0x1c000
	v_add_u32_e32 v158, s72, v174
	v_add_u32_e32 v188, s73, v174
	ds_read_b128 v[146:149], v158
	ds_read_b128 v[150:153], v158 offset:1024
	ds_read_b128 v[154:157], v158 offset:2048
	ds_read_b128 v[158:161], v158 offset:3072
	ds_read_b128 v[162:165], v188
	ds_read_b128 v[166:169], v188 offset:1024
	ds_read_b128 v[184:187], v188 offset:2048
	ds_read_b128 v[188:191], v188 offset:3072
	s_add_u32 s38, s38, 0x40000
	s_addc_u32 s39, s39, 0
	s_mov_b32 m0, s48
	ds_read_b128 v[192:195], v181 offset:32768
	ds_read_b128 v[196:199], v181 offset:33792
	ds_read_b128 v[200:203], v181 offset:34816
	ds_read_b128 v[204:207], v181 offset:35840
	ds_read_b128 v[208:211], v181 offset:36864
	ds_read_b128 v[212:215], v181 offset:37888
	ds_read_b128 v[216:219], v181 offset:38912
	ds_read_b128 v[220:223], v181 offset:39936
	global_load_lds_dwordx4 v128, s[38:39]
	s_mov_b32 m0, s49
	s_nop 0
	global_load_lds_dwordx4 v132, s[38:39]
	s_waitcnt vmcnt(8) lgkmcnt(0)
	s_barrier
	s_setprio 1
	v_mfma_f32_16x16x32_bf16 v[124:127], v[146:149], v[192:195], v[124:127]
	v_mfma_f32_16x16x32_bf16 v[120:123], v[154:157], v[192:195], v[120:123]
	v_mfma_f32_16x16x32_bf16 v[108:111], v[146:149], v[200:203], v[108:111]
	v_mfma_f32_16x16x32_bf16 v[104:107], v[154:157], v[200:203], v[104:107]
	v_mfma_f32_16x16x32_bf16 v[92:95], v[146:149], v[208:211], v[92:95]
	v_mfma_f32_16x16x32_bf16 v[88:91], v[154:157], v[208:211], v[88:91]
	v_mfma_f32_16x16x32_bf16 v[76:79], v[146:149], v[216:219], v[76:79]
	v_mfma_f32_16x16x32_bf16 v[72:75], v[154:157], v[216:219], v[72:75]
	v_mfma_f32_16x16x32_bf16 v[124:127], v[150:153], v[196:199], v[124:127]
	v_mfma_f32_16x16x32_bf16 v[120:123], v[158:161], v[196:199], v[120:123]
	v_mfma_f32_16x16x32_bf16 v[108:111], v[150:153], v[204:207], v[108:111]
	v_mfma_f32_16x16x32_bf16 v[104:107], v[158:161], v[204:207], v[104:107]
	v_mfma_f32_16x16x32_bf16 v[92:95], v[150:153], v[212:215], v[92:95]
	v_mfma_f32_16x16x32_bf16 v[88:91], v[158:161], v[212:215], v[88:91]
	v_mfma_f32_16x16x32_bf16 v[76:79], v[150:153], v[220:223], v[76:79]
	v_mfma_f32_16x16x32_bf16 v[72:75], v[158:161], v[220:223], v[72:75]
	s_setprio 0
	s_setprio 1
	v_mfma_f32_16x16x32_bf16 v[116:119], v[162:165], v[192:195], v[116:119]
	v_mfma_f32_16x16x32_bf16 v[112:115], v[184:187], v[192:195], v[112:115]
	v_mfma_f32_16x16x32_bf16 v[100:103], v[162:165], v[200:203], v[100:103]
	v_mfma_f32_16x16x32_bf16 v[96:99], v[184:187], v[200:203], v[96:99]
	v_mfma_f32_16x16x32_bf16 v[84:87], v[162:165], v[208:211], v[84:87]
	v_mfma_f32_16x16x32_bf16 v[80:83], v[184:187], v[208:211], v[80:83]
	v_mfma_f32_16x16x32_bf16 v[68:71], v[162:165], v[216:219], v[68:71]
	v_mfma_f32_16x16x32_bf16 v[64:67], v[184:187], v[216:219], v[64:67]
	v_mfma_f32_16x16x32_bf16 v[116:119], v[166:169], v[196:199], v[116:119]
	v_mfma_f32_16x16x32_bf16 v[112:115], v[188:191], v[196:199], v[112:115]
	v_mfma_f32_16x16x32_bf16 v[100:103], v[166:169], v[204:207], v[100:103]
	v_mfma_f32_16x16x32_bf16 v[96:99], v[188:191], v[204:207], v[96:99]
	v_mfma_f32_16x16x32_bf16 v[84:87], v[166:169], v[212:215], v[84:87]
	v_mfma_f32_16x16x32_bf16 v[80:83], v[188:191], v[212:215], v[80:83]
	v_mfma_f32_16x16x32_bf16 v[68:71], v[166:169], v[220:223], v[68:71]
	v_mfma_f32_16x16x32_bf16 v[64:67], v[188:191], v[220:223], v[64:67]
	s_setprio 0
	s_barrier
	s_add_i32 s38, s72, s45
	s_mov_b32 m0, s38
	ds_read_b128 v[192:195], v181 offset:49152
	ds_read_b128 v[196:199], v181 offset:50176
	ds_read_b128 v[200:203], v181 offset:51200
	ds_read_b128 v[204:207], v181 offset:52224
	ds_read_b128 v[208:211], v181 offset:53248
	ds_read_b128 v[212:215], v181 offset:54272
	ds_read_b128 v[216:219], v181 offset:55296
	ds_read_b128 v[220:223], v181 offset:56320
	global_load_lds_dwordx4 v130, s[98:99]
	s_add_i32 m0, s38, 0x2000
	s_add_u32 s12, s12, 0x40080
	s_addc_u32 s13, s13, 0
	s_add_i32 s38, s73, s45
	global_load_lds_dwordx4 v134, s[98:99]
	s_mov_b32 m0, s38
	s_nop 0
	global_load_lds_dwordx4 v130, s[12:13]
	s_add_i32 m0, s38, 0x2000
	s_nop 0
	global_load_lds_dwordx4 v134, s[12:13]
	s_mov_b32 m0, s65
	s_nop 0
	global_load_lds_dwordx4 v128, s[100:101]
	s_mov_b32 m0, s66
	s_nop 0
	global_load_lds_dwordx4 v132, s[100:101]
	s_waitcnt vmcnt(8) lgkmcnt(0)
	s_barrier
	s_setprio 1
	v_mfma_f32_16x16x32_bf16 v[60:63], v[146:149], v[192:195], v[60:63]
	v_mfma_f32_16x16x32_bf16 v[56:59], v[154:157], v[192:195], v[56:59]
	v_mfma_f32_16x16x32_bf16 v[44:47], v[146:149], v[200:203], v[44:47]
	v_mfma_f32_16x16x32_bf16 v[40:43], v[154:157], v[200:203], v[40:43]
	v_mfma_f32_16x16x32_bf16 v[28:31], v[146:149], v[208:211], v[28:31]
	v_mfma_f32_16x16x32_bf16 v[24:27], v[154:157], v[208:211], v[24:27]
	v_mfma_f32_16x16x32_bf16 v[12:15], v[146:149], v[216:219], v[12:15]
	v_mfma_f32_16x16x32_bf16 v[8:11], v[154:157], v[216:219], v[8:11]
	v_mfma_f32_16x16x32_bf16 v[60:63], v[150:153], v[196:199], v[60:63]
	v_mfma_f32_16x16x32_bf16 v[56:59], v[158:161], v[196:199], v[56:59]
	v_mfma_f32_16x16x32_bf16 v[44:47], v[150:153], v[204:207], v[44:47]
	v_mfma_f32_16x16x32_bf16 v[40:43], v[158:161], v[204:207], v[40:43]
	v_mfma_f32_16x16x32_bf16 v[28:31], v[150:153], v[212:215], v[28:31]
	v_mfma_f32_16x16x32_bf16 v[24:27], v[158:161], v[212:215], v[24:27]
	v_mfma_f32_16x16x32_bf16 v[12:15], v[150:153], v[220:223], v[12:15]
	v_mfma_f32_16x16x32_bf16 v[8:11], v[158:161], v[220:223], v[8:11]
	s_setprio 0
	s_setprio 1
	v_mfma_f32_16x16x32_bf16 v[52:55], v[162:165], v[192:195], v[52:55]
	v_mfma_f32_16x16x32_bf16 v[48:51], v[184:187], v[192:195], v[48:51]
	v_mfma_f32_16x16x32_bf16 v[36:39], v[162:165], v[200:203], v[36:39]
	v_mfma_f32_16x16x32_bf16 v[32:35], v[184:187], v[200:203], v[32:35]
	v_mfma_f32_16x16x32_bf16 v[20:23], v[162:165], v[208:211], v[20:23]
	v_mfma_f32_16x16x32_bf16 v[16:19], v[184:187], v[208:211], v[16:19]
	v_mfma_f32_16x16x32_bf16 v[4:7], v[162:165], v[216:219], v[4:7]
	v_mfma_f32_16x16x32_bf16 v[0:3], v[184:187], v[216:219], v[0:3]
	v_mfma_f32_16x16x32_bf16 v[52:55], v[166:169], v[196:199], v[52:55]
	v_mfma_f32_16x16x32_bf16 v[48:51], v[188:191], v[196:199], v[48:51]
	v_mfma_f32_16x16x32_bf16 v[36:39], v[166:169], v[204:207], v[36:39]
	v_mfma_f32_16x16x32_bf16 v[32:35], v[188:191], v[204:207], v[32:35]
	v_mfma_f32_16x16x32_bf16 v[20:23], v[166:169], v[212:215], v[20:23]
	v_mfma_f32_16x16x32_bf16 v[16:19], v[188:191], v[212:215], v[16:19]
	v_mfma_f32_16x16x32_bf16 v[4:7], v[166:169], v[220:223], v[4:7]
	v_mfma_f32_16x16x32_bf16 v[0:3], v[188:191], v[220:223], v[0:3]
	s_setprio 0
	s_barrier
	s_add_i32 s71, s71, 2
	s_add_u32 s8, s8, 0x100
	s_addc_u32 s9, s9, 0
	s_add_u32 s40, s40, 0x100
	s_addc_u32 s41, s41, 0
	s_cmp_gt_u32 s71, 13
	s_cbranch_scc0 .LBB0_2049
	s_and_b64 vcc, exec, s[20:21]
	s_cbranch_vccz .LBB0_2052
	s_barrier

; #define PG8_STAGE(bufoff, gbase, voff) do { _Pragma("unroll") for (int _i = 0; _i < 2; ++_i) \
;         __builtin_amdgcn_global_load_lds((const unsigned*)((const char*)(gbase) + (voff)[_i]), (PG8_LAS unsigned*)(lds + (bufoff) + ldsw + _i * 8192), 16, 0, 0); } while (0)
; #define PG8_LDA(dst, b, h) do { _Pragma("unroll") for (int m = 0; m < 4; ++m) _Pragma("unroll") for (int k = 0; k < 2; ++k) dst[m][k] = *(const PG8_LAS bf16x8*)(lds + PG8_SA(b, h) + aoff + m * 2048 + k * 1024); } while (0)
; #define PG8_LDB(dst, b, h) do { _Pragma("unroll") for (int n = 0; n < 2; ++n) _Pragma("unroll") for (int k = 0; k < 2; ++k) dst[n][k] = *(const PG8_LAS bf16x8*)(lds + PG8_SB(b, h) + boff + n * 2048 + k * 1024); } while (0)
; #define PG8_WAIT_V(n) asm volatile("s_waitcnt vmcnt(" #n ")" ::: "memory")
; #define PG8_WAIT_L(n) asm volatile("s_waitcnt lgkmcnt(" #n ")" ::: "memory")
; #define PG8_BAR __builtin_amdgcn_s_barrier()
; #define PG8_SCHED __builtin_amdgcn_sched_barrier(0)
; template <class Epi, class Sched, bool ALIGN_EPI = false, bool SP2 = false>
; __device__ __forceinline__ void gemm_phase(PG8_LAS unsigned char* lds, const Gemm g, const Sched& S, const Epi& E, const int wid) {
;     ...
;         const bool has_next = S.next(ui + 1, nxt);
;         const char* nA = has_next ? (const char*)g.A + (size_t)nxt.pm * tstepA : cA; const char* nB = has_next ? (const char*)g.Bt + (size_t)nxt.pn * tstepB : cB;
;         for (int t = 0; t < nt; t += 2) {
;             const bool last = (t == nt - 2);
;             const char* a1 = cA + (size_t)(t + 1) * kstep;
;             const char* a2 = last ? nA : cA + (size_t)(t + 2) * kstep; const char* b2 = last ? nB : cB + (size_t)(t + 2) * kstep;
;             const char* a3 = a2 + kstep; const char* b3 = b2 + kstep;
;             if (last && has_next) S.a_ready(nxt);
;             if constexpr (SP2) {
;             PG8_LDB(B0, 0, 0); PG8_LDB(B1, 0, 1); PG8_SCHED; PG8_LDA(At, 0, 0); PG8_STAGE(PG8_SA(1, 1), a1 + hstepA, voffA);
;             PG8_WAIT_V(8); PG8_WAIT_L(0); PG8_BAR; PG8_MMA(0, 0, At, B0); PG8_MMA(0, 1, At, B1); PG8_BAR; PG8_SCHED;
;             PG8_LDA(At, 0, 1); PG8_STAGE(PG8_SB(0, 0), b2, voffB); PG8_STAGE(PG8_SB(0, 1), b2 + hstepB, voffB); PG8_STAGE(PG8_SA(0, 0), a2, voffA);
;             PG8_WAIT_V(8); PG8_WAIT_L(0); PG8_BAR; PG8_MMA(1, 0, At, B0); PG8_MMA(1, 1, At, B1); PG8_BAR; PG8_SCHED;
.LBB0_2280:
	s_add_u32 s37, s28, s36
	s_addc_u32 s44, s29, 0
	s_add_u32 s40, s37, 0x100
	s_addc_u32 s41, s44, 0
	s_and_b64 s[38:39], s[34:35], exec
	s_cselect_b32 s39, s19, s41
	s_cselect_b32 s38, s81, s40
	s_add_u32 s36, s26, s36
	s_addc_u32 s40, s27, 0
	s_add_u32 s36, s36, 0x100
	s_addc_u32 s40, s40, 0
	s_and_b64 s[34:35], s[34:35], exec
	s_cselect_b32 s41, s17, s40
	s_cselect_b32 s40, s82, s36
	s_add_u32 s46, s37, 0x80080
	ds_read_b128 v[142:145], v157
	ds_read_b128 v[146:149], v157 offset:1024
	ds_read_b128 v[150:153], v157 offset:2048
	ds_read_b128 v[162:165], v157 offset:3072
	ds_read_b128 v[166:169], v158
	ds_read_b128 v[170:173], v158 offset:1024
	ds_read_b128 v[174:177], v158 offset:2048
	ds_read_b128 v[178:181], v158 offset:3072
	s_addc_u32 s47, s44, 0
	s_add_i32 s93, s77, s0
	s_add_i32 m0, s70, 0xc000
	s_add_i32 s94, s70, 0xe000
	s_add_i32 s89, s93, 0x2000
	s_add_u32 s44, s40, 0x10000
	s_addc_u32 s45, s41, 0
	s_add_i32 s92, s78, s0
	s_add_i32 s91, s92, 0x2000
	s_add_i32 s88, 0, 0x18000
	s_add_i32 s87, 0, 0x1c000
	s_add_u32 s36, s38, 0x80000
	s_addc_u32 s37, s39, 0
	s_add_i32 s86, s88, s0
	s_add_i32 s84, s86, 0x2000
	s_add_u32 s34, s40, 0x10080
	s_addc_u32 s35, s41, 0
	s_add_i32 s85, s87, s0
	s_add_i32 s83, s85, 0x2000
	ds_read_b128 v[182:185], v159
	ds_read_b128 v[186:189], v159 offset:1024
	ds_read_b128 v[190:193], v159 offset:2048
	ds_read_b128 v[194:197], v159 offset:3072
	ds_read_b128 v[198:201], v159 offset:4096
	ds_read_b128 v[202:205], v159 offset:5120
	ds_read_b128 v[206:209], v159 offset:6144
	ds_read_b128 v[210:213], v159 offset:7168
	global_load_lds_dwordx4 v134, s[46:47]
	s_mov_b32 m0, s94
	s_nop 0
	global_load_lds_dwordx4 v130, s[46:47]
	s_waitcnt vmcnt(8) lgkmcnt(0)
	s_barrier
	s_setprio 1
	v_mfma_f32_16x16x32_bf16 v[124:127], v[142:145], v[182:185], v[124:127]
	v_mfma_f32_16x16x32_bf16 v[120:123], v[150:153], v[182:185], v[120:123]
	v_mfma_f32_16x16x32_bf16 v[116:119], v[142:145], v[190:193], v[116:119]
	v_mfma_f32_16x16x32_bf16 v[112:115], v[150:153], v[190:193], v[112:115]
	v_mfma_f32_16x16x32_bf16 v[100:103], v[142:145], v[198:201], v[100:103]
	v_mfma_f32_16x16x32_bf16 v[96:99], v[150:153], v[198:201], v[96:99]
	v_mfma_f32_16x16x32_bf16 v[84:87], v[142:145], v[206:209], v[84:87]
	v_mfma_f32_16x16x32_bf16 v[80:83], v[150:153], v[206:209], v[80:83]
	v_mfma_f32_16x16x32_bf16 v[124:127], v[146:149], v[186:189], v[124:127]
	v_mfma_f32_16x16x32_bf16 v[120:123], v[162:165], v[186:189], v[120:123]
	v_mfma_f32_16x16x32_bf16 v[116:119], v[146:149], v[194:197], v[116:119]
	v_mfma_f32_16x16x32_bf16 v[112:115], v[162:165], v[194:197], v[112:115]
	v_mfma_f32_16x16x32_bf16 v[100:103], v[146:149], v[202:205], v[100:103]
	v_mfma_f32_16x16x32_bf16 v[96:99], v[162:165], v[202:205], v[96:99]
	v_mfma_f32_16x16x32_bf16 v[84:87], v[146:149], v[210:213], v[84:87]
	v_mfma_f32_16x16x32_bf16 v[80:83], v[162:165], v[210:213], v[80:83]
	s_setprio 0
	s_setprio 1
	v_mfma_f32_16x16x32_bf16 v[108:111], v[166:169], v[182:185], v[108:111]
	v_mfma_f32_16x16x32_bf16 v[104:107], v[174:177], v[182:185], v[104:107]
	v_mfma_f32_16x16x32_bf16 v[92:95], v[166:169], v[190:193], v[92:95]
	v_mfma_f32_16x16x32_bf16 v[88:91], v[174:177], v[190:193], v[88:91]
	v_mfma_f32_16x16x32_bf16 v[76:79], v[166:169], v[198:201], v[76:79]
	v_mfma_f32_16x16x32_bf16 v[72:75], v[174:177], v[198:201], v[72:75]
	v_mfma_f32_16x16x32_bf16 v[68:71], v[166:169], v[206:209], v[68:71]
	v_mfma_f32_16x16x32_bf16 v[64:67], v[174:177], v[206:209], v[64:67]
	v_mfma_f32_16x16x32_bf16 v[108:111], v[170:173], v[186:189], v[108:111]
	v_mfma_f32_16x16x32_bf16 v[104:107], v[178:181], v[186:189], v[104:107]
	v_mfma_f32_16x16x32_bf16 v[92:95], v[170:173], v[194:197], v[92:95]
	v_mfma_f32_16x16x32_bf16 v[88:91], v[178:181], v[194:197], v[88:91]
	v_mfma_f32_16x16x32_bf16 v[76:79], v[170:173], v[202:205], v[76:79]
	v_mfma_f32_16x16x32_bf16 v[72:75], v[178:181], v[202:205], v[72:75]
	v_mfma_f32_16x16x32_bf16 v[68:71], v[170:173], v[210:213], v[68:71]
	v_mfma_f32_16x16x32_bf16 v[64:67], v[178:181], v[210:213], v[64:67]
	s_setprio 0
	s_barrier
	s_mov_b32 m0, s93
	s_add_u32 s98, s40, 0x80
	s_addc_u32 s99, s41, 0
	ds_read_b128 v[182:185], v159 offset:16384
	ds_read_b128 v[186:189], v159 offset:17408
	ds_read_b128 v[190:193], v159 offset:18432
	ds_read_b128 v[194:197], v159 offset:19456
	ds_read_b128 v[198:201], v159 offset:20480
	ds_read_b128 v[202:205], v159 offset:21504
	ds_read_b128 v[206:209], v159 offset:22528
	ds_read_b128 v[210:213], v159 offset:23552
	global_load_lds_dwordx4 v132, s[40:41]
	s_mov_b32 m0, s89
	s_nop 0
	global_load_lds_dwordx4 v128, s[40:41]
	s_mov_b32 m0, s92
	s_add_u32 s100, s38, 0x80
	s_addc_u32 s101, s39, 0
	global_load_lds_dwordx4 v132, s[44:45]
	s_mov_b32 m0, s91
	s_nop 0
	global_load_lds_dwordx4 v128, s[44:45]
	s_mov_b32 m0, s70
	s_nop 0
	global_load_lds_dwordx4 v134, s[38:39]
	s_mov_b32 m0, s71
	s_nop 0
	global_load_lds_dwordx4 v130, s[38:39]
	s_waitcnt vmcnt(8) lgkmcnt(0)
	s_barrier
; #define PG8_STAGE(bufoff, gbase, voff) do { _Pragma("unroll") for (int _i = 0; _i < 2; ++_i) \
;         __builtin_amdgcn_global_load_lds((const unsigned*)((const char*)(gbase) + (voff)[_i]), (PG8_LAS unsigned*)(lds + (bufoff) + ldsw + _i * 8192), 16, 0, 0); } while (0)
; #define PG8_LDA(dst, b, h) do { _Pragma("unroll") for (int m = 0; m < 4; ++m) _Pragma("unroll") for (int k = 0; k < 2; ++k) dst[m][k] = *(const PG8_LAS bf16x8*)(lds + PG8_SA(b, h) + aoff + m * 2048 + k * 1024); } while (0)
; #define PG8_LDB(dst, b, h) do { _Pragma("unroll") for (int n = 0; n < 2; ++n) _Pragma("unroll") for (int k = 0; k < 2; ++k) dst[n][k] = *(const PG8_LAS bf16x8*)(lds + PG8_SB(b, h) + boff + n * 2048 + k * 1024); } while (0)
; #define PG8_MMA(ai, bj, At, Bt) do { __builtin_amdgcn_s_setprio(1); _Pragma("unroll") for (int m = 0; m < 4; ++m) _Pragma("unroll") for (int n = 0; n < 2; ++n) _Pragma("unroll") for (int k = 0; k < 2; ++k) \
;         acc[ai][bj][m][n] = __builtin_amdgcn_mfma_f32_16x16x32_bf16(Bt[n][k], At[m][k], acc[ai][bj][m][n], 0, 0, 0); __builtin_amdgcn_s_setprio(0); } while (0)
; #define PG8_WAIT_V(n) asm volatile("s_waitcnt vmcnt(" #n ")" ::: "memory")
; #define PG8_WAIT_L(n) asm volatile("s_waitcnt lgkmcnt(" #n ")" ::: "memory")
; #define PG8_BAR __builtin_amdgcn_s_barrier()
; #define PG8_SCHED __builtin_amdgcn_sched_barrier(0)
; template <class Epi, class Sched, bool ALIGN_EPI = false, bool SP2 = false>
; __device__ __forceinline__ void gemm_phase(PG8_LAS unsigned char* lds, const Gemm g, const Sched& S, const Epi& E, const int wid) {
;     ...
;             PG8_WAIT_V(8); PG8_WAIT_L(0); PG8_BAR; PG8_MMA(0, 0, At, B0); PG8_MMA(0, 1, At, B1); PG8_BAR; PG8_SCHED;
;             PG8_LDA(At, 0, 1); PG8_STAGE(PG8_SB(0, 0), b2, voffB); PG8_STAGE(PG8_SB(0, 1), b2 + hstepB, voffB); PG8_STAGE(PG8_SA(0, 0), a2, voffA);
;             PG8_WAIT_V(8); PG8_WAIT_L(0); PG8_BAR; PG8_MMA(1, 0, At, B0); PG8_MMA(1, 1, At, B1); PG8_BAR; PG8_SCHED;
;             PG8_LDB(B0, 1, 0); PG8_LDB(B1, 1, 1); PG8_SCHED; PG8_LDA(At, 1, 0); PG8_STAGE(PG8_SA(0, 1), a2 + hstepA, voffA);
;             PG8_WAIT_V(8); PG8_WAIT_L(0); PG8_BAR; PG8_MMA(0, 0, At, B0); PG8_MMA(0, 1, At, B1); PG8_BAR; PG8_SCHED;
	s_setprio 1
	v_mfma_f32_16x16x32_bf16 v[60:63], v[142:145], v[182:185], v[60:63]
	v_mfma_f32_16x16x32_bf16 v[56:59], v[150:153], v[182:185], v[56:59]
	v_mfma_f32_16x16x32_bf16 v[52:55], v[142:145], v[190:193], v[52:55]
	v_mfma_f32_16x16x32_bf16 v[48:51], v[150:153], v[190:193], v[48:51]
	v_mfma_f32_16x16x32_bf16 v[36:39], v[142:145], v[198:201], v[36:39]
	v_mfma_f32_16x16x32_bf16 v[32:35], v[150:153], v[198:201], v[32:35]
	v_mfma_f32_16x16x32_bf16 v[20:23], v[142:145], v[206:209], v[20:23]
	v_mfma_f32_16x16x32_bf16 v[16:19], v[150:153], v[206:209], v[16:19]
	v_mfma_f32_16x16x32_bf16 v[60:63], v[146:149], v[186:189], v[60:63]
	v_mfma_f32_16x16x32_bf16 v[56:59], v[162:165], v[186:189], v[56:59]
	v_mfma_f32_16x16x32_bf16 v[52:55], v[146:149], v[194:197], v[52:55]
	v_mfma_f32_16x16x32_bf16 v[48:51], v[162:165], v[194:197], v[48:51]
	v_mfma_f32_16x16x32_bf16 v[36:39], v[146:149], v[202:205], v[36:39]
	v_mfma_f32_16x16x32_bf16 v[32:35], v[162:165], v[202:205], v[32:35]
	v_mfma_f32_16x16x32_bf16 v[20:23], v[146:149], v[210:213], v[20:23]
	v_mfma_f32_16x16x32_bf16 v[16:19], v[162:165], v[210:213], v[16:19]
	s_setprio 0
	s_setprio 1
	v_mfma_f32_16x16x32_bf16 v[44:47], v[166:169], v[182:185], v[44:47]
	v_mfma_f32_16x16x32_bf16 v[40:43], v[174:177], v[182:185], v[40:43]
	v_mfma_f32_16x16x32_bf16 v[28:31], v[166:169], v[190:193], v[28:31]
	v_mfma_f32_16x16x32_bf16 v[24:27], v[174:177], v[190:193], v[24:27]
	v_mfma_f32_16x16x32_bf16 v[12:15], v[166:169], v[198:201], v[12:15]
	v_mfma_f32_16x16x32_bf16 v[8:11], v[174:177], v[198:201], v[8:11]
	v_mfma_f32_16x16x32_bf16 v[4:7], v[166:169], v[206:209], v[4:7]
	v_mfma_f32_16x16x32_bf16 v[0:3], v[174:177], v[206:209], v[0:3]
	v_mfma_f32_16x16x32_bf16 v[44:47], v[170:173], v[186:189], v[44:47]
	v_mfma_f32_16x16x32_bf16 v[40:43], v[178:181], v[186:189], v[40:43]
	v_mfma_f32_16x16x32_bf16 v[28:31], v[170:173], v[194:197], v[28:31]
	v_mfma_f32_16x16x32_bf16 v[24:27], v[178:181], v[194:197], v[24:27]
	v_mfma_f32_16x16x32_bf16 v[12:15], v[170:173], v[202:205], v[12:15]
	v_mfma_f32_16x16x32_bf16 v[8:11], v[178:181], v[202:205], v[8:11]
	v_mfma_f32_16x16x32_bf16 v[4:7], v[170:173], v[210:213], v[4:7]
	v_mfma_f32_16x16x32_bf16 v[0:3], v[178:181], v[210:213], v[0:3]
	s_setprio 0
	s_barrier
	v_add_u32_e32 v161, s88, v156
	ds_read_b128 v[142:145], v161
	ds_read_b128 v[146:149], v161 offset:1024
	ds_read_b128 v[150:153], v161 offset:2048
	ds_read_b128 v[162:165], v161 offset:3072
	v_add_u32_e32 v161, s87, v156
	ds_read_b128 v[166:169], v161
	ds_read_b128 v[170:173], v161 offset:1024
	ds_read_b128 v[174:177], v161 offset:2048
	ds_read_b128 v[178:181], v161 offset:3072
	s_mov_b32 m0, s72
	ds_read_b128 v[182:185], v159 offset:32768
	ds_read_b128 v[186:189], v159 offset:33792
	ds_read_b128 v[190:193], v159 offset:34816
	ds_read_b128 v[194:197], v159 offset:35840
	ds_read_b128 v[198:201], v159 offset:36864
	ds_read_b128 v[202:205], v159 offset:37888
	ds_read_b128 v[206:209], v159 offset:38912
	ds_read_b128 v[210:213], v159 offset:39936
	global_load_lds_dwordx4 v134, s[36:37]
	s_mov_b32 m0, s73
	s_nop 0
	global_load_lds_dwordx4 v130, s[36:37]
	s_waitcnt vmcnt(8) lgkmcnt(0)
	s_barrier
	s_setprio 1
	v_mfma_f32_16x16x32_bf16 v[124:127], v[142:145], v[182:185], v[124:127]
	v_mfma_f32_16x16x32_bf16 v[120:123], v[150:153], v[182:185], v[120:123]
	v_mfma_f32_16x16x32_bf16 v[116:119], v[142:145], v[190:193], v[116:119]
	v_mfma_f32_16x16x32_bf16 v[112:115], v[150:153], v[190:193], v[112:115]
	v_mfma_f32_16x16x32_bf16 v[100:103], v[142:145], v[198:201], v[100:103]
	v_mfma_f32_16x16x32_bf16 v[96:99], v[150:153], v[198:201], v[96:99]
	v_mfma_f32_16x16x32_bf16 v[84:87], v[142:145], v[206:209], v[84:87]
	v_mfma_f32_16x16x32_bf16 v[80:83], v[150:153], v[206:209], v[80:83]
	v_mfma_f32_16x16x32_bf16 v[124:127], v[146:149], v[186:189], v[124:127]
	v_mfma_f32_16x16x32_bf16 v[120:123], v[162:165], v[186:189], v[120:123]
	v_mfma_f32_16x16x32_bf16 v[116:119], v[146:149], v[194:197], v[116:119]
	v_mfma_f32_16x16x32_bf16 v[112:115], v[162:165], v[194:197], v[112:115]
	v_mfma_f32_16x16x32_bf16 v[100:103], v[146:149], v[202:205], v[100:103]
	v_mfma_f32_16x16x32_bf16 v[96:99], v[162:165], v[202:205], v[96:99]
	v_mfma_f32_16x16x32_bf16 v[84:87], v[146:149], v[210:213], v[84:87]
	v_mfma_f32_16x16x32_bf16 v[80:83], v[162:165], v[210:213], v[80:83]
	s_setprio 0
	s_setprio 1
	v_mfma_f32_16x16x32_bf16 v[108:111], v[166:169], v[182:185], v[108:111]
	v_mfma_f32_16x16x32_bf16 v[104:107], v[174:177], v[182:185], v[104:107]
	v_mfma_f32_16x16x32_bf16 v[92:95], v[166:169], v[190:193], v[92:95]
	v_mfma_f32_16x16x32_bf16 v[88:91], v[174:177], v[190:193], v[88:91]
	v_mfma_f32_16x16x32_bf16 v[76:79], v[166:169], v[198:201], v[76:79]
	v_mfma_f32_16x16x32_bf16 v[72:75], v[174:177], v[198:201], v[72:75]
	v_mfma_f32_16x16x32_bf16 v[68:71], v[166:169], v[206:209], v[68:71]
	v_mfma_f32_16x16x32_bf16 v[64:67], v[174:177], v[206:209], v[64:67]
	v_mfma_f32_16x16x32_bf16 v[108:111], v[170:173], v[186:189], v[108:111]
	v_mfma_f32_16x16x32_bf16 v[104:107], v[178:181], v[186:189], v[104:107]
	v_mfma_f32_16x16x32_bf16 v[92:95], v[170:173], v[194:197], v[92:95]
	v_mfma_f32_16x16x32_bf16 v[88:91], v[178:181], v[194:197], v[88:91]
	v_mfma_f32_16x16x32_bf16 v[76:79], v[170:173], v[202:205], v[76:79]
	v_mfma_f32_16x16x32_bf16 v[72:75], v[178:181], v[202:205], v[72:75]
	v_mfma_f32_16x16x32_bf16 v[68:71], v[170:173], v[210:213], v[68:71]
	v_mfma_f32_16x16x32_bf16 v[64:67], v[178:181], v[210:213], v[64:67]
	s_setprio 0
	s_barrier
; #define PG8_STAGE(bufoff, gbase, voff) do { _Pragma("unroll") for (int _i = 0; _i < 2; ++_i) \
;         __builtin_amdgcn_global_load_lds((const unsigned*)((const char*)(gbase) + (voff)[_i]), (PG8_LAS unsigned*)(lds + (bufoff) + ldsw + _i * 8192), 16, 0, 0); } while (0)
; #define PG8_LDA(dst, b, h) do { _Pragma("unroll") for (int m = 0; m < 4; ++m) _Pragma("unroll") for (int k = 0; k < 2; ++k) dst[m][k] = *(const PG8_LAS bf16x8*)(lds + PG8_SA(b, h) + aoff + m * 2048 + k * 1024); } while (0)
; #define PG8_MMA(ai, bj, At, Bt) do { __builtin_amdgcn_s_setprio(1); _Pragma("unroll") for (int m = 0; m < 4; ++m) _Pragma("unroll") for (int n = 0; n < 2; ++n) _Pragma("unroll") for (int k = 0; k < 2; ++k) \
;         acc[ai][bj][m][n] = __builtin_amdgcn_mfma_f32_16x16x32_bf16(Bt[n][k], At[m][k], acc[ai][bj][m][n], 0, 0, 0); __builtin_amdgcn_s_setprio(0); } while (0)
; #define PG8_WAIT_V(n) asm volatile("s_waitcnt vmcnt(" #n ")" ::: "memory")
; #define PG8_WAIT_L(n) asm volatile("s_waitcnt lgkmcnt(" #n ")" ::: "memory")
; #define PG8_BAR __builtin_amdgcn_s_barrier()
; #define PG8_SCHED __builtin_amdgcn_sched_barrier(0)
; template <class Epi, class Sched, bool ALIGN_EPI = false, bool SP2 = false>
; __device__ __forceinline__ void gemm_phase(PG8_LAS unsigned char* lds, const Gemm g, const Sched& S, const Epi& E, const int wid) {
;     ...
;         for (int t = 0; t < nt; t += 2) {
;     ...
;             PG8_LDA(At, 1, 1); PG8_STAGE(PG8_SB(1, 0), b3, voffB); PG8_STAGE(PG8_SB(1, 1), b3 + hstepB, voffB); PG8_STAGE(PG8_SA(1, 0), a3, voffA);
;             PG8_WAIT_V(8); PG8_WAIT_L(0); PG8_BAR; PG8_MMA(1, 0, At, B0); PG8_MMA(1, 1, At, B1); PG8_BAR; PG8_SCHED;
	s_mov_b32 m0, s86
	ds_read_b128 v[182:185], v159 offset:49152
	ds_read_b128 v[186:189], v159 offset:50176
	ds_read_b128 v[190:193], v159 offset:51200
	ds_read_b128 v[194:197], v159 offset:52224
	ds_read_b128 v[198:201], v159 offset:53248
	ds_read_b128 v[202:205], v159 offset:54272
	ds_read_b128 v[206:209], v159 offset:55296
	ds_read_b128 v[210:213], v159 offset:56320
	global_load_lds_dwordx4 v132, s[98:99]
	s_mov_b32 m0, s84
	s_nop 0
	global_load_lds_dwordx4 v128, s[98:99]
	s_mov_b32 m0, s85
	s_nop 0
	global_load_lds_dwordx4 v132, s[34:35]
	s_mov_b32 m0, s83
	s_nop 0
	global_load_lds_dwordx4 v128, s[34:35]
	s_mov_b32 m0, s74
	s_nop 0
	global_load_lds_dwordx4 v134, s[100:101]
	s_mov_b32 m0, s75
	s_nop 0
	global_load_lds_dwordx4 v130, s[100:101]
	s_waitcnt vmcnt(8) lgkmcnt(0)
	s_barrier
	s_setprio 1
	v_mfma_f32_16x16x32_bf16 v[60:63], v[142:145], v[182:185], v[60:63]
	v_mfma_f32_16x16x32_bf16 v[56:59], v[150:153], v[182:185], v[56:59]
	v_mfma_f32_16x16x32_bf16 v[52:55], v[142:145], v[190:193], v[52:55]
	v_mfma_f32_16x16x32_bf16 v[48:51], v[150:153], v[190:193], v[48:51]
	v_mfma_f32_16x16x32_bf16 v[36:39], v[142:145], v[198:201], v[36:39]
	v_mfma_f32_16x16x32_bf16 v[32:35], v[150:153], v[198:201], v[32:35]
	v_mfma_f32_16x16x32_bf16 v[20:23], v[142:145], v[206:209], v[20:23]
	v_mfma_f32_16x16x32_bf16 v[16:19], v[150:153], v[206:209], v[16:19]
	v_mfma_f32_16x16x32_bf16 v[60:63], v[146:149], v[186:189], v[60:63]
	v_mfma_f32_16x16x32_bf16 v[56:59], v[162:165], v[186:189], v[56:59]
	v_mfma_f32_16x16x32_bf16 v[52:55], v[146:149], v[194:197], v[52:55]
	v_mfma_f32_16x16x32_bf16 v[48:51], v[162:165], v[194:197], v[48:51]
	v_mfma_f32_16x16x32_bf16 v[36:39], v[146:149], v[202:205], v[36:39]
	v_mfma_f32_16x16x32_bf16 v[32:35], v[162:165], v[202:205], v[32:35]
	v_mfma_f32_16x16x32_bf16 v[20:23], v[146:149], v[210:213], v[20:23]
	v_mfma_f32_16x16x32_bf16 v[16:19], v[162:165], v[210:213], v[16:19]
	s_setprio 0
	s_setprio 1
	v_mfma_f32_16x16x32_bf16 v[44:47], v[166:169], v[182:185], v[44:47]
	v_mfma_f32_16x16x32_bf16 v[40:43], v[174:177], v[182:185], v[40:43]
	v_mfma_f32_16x16x32_bf16 v[28:31], v[166:169], v[190:193], v[28:31]
	v_mfma_f32_16x16x32_bf16 v[24:27], v[174:177], v[190:193], v[24:27]
	v_mfma_f32_16x16x32_bf16 v[12:15], v[166:169], v[198:201], v[12:15]
	v_mfma_f32_16x16x32_bf16 v[8:11], v[174:177], v[198:201], v[8:11]
	v_mfma_f32_16x16x32_bf16 v[4:7], v[166:169], v[206:209], v[4:7]
	v_mfma_f32_16x16x32_bf16 v[0:3], v[174:177], v[206:209], v[0:3]
	v_mfma_f32_16x16x32_bf16 v[44:47], v[170:173], v[186:189], v[44:47]
	v_mfma_f32_16x16x32_bf16 v[40:43], v[178:181], v[186:189], v[40:43]
	v_mfma_f32_16x16x32_bf16 v[28:31], v[170:173], v[194:197], v[28:31]
	v_mfma_f32_16x16x32_bf16 v[24:27], v[178:181], v[194:197], v[24:27]
	v_mfma_f32_16x16x32_bf16 v[12:15], v[170:173], v[202:205], v[12:15]
	v_mfma_f32_16x16x32_bf16 v[8:11], v[178:181], v[202:205], v[8:11]
	v_mfma_f32_16x16x32_bf16 v[4:7], v[170:173], v[210:213], v[4:7]
	v_mfma_f32_16x16x32_bf16 v[0:3], v[178:181], v[210:213], v[0:3]
	s_setprio 0
	s_barrier
	s_movk_i32 s36, 0x100
	s_andn2_b64 vcc, exec, s[30:31]
	s_mov_b64 s[34:35], -1
	s_mov_b64 s[30:31], 0
	s_cbranch_vccz .LBB0_2280
	s_and_b64 vcc, exec, s[14:15]
	s_cbranch_vccz .LBB0_2283
	s_barrier

; #define PG8_STAGE(bufoff, gbase, voff) do { _Pragma("unroll") for (int _i = 0; _i < 2; ++_i) \
;         __builtin_amdgcn_global_load_lds((const unsigned*)((const char*)(gbase) + (voff)[_i]), (PG8_LAS unsigned*)(lds + (bufoff) + ldsw + _i * 8192), 16, 0, 0); } while (0)
; #define PG8_LDA(dst, b, h) do { _Pragma("unroll") for (int m = 0; m < 4; ++m) _Pragma("unroll") for (int k = 0; k < 2; ++k) dst[m][k] = *(const PG8_LAS bf16x8*)(lds + PG8_SA(b, h) + aoff + m * 2048 + k * 1024); } while (0)
; #define PG8_LDB(dst, b, h) do { _Pragma("unroll") for (int n = 0; n < 2; ++n) _Pragma("unroll") for (int k = 0; k < 2; ++k) dst[n][k] = *(const PG8_LAS bf16x8*)(lds + PG8_SB(b, h) + boff + n * 2048 + k * 1024); } while (0)
; #define PG8_WAIT_V(n) asm volatile("s_waitcnt vmcnt(" #n ")" ::: "memory")
; #define PG8_WAIT_L(n) asm volatile("s_waitcnt lgkmcnt(" #n ")" ::: "memory")
; #define PG8_BAR __builtin_amdgcn_s_barrier()
; #define PG8_SCHED __builtin_amdgcn_sched_barrier(0)
; template <class Epi, class Sched, bool ALIGN_EPI = false, bool SP2 = false>
; __device__ __forceinline__ void gemm_phase(PG8_LAS unsigned char* lds, const Gemm g, const Sched& S, const Epi& E, const int wid) {
;     ...
;         const bool has_next = S.next(ui + 1, nxt);
;         const char* nA = has_next ? (const char*)g.A + (size_t)nxt.pm * tstepA : cA; const char* nB = has_next ? (const char*)g.Bt + (size_t)nxt.pn * tstepB : cB;
;         for (int t = 0; t < nt; t += 2) {
;             const bool last = (t == nt - 2);
;             const char* a1 = cA + (size_t)(t + 1) * kstep;
;             const char* a2 = last ? nA : cA + (size_t)(t + 2) * kstep; const char* b2 = last ? nB : cB + (size_t)(t + 2) * kstep;
;             const char* a3 = a2 + kstep; const char* b3 = b2 + kstep;
;             if (last && has_next) S.a_ready(nxt);
;             if constexpr (SP2) {
;             PG8_LDB(B0, 0, 0); PG8_LDB(B1, 0, 1); PG8_SCHED; PG8_LDA(At, 0, 0); PG8_STAGE(PG8_SA(1, 1), a1 + hstepA, voffA);
;             PG8_WAIT_V(8); PG8_WAIT_L(0); PG8_BAR; PG8_MMA(0, 0, At, B0); PG8_MMA(0, 1, At, B1); PG8_BAR; PG8_SCHED;
;             PG8_LDA(At, 0, 1); PG8_STAGE(PG8_SB(0, 0), b2, voffB); PG8_STAGE(PG8_SB(0, 1), b2 + hstepB, voffB); PG8_STAGE(PG8_SA(0, 0), a2, voffA);
;             PG8_WAIT_V(8); PG8_WAIT_L(0); PG8_BAR; PG8_MMA(1, 0, At, B0); PG8_MMA(1, 1, At, B1); PG8_BAR; PG8_SCHED;
.LBB0_2725:
	ds_read_b128 v[128:131], v190
	ds_read_b128 v[132:135], v190 offset:1024
	ds_read_b128 v[136:139], v190 offset:2048
	ds_read_b128 v[140:143], v190 offset:3072
	ds_read_b128 v[144:147], v191
	ds_read_b128 v[148:151], v191 offset:1024
	ds_read_b128 v[172:175], v191 offset:2048
	ds_read_b128 v[176:179], v191 offset:3072
	s_add_u32 s34, s30, 0xfffc0080
	s_addc_u32 s35, s31, -1
	s_cmp_eq_u32 s60, 12
	s_cselect_b32 s37, s21, s35
	s_cselect_b32 s36, s27, s34
	s_cselect_b32 s35, s19, s59
	s_cselect_b32 s34, s29, s58
	s_add_i32 m0, s40, 0xc000
	ds_read_b128 v[180:183], v192
	ds_read_b128 v[184:187], v192 offset:1024
	ds_read_b128 v[194:197], v192 offset:2048
	ds_read_b128 v[198:201], v192 offset:3072
	ds_read_b128 v[202:205], v192 offset:4096
	ds_read_b128 v[206:209], v192 offset:5120
	ds_read_b128 v[210:213], v192 offset:6144
	ds_read_b128 v[214:217], v192 offset:7168
	global_load_lds_dwordx4 v164, s[30:31]
	s_add_i32 m0, s40, 0xe000
	s_nop 0
	global_load_lds_dwordx4 v166, s[30:31]
	s_waitcnt vmcnt(8) lgkmcnt(0)
	s_barrier
	s_setprio 1
	v_mfma_f32_16x16x32_bf16 v[124:127], v[128:131], v[180:183], v[124:127]
	v_mfma_f32_16x16x32_bf16 v[120:123], v[136:139], v[180:183], v[120:123]
	v_mfma_f32_16x16x32_bf16 v[108:111], v[128:131], v[194:197], v[108:111]
	v_mfma_f32_16x16x32_bf16 v[104:107], v[136:139], v[194:197], v[104:107]
	v_mfma_f32_16x16x32_bf16 v[92:95], v[128:131], v[202:205], v[92:95]
	v_mfma_f32_16x16x32_bf16 v[88:91], v[136:139], v[202:205], v[88:91]
	v_mfma_f32_16x16x32_bf16 v[76:79], v[128:131], v[210:213], v[76:79]
	v_mfma_f32_16x16x32_bf16 v[72:75], v[136:139], v[210:213], v[72:75]
	v_mfma_f32_16x16x32_bf16 v[124:127], v[132:135], v[184:187], v[124:127]
	v_mfma_f32_16x16x32_bf16 v[120:123], v[140:143], v[184:187], v[120:123]
	v_mfma_f32_16x16x32_bf16 v[108:111], v[132:135], v[198:201], v[108:111]
	v_mfma_f32_16x16x32_bf16 v[104:107], v[140:143], v[198:201], v[104:107]
	v_mfma_f32_16x16x32_bf16 v[92:95], v[132:135], v[206:209], v[92:95]
	v_mfma_f32_16x16x32_bf16 v[88:91], v[140:143], v[206:209], v[88:91]
	v_mfma_f32_16x16x32_bf16 v[76:79], v[132:135], v[214:217], v[76:79]
	v_mfma_f32_16x16x32_bf16 v[72:75], v[140:143], v[214:217], v[72:75]
	s_setprio 0
	s_setprio 1
	v_mfma_f32_16x16x32_bf16 v[116:119], v[144:147], v[180:183], v[116:119]
	v_mfma_f32_16x16x32_bf16 v[112:115], v[172:175], v[180:183], v[112:115]
	v_mfma_f32_16x16x32_bf16 v[100:103], v[144:147], v[194:197], v[100:103]
	v_mfma_f32_16x16x32_bf16 v[96:99], v[172:175], v[194:197], v[96:99]
	v_mfma_f32_16x16x32_bf16 v[84:87], v[144:147], v[202:205], v[84:87]
	v_mfma_f32_16x16x32_bf16 v[80:83], v[172:175], v[202:205], v[80:83]
	v_mfma_f32_16x16x32_bf16 v[68:71], v[144:147], v[210:213], v[68:71]
	v_mfma_f32_16x16x32_bf16 v[64:67], v[172:175], v[210:213], v[64:67]
	v_mfma_f32_16x16x32_bf16 v[116:119], v[148:151], v[184:187], v[116:119]
	v_mfma_f32_16x16x32_bf16 v[112:115], v[176:179], v[184:187], v[112:115]
	v_mfma_f32_16x16x32_bf16 v[100:103], v[148:151], v[198:201], v[100:103]
	v_mfma_f32_16x16x32_bf16 v[96:99], v[176:179], v[198:201], v[96:99]
	v_mfma_f32_16x16x32_bf16 v[84:87], v[148:151], v[206:209], v[84:87]
	v_mfma_f32_16x16x32_bf16 v[80:83], v[176:179], v[206:209], v[80:83]
	v_mfma_f32_16x16x32_bf16 v[68:71], v[148:151], v[214:217], v[68:71]
	v_mfma_f32_16x16x32_bf16 v[64:67], v[176:179], v[214:217], v[64:67]
	s_setprio 0
	s_barrier
	s_add_i32 s61, s49, s39
	s_add_u32 s98, s34, 0x80
	s_addc_u32 s99, s35, 0
	s_mov_b32 m0, s61
	ds_read_b128 v[180:183], v192 offset:16384
	ds_read_b128 v[184:187], v192 offset:17408
	ds_read_b128 v[194:197], v192 offset:18432
	ds_read_b128 v[198:201], v192 offset:19456
	ds_read_b128 v[202:205], v192 offset:20480
	ds_read_b128 v[206:209], v192 offset:21504
	ds_read_b128 v[210:213], v192 offset:22528
	ds_read_b128 v[214:217], v192 offset:23552
	global_load_lds_dwordx4 v154, s[34:35]
	s_add_i32 m0, s61, 0x2000
	s_add_u32 s62, s34, 0x40000
	s_addc_u32 s63, s35, 0
	s_add_i32 s61, s56, s39
	global_load_lds_dwordx4 v158, s[34:35]
	s_mov_b32 m0, s61
	s_add_u32 s100, s36, 0x80
	s_addc_u32 s101, s37, 0
	global_load_lds_dwordx4 v154, s[62:63]
	s_add_i32 m0, s61, 0x2000
	s_nop 0
	global_load_lds_dwordx4 v158, s[62:63]
	s_mov_b32 m0, s40
	s_nop 0
	global_load_lds_dwordx4 v152, s[36:37]
	s_mov_b32 m0, s41
	s_nop 0
	global_load_lds_dwordx4 v156, s[36:37]
	s_waitcnt vmcnt(8) lgkmcnt(0)
	s_barrier
	s_setprio 1
	v_mfma_f32_16x16x32_bf16 v[60:63], v[128:131], v[180:183], v[60:63]
	v_mfma_f32_16x16x32_bf16 v[56:59], v[136:139], v[180:183], v[56:59]
	v_mfma_f32_16x16x32_bf16 v[44:47], v[128:131], v[194:197], v[44:47]
	v_mfma_f32_16x16x32_bf16 v[40:43], v[136:139], v[194:197], v[40:43]
	v_mfma_f32_16x16x32_bf16 v[28:31], v[128:131], v[202:205], v[28:31]
	v_mfma_f32_16x16x32_bf16 v[24:27], v[136:139], v[202:205], v[24:27]
	v_mfma_f32_16x16x32_bf16 v[12:15], v[128:131], v[210:213], v[12:15]
	v_mfma_f32_16x16x32_bf16 v[8:11], v[136:139], v[210:213], v[8:11]
	v_mfma_f32_16x16x32_bf16 v[60:63], v[132:135], v[184:187], v[60:63]
	v_mfma_f32_16x16x32_bf16 v[56:59], v[140:143], v[184:187], v[56:59]
	v_mfma_f32_16x16x32_bf16 v[44:47], v[132:135], v[198:201], v[44:47]
	v_mfma_f32_16x16x32_bf16 v[40:43], v[140:143], v[198:201], v[40:43]
	v_mfma_f32_16x16x32_bf16 v[28:31], v[132:135], v[206:209], v[28:31]
	v_mfma_f32_16x16x32_bf16 v[24:27], v[140:143], v[206:209], v[24:27]
	v_mfma_f32_16x16x32_bf16 v[12:15], v[132:135], v[214:217], v[12:15]
	v_mfma_f32_16x16x32_bf16 v[8:11], v[140:143], v[214:217], v[8:11]
	s_setprio 0
	s_setprio 1
	v_mfma_f32_16x16x32_bf16 v[52:55], v[144:147], v[180:183], v[52:55]
	v_mfma_f32_16x16x32_bf16 v[48:51], v[172:175], v[180:183], v[48:51]
	v_mfma_f32_16x16x32_bf16 v[36:39], v[144:147], v[194:197], v[36:39]
	v_mfma_f32_16x16x32_bf16 v[32:35], v[172:175], v[194:197], v[32:35]
	v_mfma_f32_16x16x32_bf16 v[20:23], v[144:147], v[202:205], v[20:23]
	v_mfma_f32_16x16x32_bf16 v[16:19], v[172:175], v[202:205], v[16:19]
	v_mfma_f32_16x16x32_bf16 v[4:7], v[144:147], v[210:213], v[4:7]
	v_mfma_f32_16x16x32_bf16 v[0:3], v[172:175], v[210:213], v[0:3]
	v_mfma_f32_16x16x32_bf16 v[52:55], v[148:151], v[184:187], v[52:55]
	v_mfma_f32_16x16x32_bf16 v[48:51], v[176:179], v[184:187], v[48:51]
	v_mfma_f32_16x16x32_bf16 v[36:39], v[148:151], v[198:201], v[36:39]
	v_mfma_f32_16x16x32_bf16 v[32:35], v[176:179], v[198:201], v[32:35]
	v_mfma_f32_16x16x32_bf16 v[20:23], v[148:151], v[206:209], v[20:23]
	v_mfma_f32_16x16x32_bf16 v[16:19], v[176:179], v[206:209], v[16:19]
	v_mfma_f32_16x16x32_bf16 v[4:7], v[148:151], v[214:217], v[4:7]
	v_mfma_f32_16x16x32_bf16 v[0:3], v[176:179], v[214:217], v[0:3]
	s_setprio 0
	s_barrier
; #define PG8_STAGE(bufoff, gbase, voff) do { _Pragma("unroll") for (int _i = 0; _i < 2; ++_i) \
;         __builtin_amdgcn_global_load_lds((const unsigned*)((const char*)(gbase) + (voff)[_i]), (PG8_LAS unsigned*)(lds + (bufoff) + ldsw + _i * 8192), 16, 0, 0); } while (0)
; #define PG8_LDA(dst, b, h) do { _Pragma("unroll") for (int m = 0; m < 4; ++m) _Pragma("unroll") for (int k = 0; k < 2; ++k) dst[m][k] = *(const PG8_LAS bf16x8*)(lds + PG8_SA(b, h) + aoff + m * 2048 + k * 1024); } while (0)
; #define PG8_WAIT_V(n) asm volatile("s_waitcnt vmcnt(" #n ")" ::: "memory")
; #define PG8_WAIT_L(n) asm volatile("s_waitcnt lgkmcnt(" #n ")" ::: "memory")
; #define PG8_BAR __builtin_amdgcn_s_barrier()
; template <class Epi, class Sched, bool ALIGN_EPI = false, bool SP2 = false>
; __device__ __forceinline__ void gemm_phase(PG8_LAS unsigned char* lds, const Gemm g, const Sched& S, const Epi& E, const int wid) {
;     ...
;         for (int t = 0; t < nt; t += 2) {
;             const bool last = (t == nt - 2);
;             const char* a1 = cA + (size_t)(t + 1) * kstep;
;             const char* a2 = last ? nA : cA + (size_t)(t + 2) * kstep; const char* b2 = last ? nB : cB + (size_t)(t + 2) * kstep;
;             const char* a3 = a2 + kstep; const char* b3 = b2 + kstep;
;             if (last && has_next) S.a_ready(nxt);
;             if constexpr (SP2) {
;             PG8_LDB(B0, 0, 0); PG8_LDB(B1, 0, 1); PG8_SCHED; PG8_LDA(At, 0, 0); PG8_STAGE(PG8_SA(1, 1), a1 + hstepA, voffA);
;             PG8_WAIT_V(8); PG8_WAIT_L(0); PG8_BAR; PG8_MMA(0, 0, At, B0); PG8_MMA(0, 1, At, B1); PG8_BAR; PG8_SCHED;
;             PG8_LDA(At, 0, 1); PG8_STAGE(PG8_SB(0, 0), b2, voffB); PG8_STAGE(PG8_SB(0, 1), b2 + hstepB, voffB); PG8_STAGE(PG8_SA(0, 0), a2, voffA);
;             PG8_WAIT_V(8); PG8_WAIT_L(0); PG8_BAR; PG8_MMA(1, 0, At, B0); PG8_MMA(1, 1, At, B1); PG8_BAR; PG8_SCHED;
;             PG8_LDB(B0, 1, 0); PG8_LDB(B1, 1, 1); PG8_SCHED; PG8_LDA(At, 1, 0); PG8_STAGE(PG8_SA(0, 1), a2 + hstepA, voffA);
;             PG8_WAIT_V(8); PG8_WAIT_L(0); PG8_BAR; PG8_MMA(0, 0, At, B0); PG8_MMA(0, 1, At, B1); PG8_BAR; PG8_SCHED;
;             PG8_LDA(At, 1, 1); PG8_STAGE(PG8_SB(1, 0), b3, voffB); PG8_STAGE(PG8_SB(1, 1), b3 + hstepB, voffB); PG8_STAGE(PG8_SA(1, 0), a3, voffA);
;             PG8_WAIT_V(8); PG8_WAIT_L(0); PG8_BAR; PG8_MMA(1, 0, At, B0); PG8_MMA(1, 1, At, B1); PG8_BAR; PG8_SCHED;
	s_add_i32 s61, 0, 0x18000
	s_add_i32 s62, 0, 0x1c000
	v_add_u32_e32 v140, s61, v189
	v_add_u32_e32 v176, s62, v189
	ds_read_b128 v[128:131], v140
	ds_read_b128 v[132:135], v140 offset:1024
	ds_read_b128 v[136:139], v140 offset:2048
	ds_read_b128 v[140:143], v140 offset:3072
	ds_read_b128 v[144:147], v176
	ds_read_b128 v[148:151], v176 offset:1024
	ds_read_b128 v[172:175], v176 offset:2048
	ds_read_b128 v[176:179], v176 offset:3072
	s_add_u32 s36, s36, 0x40000
	s_addc_u32 s37, s37, 0
	s_mov_b32 m0, s42
	ds_read_b128 v[180:183], v192 offset:32768
	ds_read_b128 v[184:187], v192 offset:33792
	ds_read_b128 v[194:197], v192 offset:34816
	ds_read_b128 v[198:201], v192 offset:35840
	ds_read_b128 v[202:205], v192 offset:36864
	ds_read_b128 v[206:209], v192 offset:37888
	ds_read_b128 v[210:213], v192 offset:38912
	ds_read_b128 v[214:217], v192 offset:39936
	global_load_lds_dwordx4 v152, s[36:37]
	s_mov_b32 m0, s43
	s_nop 0
	global_load_lds_dwordx4 v156, s[36:37]
	s_waitcnt vmcnt(8) lgkmcnt(0)
	s_barrier
	s_setprio 1
	v_mfma_f32_16x16x32_bf16 v[124:127], v[128:131], v[180:183], v[124:127]
	v_mfma_f32_16x16x32_bf16 v[120:123], v[136:139], v[180:183], v[120:123]
	v_mfma_f32_16x16x32_bf16 v[108:111], v[128:131], v[194:197], v[108:111]
	v_mfma_f32_16x16x32_bf16 v[104:107], v[136:139], v[194:197], v[104:107]
	v_mfma_f32_16x16x32_bf16 v[92:95], v[128:131], v[202:205], v[92:95]
	v_mfma_f32_16x16x32_bf16 v[88:91], v[136:139], v[202:205], v[88:91]
	v_mfma_f32_16x16x32_bf16 v[76:79], v[128:131], v[210:213], v[76:79]
	v_mfma_f32_16x16x32_bf16 v[72:75], v[136:139], v[210:213], v[72:75]
	v_mfma_f32_16x16x32_bf16 v[124:127], v[132:135], v[184:187], v[124:127]
	v_mfma_f32_16x16x32_bf16 v[120:123], v[140:143], v[184:187], v[120:123]
	v_mfma_f32_16x16x32_bf16 v[108:111], v[132:135], v[198:201], v[108:111]
	v_mfma_f32_16x16x32_bf16 v[104:107], v[140:143], v[198:201], v[104:107]
	v_mfma_f32_16x16x32_bf16 v[92:95], v[132:135], v[206:209], v[92:95]
	v_mfma_f32_16x16x32_bf16 v[88:91], v[140:143], v[206:209], v[88:91]
	v_mfma_f32_16x16x32_bf16 v[76:79], v[132:135], v[214:217], v[76:79]
	v_mfma_f32_16x16x32_bf16 v[72:75], v[140:143], v[214:217], v[72:75]
	s_setprio 0
	s_setprio 1
	v_mfma_f32_16x16x32_bf16 v[116:119], v[144:147], v[180:183], v[116:119]
	v_mfma_f32_16x16x32_bf16 v[112:115], v[172:175], v[180:183], v[112:115]
	v_mfma_f32_16x16x32_bf16 v[100:103], v[144:147], v[194:197], v[100:103]
	v_mfma_f32_16x16x32_bf16 v[96:99], v[172:175], v[194:197], v[96:99]
	v_mfma_f32_16x16x32_bf16 v[84:87], v[144:147], v[202:205], v[84:87]
	v_mfma_f32_16x16x32_bf16 v[80:83], v[172:175], v[202:205], v[80:83]
	v_mfma_f32_16x16x32_bf16 v[68:71], v[144:147], v[210:213], v[68:71]
	v_mfma_f32_16x16x32_bf16 v[64:67], v[172:175], v[210:213], v[64:67]
	v_mfma_f32_16x16x32_bf16 v[116:119], v[148:151], v[184:187], v[116:119]
	v_mfma_f32_16x16x32_bf16 v[112:115], v[176:179], v[184:187], v[112:115]
	v_mfma_f32_16x16x32_bf16 v[100:103], v[148:151], v[198:201], v[100:103]
	v_mfma_f32_16x16x32_bf16 v[96:99], v[176:179], v[198:201], v[96:99]
	v_mfma_f32_16x16x32_bf16 v[84:87], v[148:151], v[206:209], v[84:87]
	v_mfma_f32_16x16x32_bf16 v[80:83], v[176:179], v[206:209], v[80:83]
	v_mfma_f32_16x16x32_bf16 v[68:71], v[148:151], v[214:217], v[68:71]
	v_mfma_f32_16x16x32_bf16 v[64:67], v[176:179], v[214:217], v[64:67]
	s_setprio 0
	s_barrier
	s_add_i32 s36, s61, s39
	s_mov_b32 m0, s36
	ds_read_b128 v[180:183], v192 offset:49152
	ds_read_b128 v[184:187], v192 offset:50176
	ds_read_b128 v[194:197], v192 offset:51200
	ds_read_b128 v[198:201], v192 offset:52224
	ds_read_b128 v[202:205], v192 offset:53248
	ds_read_b128 v[206:209], v192 offset:54272
	ds_read_b128 v[210:213], v192 offset:55296
	ds_read_b128 v[214:217], v192 offset:56320
	global_load_lds_dwordx4 v154, s[98:99]
	s_add_i32 m0, s36, 0x2000
	s_add_u32 s34, s34, 0x40080
	s_addc_u32 s35, s35, 0
	s_add_i32 s36, s62, s39
	global_load_lds_dwordx4 v158, s[98:99]
	s_mov_b32 m0, s36
	s_nop 0
	global_load_lds_dwordx4 v154, s[34:35]
	s_add_i32 m0, s36, 0x2000
	s_nop 0
	global_load_lds_dwordx4 v158, s[34:35]
	s_mov_b32 m0, s45
	s_nop 0
	global_load_lds_dwordx4 v152, s[100:101]
	s_mov_b32 m0, s46
	s_nop 0
	global_load_lds_dwordx4 v156, s[100:101]
	s_waitcnt vmcnt(8) lgkmcnt(0)
	s_barrier
	s_setprio 1
	v_mfma_f32_16x16x32_bf16 v[60:63], v[128:131], v[180:183], v[60:63]
	v_mfma_f32_16x16x32_bf16 v[56:59], v[136:139], v[180:183], v[56:59]
	v_mfma_f32_16x16x32_bf16 v[44:47], v[128:131], v[194:197], v[44:47]
	v_mfma_f32_16x16x32_bf16 v[40:43], v[136:139], v[194:197], v[40:43]
	v_mfma_f32_16x16x32_bf16 v[28:31], v[128:131], v[202:205], v[28:31]
	v_mfma_f32_16x16x32_bf16 v[24:27], v[136:139], v[202:205], v[24:27]
	v_mfma_f32_16x16x32_bf16 v[12:15], v[128:131], v[210:213], v[12:15]
	v_mfma_f32_16x16x32_bf16 v[8:11], v[136:139], v[210:213], v[8:11]
	v_mfma_f32_16x16x32_bf16 v[60:63], v[132:135], v[184:187], v[60:63]
	v_mfma_f32_16x16x32_bf16 v[56:59], v[140:143], v[184:187], v[56:59]
	v_mfma_f32_16x16x32_bf16 v[44:47], v[132:135], v[198:201], v[44:47]
	v_mfma_f32_16x16x32_bf16 v[40:43], v[140:143], v[198:201], v[40:43]
	v_mfma_f32_16x16x32_bf16 v[28:31], v[132:135], v[206:209], v[28:31]
	v_mfma_f32_16x16x32_bf16 v[24:27], v[140:143], v[206:209], v[24:27]
	v_mfma_f32_16x16x32_bf16 v[12:15], v[132:135], v[214:217], v[12:15]
	v_mfma_f32_16x16x32_bf16 v[8:11], v[140:143], v[214:217], v[8:11]
	s_setprio 0
	s_setprio 1
	v_mfma_f32_16x16x32_bf16 v[52:55], v[144:147], v[180:183], v[52:55]
	v_mfma_f32_16x16x32_bf16 v[48:51], v[172:175], v[180:183], v[48:51]
	v_mfma_f32_16x16x32_bf16 v[36:39], v[144:147], v[194:197], v[36:39]
	v_mfma_f32_16x16x32_bf16 v[32:35], v[172:175], v[194:197], v[32:35]
	v_mfma_f32_16x16x32_bf16 v[20:23], v[144:147], v[202:205], v[20:23]
	v_mfma_f32_16x16x32_bf16 v[16:19], v[172:175], v[202:205], v[16:19]
	v_mfma_f32_16x16x32_bf16 v[4:7], v[144:147], v[210:213], v[4:7]
	v_mfma_f32_16x16x32_bf16 v[0:3], v[172:175], v[210:213], v[0:3]
	v_mfma_f32_16x16x32_bf16 v[52:55], v[148:151], v[184:187], v[52:55]
	v_mfma_f32_16x16x32_bf16 v[48:51], v[176:179], v[184:187], v[48:51]
	v_mfma_f32_16x16x32_bf16 v[36:39], v[148:151], v[198:201], v[36:39]
	v_mfma_f32_16x16x32_bf16 v[32:35], v[176:179], v[198:201], v[32:35]
	v_mfma_f32_16x16x32_bf16 v[20:23], v[148:151], v[206:209], v[20:23]
	v_mfma_f32_16x16x32_bf16 v[16:19], v[176:179], v[206:209], v[16:19]
	v_mfma_f32_16x16x32_bf16 v[4:7], v[148:151], v[214:217], v[4:7]
	v_mfma_f32_16x16x32_bf16 v[0:3], v[176:179], v[214:217], v[0:3]
	s_setprio 0
	s_barrier
	s_add_i32 s60, s60, 2
	s_add_u32 s30, s30, 0x100
	s_addc_u32 s31, s31, 0
	s_add_u32 s58, s58, 0x100
	s_addc_u32 s59, s59, 0
	s_cmp_gt_u32 s60, 13
	s_cbranch_scc0 .LBB0_2725
	s_and_b64 vcc, exec, s[16:17]
	s_cbranch_vccz .LBB0_2728
	s_barrier

; #define PG8_STAGE(bufoff, gbase, voff) do { _Pragma("unroll") for (int _i = 0; _i < 2; ++_i) \
;         __builtin_amdgcn_global_load_lds((const unsigned*)((const char*)(gbase) + (voff)[_i]), (PG8_LAS unsigned*)(lds + (bufoff) + ldsw + _i * 8192), 16, 0, 0); } while (0)
; #define PG8_LDA(dst, b, h) do { _Pragma("unroll") for (int m = 0; m < 4; ++m) _Pragma("unroll") for (int k = 0; k < 2; ++k) dst[m][k] = *(const PG8_LAS bf16x8*)(lds + PG8_SA(b, h) + aoff + m * 2048 + k * 1024); } while (0)
; #define PG8_LDB(dst, b, h) do { _Pragma("unroll") for (int n = 0; n < 2; ++n) _Pragma("unroll") for (int k = 0; k < 2; ++k) dst[n][k] = *(const PG8_LAS bf16x8*)(lds + PG8_SB(b, h) + boff + n * 2048 + k * 1024); } while (0)
; #define PG8_WAIT_V(n) asm volatile("s_waitcnt vmcnt(" #n ")" ::: "memory")
; #define PG8_WAIT_L(n) asm volatile("s_waitcnt lgkmcnt(" #n ")" ::: "memory")
; #define PG8_BAR __builtin_amdgcn_s_barrier()
; #define PG8_SCHED __builtin_amdgcn_sched_barrier(0)
; template <class Epi, class Sched, bool ALIGN_EPI = false, bool SP2 = false>
; __device__ __forceinline__ void gemm_phase(PG8_LAS unsigned char* lds, const Gemm g, const Sched& S, const Epi& E, const int wid) {
;     ...
;         const bool has_next = S.next(ui + 1, nxt);
;         const char* nA = has_next ? (const char*)g.A + (size_t)nxt.pm * tstepA : cA; const char* nB = has_next ? (const char*)g.Bt + (size_t)nxt.pn * tstepB : cB;
;         for (int t = 0; t < nt; t += 2) {
;             const bool last = (t == nt - 2);
;             const char* a1 = cA + (size_t)(t + 1) * kstep;
;             const char* a2 = last ? nA : cA + (size_t)(t + 2) * kstep; const char* b2 = last ? nB : cB + (size_t)(t + 2) * kstep;
;             const char* a3 = a2 + kstep; const char* b3 = b2 + kstep;
;             if (last && has_next) S.a_ready(nxt);
;             if constexpr (SP2) {
;             PG8_LDB(B0, 0, 0); PG8_LDB(B1, 0, 1); PG8_SCHED; PG8_LDA(At, 0, 0); PG8_STAGE(PG8_SA(1, 1), a1 + hstepA, voffA);
;             PG8_WAIT_V(8); PG8_WAIT_L(0); PG8_BAR; PG8_MMA(0, 0, At, B0); PG8_MMA(0, 1, At, B1); PG8_BAR; PG8_SCHED;
;             PG8_LDA(At, 0, 1); PG8_STAGE(PG8_SB(0, 0), b2, voffB); PG8_STAGE(PG8_SB(0, 1), b2 + hstepB, voffB); PG8_STAGE(PG8_SA(0, 0), a2, voffA);
;             PG8_WAIT_V(8); PG8_WAIT_L(0); PG8_BAR; PG8_MMA(1, 0, At, B0); PG8_MMA(1, 1, At, B1); PG8_BAR; PG8_SCHED;
.LBB0_2812:
	ds_read_b128 v[148:151], v166
	ds_read_b128 v[152:155], v166 offset:1024
	ds_read_b128 v[156:159], v166 offset:2048
	ds_read_b128 v[160:163], v166 offset:3072
	ds_read_b128 v[172:175], v167
	ds_read_b128 v[176:179], v167 offset:1024
	ds_read_b128 v[180:183], v167 offset:2048
	ds_read_b128 v[184:187], v167 offset:3072
	s_add_u32 s26, s24, 0xfffc0080
	s_addc_u32 s27, s25, -1
	s_cmp_eq_u32 s57, 12
	s_cselect_b32 s29, s17, s27
	s_cselect_b32 s28, s47, s26
	s_cselect_b32 s27, s15, s56
	s_cselect_b32 s26, s48, s49
	s_add_i32 m0, s36, 0xc000
	ds_read_b128 v[188:191], v168
	ds_read_b128 v[192:195], v168 offset:1024
	ds_read_b128 v[196:199], v168 offset:2048
	ds_read_b128 v[200:203], v168 offset:3072
	ds_read_b128 v[204:207], v168 offset:4096
	ds_read_b128 v[208:211], v168 offset:5120
	ds_read_b128 v[212:215], v168 offset:6144
	ds_read_b128 v[216:219], v168 offset:7168
	global_load_lds_dwordx4 v140, s[24:25]
	s_add_i32 m0, s36, 0xe000
	s_nop 0
	global_load_lds_dwordx4 v142, s[24:25]
	s_waitcnt vmcnt(8) lgkmcnt(0)
	s_barrier
	s_setprio 1
	v_mfma_f32_16x16x32_bf16 v[124:127], v[148:151], v[188:191], v[124:127]
	v_mfma_f32_16x16x32_bf16 v[116:119], v[156:159], v[188:191], v[116:119]
	v_mfma_f32_16x16x32_bf16 v[108:111], v[148:151], v[196:199], v[108:111]
	v_mfma_f32_16x16x32_bf16 v[100:103], v[156:159], v[196:199], v[100:103]
	v_mfma_f32_16x16x32_bf16 v[92:95], v[148:151], v[204:207], v[92:95]
	v_mfma_f32_16x16x32_bf16 v[84:87], v[156:159], v[204:207], v[84:87]
	v_mfma_f32_16x16x32_bf16 v[76:79], v[148:151], v[212:215], v[76:79]
	v_mfma_f32_16x16x32_bf16 v[68:71], v[156:159], v[212:215], v[68:71]
	v_mfma_f32_16x16x32_bf16 v[124:127], v[152:155], v[192:195], v[124:127]
	v_mfma_f32_16x16x32_bf16 v[116:119], v[160:163], v[192:195], v[116:119]
	v_mfma_f32_16x16x32_bf16 v[108:111], v[152:155], v[200:203], v[108:111]
	v_mfma_f32_16x16x32_bf16 v[100:103], v[160:163], v[200:203], v[100:103]
	v_mfma_f32_16x16x32_bf16 v[92:95], v[152:155], v[208:211], v[92:95]
	v_mfma_f32_16x16x32_bf16 v[84:87], v[160:163], v[208:211], v[84:87]
	v_mfma_f32_16x16x32_bf16 v[76:79], v[152:155], v[216:219], v[76:79]
	v_mfma_f32_16x16x32_bf16 v[68:71], v[160:163], v[216:219], v[68:71]
	s_setprio 0
	s_setprio 1
	v_mfma_f32_16x16x32_bf16 v[120:123], v[172:175], v[188:191], v[120:123]
	v_mfma_f32_16x16x32_bf16 v[112:115], v[180:183], v[188:191], v[112:115]
	v_mfma_f32_16x16x32_bf16 v[104:107], v[172:175], v[196:199], v[104:107]
	v_mfma_f32_16x16x32_bf16 v[96:99], v[180:183], v[196:199], v[96:99]
	v_mfma_f32_16x16x32_bf16 v[88:91], v[172:175], v[204:207], v[88:91]
	v_mfma_f32_16x16x32_bf16 v[80:83], v[180:183], v[204:207], v[80:83]
	v_mfma_f32_16x16x32_bf16 v[72:75], v[172:175], v[212:215], v[72:75]
	v_mfma_f32_16x16x32_bf16 v[64:67], v[180:183], v[212:215], v[64:67]
	v_mfma_f32_16x16x32_bf16 v[120:123], v[176:179], v[192:195], v[120:123]
	v_mfma_f32_16x16x32_bf16 v[112:115], v[184:187], v[192:195], v[112:115]
	v_mfma_f32_16x16x32_bf16 v[104:107], v[176:179], v[200:203], v[104:107]
	v_mfma_f32_16x16x32_bf16 v[96:99], v[184:187], v[200:203], v[96:99]
	v_mfma_f32_16x16x32_bf16 v[88:91], v[176:179], v[208:211], v[88:91]
	v_mfma_f32_16x16x32_bf16 v[80:83], v[184:187], v[208:211], v[80:83]
	v_mfma_f32_16x16x32_bf16 v[72:75], v[176:179], v[216:219], v[72:75]
	v_mfma_f32_16x16x32_bf16 v[64:67], v[184:187], v[216:219], v[64:67]
	s_setprio 0
	s_barrier
	s_add_i32 s58, s43, s33
	s_add_u32 s98, s26, 0x80
	s_addc_u32 s99, s27, 0
	s_mov_b32 m0, s58
	ds_read_b128 v[188:191], v168 offset:16384
	ds_read_b128 v[192:195], v168 offset:17408
	ds_read_b128 v[196:199], v168 offset:18432
	ds_read_b128 v[200:203], v168 offset:19456
	ds_read_b128 v[204:207], v168 offset:20480
	ds_read_b128 v[208:211], v168 offset:21504
	ds_read_b128 v[212:215], v168 offset:22528
	ds_read_b128 v[216:219], v168 offset:23552
	global_load_lds_dwordx4 v132, s[26:27]
	s_add_i32 m0, s58, 0x2000
	s_add_u32 s58, s26, 0x40000
	s_addc_u32 s59, s27, 0
	s_add_i32 s60, s44, s33
	global_load_lds_dwordx4 v128, s[26:27]
	s_mov_b32 m0, s60
	s_add_u32 s100, s28, 0x80
	s_addc_u32 s101, s29, 0
	global_load_lds_dwordx4 v132, s[58:59]
	s_add_i32 m0, s60, 0x2000
	s_nop 0
	global_load_lds_dwordx4 v128, s[58:59]
	s_mov_b32 m0, s36
	s_nop 0
	global_load_lds_dwordx4 v134, s[28:29]
	s_mov_b32 m0, s37
	s_nop 0
	global_load_lds_dwordx4 v130, s[28:29]
	s_waitcnt vmcnt(8) lgkmcnt(0)
	s_barrier
	s_setprio 1
	v_mfma_f32_16x16x32_bf16 v[60:63], v[148:151], v[188:191], v[60:63]
	v_mfma_f32_16x16x32_bf16 v[52:55], v[156:159], v[188:191], v[52:55]
	v_mfma_f32_16x16x32_bf16 v[44:47], v[148:151], v[196:199], v[44:47]
	v_mfma_f32_16x16x32_bf16 v[36:39], v[156:159], v[196:199], v[36:39]
	v_mfma_f32_16x16x32_bf16 v[28:31], v[148:151], v[204:207], v[28:31]
	v_mfma_f32_16x16x32_bf16 v[20:23], v[156:159], v[204:207], v[20:23]
	v_mfma_f32_16x16x32_bf16 v[12:15], v[148:151], v[212:215], v[12:15]
	v_mfma_f32_16x16x32_bf16 v[4:7], v[156:159], v[212:215], v[4:7]
	v_mfma_f32_16x16x32_bf16 v[60:63], v[152:155], v[192:195], v[60:63]
	v_mfma_f32_16x16x32_bf16 v[52:55], v[160:163], v[192:195], v[52:55]
	v_mfma_f32_16x16x32_bf16 v[44:47], v[152:155], v[200:203], v[44:47]
	v_mfma_f32_16x16x32_bf16 v[36:39], v[160:163], v[200:203], v[36:39]
	v_mfma_f32_16x16x32_bf16 v[28:31], v[152:155], v[208:211], v[28:31]
	v_mfma_f32_16x16x32_bf16 v[20:23], v[160:163], v[208:211], v[20:23]
	v_mfma_f32_16x16x32_bf16 v[12:15], v[152:155], v[216:219], v[12:15]
	v_mfma_f32_16x16x32_bf16 v[4:7], v[160:163], v[216:219], v[4:7]
	s_setprio 0
	s_setprio 1
	v_mfma_f32_16x16x32_bf16 v[56:59], v[172:175], v[188:191], v[56:59]
	v_mfma_f32_16x16x32_bf16 v[48:51], v[180:183], v[188:191], v[48:51]
	v_mfma_f32_16x16x32_bf16 v[40:43], v[172:175], v[196:199], v[40:43]
	v_mfma_f32_16x16x32_bf16 v[32:35], v[180:183], v[196:199], v[32:35]
	v_mfma_f32_16x16x32_bf16 v[24:27], v[172:175], v[204:207], v[24:27]
	v_mfma_f32_16x16x32_bf16 v[16:19], v[180:183], v[204:207], v[16:19]
	v_mfma_f32_16x16x32_bf16 v[8:11], v[172:175], v[212:215], v[8:11]
	v_mfma_f32_16x16x32_bf16 v[0:3], v[180:183], v[212:215], v[0:3]
	v_mfma_f32_16x16x32_bf16 v[56:59], v[176:179], v[192:195], v[56:59]
	v_mfma_f32_16x16x32_bf16 v[48:51], v[184:187], v[192:195], v[48:51]
	v_mfma_f32_16x16x32_bf16 v[40:43], v[176:179], v[200:203], v[40:43]
	v_mfma_f32_16x16x32_bf16 v[32:35], v[184:187], v[200:203], v[32:35]
	v_mfma_f32_16x16x32_bf16 v[24:27], v[176:179], v[208:211], v[24:27]
	v_mfma_f32_16x16x32_bf16 v[16:19], v[184:187], v[208:211], v[16:19]
	v_mfma_f32_16x16x32_bf16 v[8:11], v[176:179], v[216:219], v[8:11]
	v_mfma_f32_16x16x32_bf16 v[0:3], v[184:187], v[216:219], v[0:3]
	s_setprio 0
	s_barrier
; #define PG8_STAGE(bufoff, gbase, voff) do { _Pragma("unroll") for (int _i = 0; _i < 2; ++_i) \
;         __builtin_amdgcn_global_load_lds((const unsigned*)((const char*)(gbase) + (voff)[_i]), (PG8_LAS unsigned*)(lds + (bufoff) + ldsw + _i * 8192), 16, 0, 0); } while (0)
; #define PG8_LDA(dst, b, h) do { _Pragma("unroll") for (int m = 0; m < 4; ++m) _Pragma("unroll") for (int k = 0; k < 2; ++k) dst[m][k] = *(const PG8_LAS bf16x8*)(lds + PG8_SA(b, h) + aoff + m * 2048 + k * 1024); } while (0)
; #define PG8_WAIT_V(n) asm volatile("s_waitcnt vmcnt(" #n ")" ::: "memory")
; #define PG8_WAIT_L(n) asm volatile("s_waitcnt lgkmcnt(" #n ")" ::: "memory")
; #define PG8_BAR __builtin_amdgcn_s_barrier()
; template <class Epi, class Sched, bool ALIGN_EPI = false, bool SP2 = false>
; __device__ __forceinline__ void gemm_phase(PG8_LAS unsigned char* lds, const Gemm g, const Sched& S, const Epi& E, const int wid) {
;     ...
;         for (int t = 0; t < nt; t += 2) {
;             const bool last = (t == nt - 2);
;             const char* a1 = cA + (size_t)(t + 1) * kstep;
;             const char* a2 = last ? nA : cA + (size_t)(t + 2) * kstep; const char* b2 = last ? nB : cB + (size_t)(t + 2) * kstep;
;             const char* a3 = a2 + kstep; const char* b3 = b2 + kstep;
;             if (last && has_next) S.a_ready(nxt);
;             if constexpr (SP2) {
;             PG8_LDB(B0, 0, 0); PG8_LDB(B1, 0, 1); PG8_SCHED; PG8_LDA(At, 0, 0); PG8_STAGE(PG8_SA(1, 1), a1 + hstepA, voffA);
;             PG8_WAIT_V(8); PG8_WAIT_L(0); PG8_BAR; PG8_MMA(0, 0, At, B0); PG8_MMA(0, 1, At, B1); PG8_BAR; PG8_SCHED;
;             PG8_LDA(At, 0, 1); PG8_STAGE(PG8_SB(0, 0), b2, voffB); PG8_STAGE(PG8_SB(0, 1), b2 + hstepB, voffB); PG8_STAGE(PG8_SA(0, 0), a2, voffA);
;             PG8_WAIT_V(8); PG8_WAIT_L(0); PG8_BAR; PG8_MMA(1, 0, At, B0); PG8_MMA(1, 1, At, B1); PG8_BAR; PG8_SCHED;
;             PG8_LDB(B0, 1, 0); PG8_LDB(B1, 1, 1); PG8_SCHED; PG8_LDA(At, 1, 0); PG8_STAGE(PG8_SA(0, 1), a2 + hstepA, voffA);
;             PG8_WAIT_V(8); PG8_WAIT_L(0); PG8_BAR; PG8_MMA(0, 0, At, B0); PG8_MMA(0, 1, At, B1); PG8_BAR; PG8_SCHED;
;             PG8_LDA(At, 1, 1); PG8_STAGE(PG8_SB(1, 0), b3, voffB); PG8_STAGE(PG8_SB(1, 1), b3 + hstepB, voffB); PG8_STAGE(PG8_SA(1, 0), a3, voffA);
;             PG8_WAIT_V(8); PG8_WAIT_L(0); PG8_BAR; PG8_MMA(1, 0, At, B0); PG8_MMA(1, 1, At, B1); PG8_BAR; PG8_SCHED;
	s_add_i32 s58, 0, 0x18000
	s_add_i32 s59, 0, 0x1c000
	v_add_u32_e32 v160, s58, v165
	v_add_u32_e32 v171, s59, v165
	ds_read_b128 v[148:151], v160
	ds_read_b128 v[152:155], v160 offset:1024
	ds_read_b128 v[156:159], v160 offset:2048
	ds_read_b128 v[160:163], v160 offset:3072
	ds_read_b128 v[172:175], v171
	ds_read_b128 v[176:179], v171 offset:1024
	ds_read_b128 v[180:183], v171 offset:2048
	ds_read_b128 v[184:187], v171 offset:3072
	s_add_u32 s28, s28, 0x40000
	s_addc_u32 s29, s29, 0
	s_mov_b32 m0, s38
	ds_read_b128 v[188:191], v168 offset:32768
	ds_read_b128 v[192:195], v168 offset:33792
	ds_read_b128 v[196:199], v168 offset:34816
	ds_read_b128 v[200:203], v168 offset:35840
	ds_read_b128 v[204:207], v168 offset:36864
	ds_read_b128 v[208:211], v168 offset:37888
	ds_read_b128 v[212:215], v168 offset:38912
	ds_read_b128 v[216:219], v168 offset:39936
	global_load_lds_dwordx4 v134, s[28:29]
	s_mov_b32 m0, s39
	s_nop 0
	global_load_lds_dwordx4 v130, s[28:29]
	s_waitcnt vmcnt(8) lgkmcnt(0)
	s_barrier
	s_setprio 1
	v_mfma_f32_16x16x32_bf16 v[124:127], v[148:151], v[188:191], v[124:127]
	v_mfma_f32_16x16x32_bf16 v[116:119], v[156:159], v[188:191], v[116:119]
	v_mfma_f32_16x16x32_bf16 v[108:111], v[148:151], v[196:199], v[108:111]
	v_mfma_f32_16x16x32_bf16 v[100:103], v[156:159], v[196:199], v[100:103]
	v_mfma_f32_16x16x32_bf16 v[92:95], v[148:151], v[204:207], v[92:95]
	v_mfma_f32_16x16x32_bf16 v[84:87], v[156:159], v[204:207], v[84:87]
	v_mfma_f32_16x16x32_bf16 v[76:79], v[148:151], v[212:215], v[76:79]
	v_mfma_f32_16x16x32_bf16 v[68:71], v[156:159], v[212:215], v[68:71]
	v_mfma_f32_16x16x32_bf16 v[124:127], v[152:155], v[192:195], v[124:127]
	v_mfma_f32_16x16x32_bf16 v[116:119], v[160:163], v[192:195], v[116:119]
	v_mfma_f32_16x16x32_bf16 v[108:111], v[152:155], v[200:203], v[108:111]
	v_mfma_f32_16x16x32_bf16 v[100:103], v[160:163], v[200:203], v[100:103]
	v_mfma_f32_16x16x32_bf16 v[92:95], v[152:155], v[208:211], v[92:95]
	v_mfma_f32_16x16x32_bf16 v[84:87], v[160:163], v[208:211], v[84:87]
	v_mfma_f32_16x16x32_bf16 v[76:79], v[152:155], v[216:219], v[76:79]
	v_mfma_f32_16x16x32_bf16 v[68:71], v[160:163], v[216:219], v[68:71]
	s_setprio 0
	s_setprio 1
	v_mfma_f32_16x16x32_bf16 v[120:123], v[172:175], v[188:191], v[120:123]
	v_mfma_f32_16x16x32_bf16 v[112:115], v[180:183], v[188:191], v[112:115]
	v_mfma_f32_16x16x32_bf16 v[104:107], v[172:175], v[196:199], v[104:107]
	v_mfma_f32_16x16x32_bf16 v[96:99], v[180:183], v[196:199], v[96:99]
	v_mfma_f32_16x16x32_bf16 v[88:91], v[172:175], v[204:207], v[88:91]
	v_mfma_f32_16x16x32_bf16 v[80:83], v[180:183], v[204:207], v[80:83]
	v_mfma_f32_16x16x32_bf16 v[72:75], v[172:175], v[212:215], v[72:75]
	v_mfma_f32_16x16x32_bf16 v[64:67], v[180:183], v[212:215], v[64:67]
	v_mfma_f32_16x16x32_bf16 v[120:123], v[176:179], v[192:195], v[120:123]
	v_mfma_f32_16x16x32_bf16 v[112:115], v[184:187], v[192:195], v[112:115]
	v_mfma_f32_16x16x32_bf16 v[104:107], v[176:179], v[200:203], v[104:107]
	v_mfma_f32_16x16x32_bf16 v[96:99], v[184:187], v[200:203], v[96:99]
	v_mfma_f32_16x16x32_bf16 v[88:91], v[176:179], v[208:211], v[88:91]
	v_mfma_f32_16x16x32_bf16 v[80:83], v[184:187], v[208:211], v[80:83]
	v_mfma_f32_16x16x32_bf16 v[72:75], v[176:179], v[216:219], v[72:75]
	v_mfma_f32_16x16x32_bf16 v[64:67], v[184:187], v[216:219], v[64:67]
	s_setprio 0
	s_barrier
	s_add_i32 s28, s58, s33
	s_mov_b32 m0, s28
	ds_read_b128 v[188:191], v168 offset:49152
	ds_read_b128 v[192:195], v168 offset:50176
	ds_read_b128 v[196:199], v168 offset:51200
	ds_read_b128 v[200:203], v168 offset:52224
	ds_read_b128 v[204:207], v168 offset:53248
	ds_read_b128 v[208:211], v168 offset:54272
	ds_read_b128 v[212:215], v168 offset:55296
	ds_read_b128 v[216:219], v168 offset:56320
	global_load_lds_dwordx4 v132, s[98:99]
	s_add_i32 m0, s28, 0x2000
	s_add_u32 s26, s26, 0x40080
	s_addc_u32 s27, s27, 0
	s_add_i32 s28, s59, s33
	global_load_lds_dwordx4 v128, s[98:99]
	s_mov_b32 m0, s28
	s_nop 0
	global_load_lds_dwordx4 v132, s[26:27]
	s_add_i32 m0, s28, 0x2000
	s_nop 0
	global_load_lds_dwordx4 v128, s[26:27]
	s_mov_b32 m0, s40
	s_nop 0
	global_load_lds_dwordx4 v134, s[100:101]
	s_mov_b32 m0, s41
	s_nop 0
	global_load_lds_dwordx4 v130, s[100:101]
	s_waitcnt vmcnt(8) lgkmcnt(0)
	s_barrier
	s_setprio 1
	v_mfma_f32_16x16x32_bf16 v[60:63], v[148:151], v[188:191], v[60:63]
	v_mfma_f32_16x16x32_bf16 v[52:55], v[156:159], v[188:191], v[52:55]
	v_mfma_f32_16x16x32_bf16 v[44:47], v[148:151], v[196:199], v[44:47]
	v_mfma_f32_16x16x32_bf16 v[36:39], v[156:159], v[196:199], v[36:39]
	v_mfma_f32_16x16x32_bf16 v[28:31], v[148:151], v[204:207], v[28:31]
	v_mfma_f32_16x16x32_bf16 v[20:23], v[156:159], v[204:207], v[20:23]
	v_mfma_f32_16x16x32_bf16 v[12:15], v[148:151], v[212:215], v[12:15]
	v_mfma_f32_16x16x32_bf16 v[4:7], v[156:159], v[212:215], v[4:7]
	v_mfma_f32_16x16x32_bf16 v[60:63], v[152:155], v[192:195], v[60:63]
	v_mfma_f32_16x16x32_bf16 v[52:55], v[160:163], v[192:195], v[52:55]
	v_mfma_f32_16x16x32_bf16 v[44:47], v[152:155], v[200:203], v[44:47]
	v_mfma_f32_16x16x32_bf16 v[36:39], v[160:163], v[200:203], v[36:39]
	v_mfma_f32_16x16x32_bf16 v[28:31], v[152:155], v[208:211], v[28:31]
	v_mfma_f32_16x16x32_bf16 v[20:23], v[160:163], v[208:211], v[20:23]
	v_mfma_f32_16x16x32_bf16 v[12:15], v[152:155], v[216:219], v[12:15]
	v_mfma_f32_16x16x32_bf16 v[4:7], v[160:163], v[216:219], v[4:7]
	s_setprio 0
	s_setprio 1
	v_mfma_f32_16x16x32_bf16 v[56:59], v[172:175], v[188:191], v[56:59]
	v_mfma_f32_16x16x32_bf16 v[48:51], v[180:183], v[188:191], v[48:51]
	v_mfma_f32_16x16x32_bf16 v[40:43], v[172:175], v[196:199], v[40:43]
	v_mfma_f32_16x16x32_bf16 v[32:35], v[180:183], v[196:199], v[32:35]
	v_mfma_f32_16x16x32_bf16 v[24:27], v[172:175], v[204:207], v[24:27]
	v_mfma_f32_16x16x32_bf16 v[16:19], v[180:183], v[204:207], v[16:19]
	v_mfma_f32_16x16x32_bf16 v[8:11], v[172:175], v[212:215], v[8:11]
	v_mfma_f32_16x16x32_bf16 v[0:3], v[180:183], v[212:215], v[0:3]
	v_mfma_f32_16x16x32_bf16 v[56:59], v[176:179], v[192:195], v[56:59]
	v_mfma_f32_16x16x32_bf16 v[48:51], v[184:187], v[192:195], v[48:51]
	v_mfma_f32_16x16x32_bf16 v[40:43], v[176:179], v[200:203], v[40:43]
	v_mfma_f32_16x16x32_bf16 v[32:35], v[184:187], v[200:203], v[32:35]
	v_mfma_f32_16x16x32_bf16 v[24:27], v[176:179], v[208:211], v[24:27]
	v_mfma_f32_16x16x32_bf16 v[16:19], v[184:187], v[208:211], v[16:19]
	v_mfma_f32_16x16x32_bf16 v[8:11], v[176:179], v[216:219], v[8:11]
	v_mfma_f32_16x16x32_bf16 v[0:3], v[184:187], v[216:219], v[0:3]
	s_setprio 0
	s_barrier
	s_add_i32 s57, s57, 2
	s_add_u32 s24, s24, 0x100
	s_addc_u32 s25, s25, 0
	s_add_u32 s49, s49, 0x100
	s_addc_u32 s56, s56, 0
	s_cmp_gt_u32 s57, 13
	s_cbranch_scc0 .LBB0_2812
	s_and_b64 vcc, exec, s[12:13]
	s_cbranch_vccz .LBB0_2815
	s_barrier

; #define PG8_STAGE(bufoff, gbase, voff) do { _Pragma("unroll") for (int _i = 0; _i < 2; ++_i) \
;         __builtin_amdgcn_global_load_lds((const unsigned*)((const char*)(gbase) + (voff)[_i]), (PG8_LAS unsigned*)(lds + (bufoff) + ldsw + _i * 8192), 16, 0, 0); } while (0)
; #define PG8_LDA(dst, b, h) do { _Pragma("unroll") for (int m = 0; m < 4; ++m) _Pragma("unroll") for (int k = 0; k < 2; ++k) dst[m][k] = *(const PG8_LAS bf16x8*)(lds + PG8_SA(b, h) + aoff + m * 2048 + k * 1024); } while (0)
; #define PG8_LDB(dst, b, h) do { _Pragma("unroll") for (int n = 0; n < 2; ++n) _Pragma("unroll") for (int k = 0; k < 2; ++k) dst[n][k] = *(const PG8_LAS bf16x8*)(lds + PG8_SB(b, h) + boff + n * 2048 + k * 1024); } while (0)
; #define PG8_WAIT_V(n) asm volatile("s_waitcnt vmcnt(" #n ")" ::: "memory")
; #define PG8_WAIT_L(n) asm volatile("s_waitcnt lgkmcnt(" #n ")" ::: "memory")
; #define PG8_BAR __builtin_amdgcn_s_barrier()
; #define PG8_SCHED __builtin_amdgcn_sched_barrier(0)
; template <class Epi, class Sched, bool ALIGN_EPI = false, bool SP2 = false>
; __device__ __forceinline__ void gemm_phase(PG8_LAS unsigned char* lds, const Gemm g, const Sched& S, const Epi& E, const int wid) {
;     ...
;         const bool has_next = S.next(ui + 1, nxt);
;         const char* nA = has_next ? (const char*)g.A + (size_t)nxt.pm * tstepA : cA; const char* nB = has_next ? (const char*)g.Bt + (size_t)nxt.pn * tstepB : cB;
;         for (int t = 0; t < nt; t += 2) {
;             const bool last = (t == nt - 2);
;             const char* a1 = cA + (size_t)(t + 1) * kstep;
;             const char* a2 = last ? nA : cA + (size_t)(t + 2) * kstep; const char* b2 = last ? nB : cB + (size_t)(t + 2) * kstep;
;             const char* a3 = a2 + kstep; const char* b3 = b2 + kstep;
;             if (last && has_next) S.a_ready(nxt);
;             if constexpr (SP2) {
;             PG8_LDB(B0, 0, 0); PG8_LDB(B1, 0, 1); PG8_SCHED; PG8_LDA(At, 0, 0); PG8_STAGE(PG8_SA(1, 1), a1 + hstepA, voffA);
;             PG8_WAIT_V(8); PG8_WAIT_L(0); PG8_BAR; PG8_MMA(0, 0, At, B0); PG8_MMA(0, 1, At, B1); PG8_BAR; PG8_SCHED;
;             PG8_LDA(At, 0, 1); PG8_STAGE(PG8_SB(0, 0), b2, voffB); PG8_STAGE(PG8_SB(0, 1), b2 + hstepB, voffB); PG8_STAGE(PG8_SA(0, 0), a2, voffA);
;             PG8_WAIT_V(8); PG8_WAIT_L(0); PG8_BAR; PG8_MMA(1, 0, At, B0); PG8_MMA(1, 1, At, B1); PG8_BAR; PG8_SCHED;
.LBB0_2897:
	ds_read_b128 v[128:131], v190
	ds_read_b128 v[132:135], v190 offset:1024
	ds_read_b128 v[136:139], v190 offset:2048
	ds_read_b128 v[140:143], v190 offset:3072
	ds_read_b128 v[144:147], v191
	ds_read_b128 v[148:151], v191 offset:1024
	ds_read_b128 v[172:175], v191 offset:2048
	ds_read_b128 v[176:179], v191 offset:3072
	s_add_u32 s24, s22, 0x100
	s_addc_u32 s25, s23, 0
	s_cmp_eq_u32 s58, 40
	s_cselect_b32 s29, s7, s25
	s_cselect_b32 s28, s6, s24
	s_cselect_b32 s27, s21, s57
	s_cselect_b32 s26, s20, s56
	s_add_i32 m0, s34, 0xc000
	ds_read_b128 v[180:183], v192
	ds_read_b128 v[184:187], v192 offset:1024
	ds_read_b128 v[194:197], v192 offset:2048
	ds_read_b128 v[198:201], v192 offset:3072
	ds_read_b128 v[202:205], v192 offset:4096
	ds_read_b128 v[206:209], v192 offset:5120
	ds_read_b128 v[210:213], v192 offset:6144
	ds_read_b128 v[214:217], v192 offset:7168
	global_load_lds_dwordx4 v164, s[22:23]
	s_add_i32 m0, s34, 0xe000
	s_nop 0
	global_load_lds_dwordx4 v166, s[22:23]
	s_waitcnt vmcnt(8) lgkmcnt(0)
	s_barrier
	s_setprio 1
	v_mfma_f32_16x16x32_bf16 v[124:127], v[128:131], v[180:183], v[124:127]
	v_mfma_f32_16x16x32_bf16 v[120:123], v[136:139], v[180:183], v[120:123]
	v_mfma_f32_16x16x32_bf16 v[108:111], v[128:131], v[194:197], v[108:111]
	v_mfma_f32_16x16x32_bf16 v[104:107], v[136:139], v[194:197], v[104:107]
	v_mfma_f32_16x16x32_bf16 v[92:95], v[128:131], v[202:205], v[92:95]
	v_mfma_f32_16x16x32_bf16 v[88:91], v[136:139], v[202:205], v[88:91]
	v_mfma_f32_16x16x32_bf16 v[76:79], v[128:131], v[210:213], v[76:79]
	v_mfma_f32_16x16x32_bf16 v[72:75], v[136:139], v[210:213], v[72:75]
	v_mfma_f32_16x16x32_bf16 v[124:127], v[132:135], v[184:187], v[124:127]
	v_mfma_f32_16x16x32_bf16 v[120:123], v[140:143], v[184:187], v[120:123]
	v_mfma_f32_16x16x32_bf16 v[108:111], v[132:135], v[198:201], v[108:111]
	v_mfma_f32_16x16x32_bf16 v[104:107], v[140:143], v[198:201], v[104:107]
	v_mfma_f32_16x16x32_bf16 v[92:95], v[132:135], v[206:209], v[92:95]
	v_mfma_f32_16x16x32_bf16 v[88:91], v[140:143], v[206:209], v[88:91]
	v_mfma_f32_16x16x32_bf16 v[76:79], v[132:135], v[214:217], v[76:79]
	v_mfma_f32_16x16x32_bf16 v[72:75], v[140:143], v[214:217], v[72:75]
	s_setprio 0
	s_setprio 1
	v_mfma_f32_16x16x32_bf16 v[116:119], v[144:147], v[180:183], v[116:119]
	v_mfma_f32_16x16x32_bf16 v[112:115], v[172:175], v[180:183], v[112:115]
	v_mfma_f32_16x16x32_bf16 v[100:103], v[144:147], v[194:197], v[100:103]
	v_mfma_f32_16x16x32_bf16 v[96:99], v[172:175], v[194:197], v[96:99]
	v_mfma_f32_16x16x32_bf16 v[84:87], v[144:147], v[202:205], v[84:87]
	v_mfma_f32_16x16x32_bf16 v[80:83], v[172:175], v[202:205], v[80:83]
	v_mfma_f32_16x16x32_bf16 v[68:71], v[144:147], v[210:213], v[68:71]
	v_mfma_f32_16x16x32_bf16 v[64:67], v[172:175], v[210:213], v[64:67]
	v_mfma_f32_16x16x32_bf16 v[116:119], v[148:151], v[184:187], v[116:119]
	v_mfma_f32_16x16x32_bf16 v[112:115], v[176:179], v[184:187], v[112:115]
	v_mfma_f32_16x16x32_bf16 v[100:103], v[148:151], v[198:201], v[100:103]
	v_mfma_f32_16x16x32_bf16 v[96:99], v[176:179], v[198:201], v[96:99]
	v_mfma_f32_16x16x32_bf16 v[84:87], v[148:151], v[206:209], v[84:87]
	v_mfma_f32_16x16x32_bf16 v[80:83], v[176:179], v[206:209], v[80:83]
	v_mfma_f32_16x16x32_bf16 v[68:71], v[148:151], v[214:217], v[68:71]
	v_mfma_f32_16x16x32_bf16 v[64:67], v[176:179], v[214:217], v[64:67]
	s_setprio 0
	s_barrier
	s_add_i32 s22, s43, s33
	s_add_u32 s98, s26, 0x80
	s_addc_u32 s99, s27, 0
	s_mov_b32 m0, s22
	ds_read_b128 v[180:183], v192 offset:16384
	ds_read_b128 v[184:187], v192 offset:17408
	ds_read_b128 v[194:197], v192 offset:18432
	ds_read_b128 v[198:201], v192 offset:19456
	ds_read_b128 v[202:205], v192 offset:20480
	ds_read_b128 v[206:209], v192 offset:21504
	ds_read_b128 v[210:213], v192 offset:22528
	ds_read_b128 v[214:217], v192 offset:23552
	global_load_lds_dwordx4 v154, s[26:27]
	s_add_i32 m0, s22, 0x2000
	s_add_u32 s22, s26, 0xb0000
	s_addc_u32 s23, s27, 0
	s_add_i32 s59, s44, s33
	global_load_lds_dwordx4 v158, s[26:27]
	s_mov_b32 m0, s59
	s_add_u32 s100, s28, 0x80
	s_addc_u32 s101, s29, 0
	global_load_lds_dwordx4 v154, s[22:23]
	s_add_i32 m0, s59, 0x2000
	s_nop 0
	global_load_lds_dwordx4 v158, s[22:23]
	s_mov_b32 m0, s34
	s_nop 0
	global_load_lds_dwordx4 v152, s[28:29]
	s_mov_b32 m0, s35
	s_nop 0
	global_load_lds_dwordx4 v156, s[28:29]
	s_waitcnt vmcnt(8) lgkmcnt(0)
	s_barrier
	s_setprio 1
	v_mfma_f32_16x16x32_bf16 v[60:63], v[128:131], v[180:183], v[60:63]
	v_mfma_f32_16x16x32_bf16 v[56:59], v[136:139], v[180:183], v[56:59]
	v_mfma_f32_16x16x32_bf16 v[44:47], v[128:131], v[194:197], v[44:47]
	v_mfma_f32_16x16x32_bf16 v[40:43], v[136:139], v[194:197], v[40:43]
	v_mfma_f32_16x16x32_bf16 v[28:31], v[128:131], v[202:205], v[28:31]
	v_mfma_f32_16x16x32_bf16 v[24:27], v[136:139], v[202:205], v[24:27]
	v_mfma_f32_16x16x32_bf16 v[12:15], v[128:131], v[210:213], v[12:15]
	v_mfma_f32_16x16x32_bf16 v[8:11], v[136:139], v[210:213], v[8:11]
	v_mfma_f32_16x16x32_bf16 v[60:63], v[132:135], v[184:187], v[60:63]
	v_mfma_f32_16x16x32_bf16 v[56:59], v[140:143], v[184:187], v[56:59]
	v_mfma_f32_16x16x32_bf16 v[44:47], v[132:135], v[198:201], v[44:47]
	v_mfma_f32_16x16x32_bf16 v[40:43], v[140:143], v[198:201], v[40:43]
	v_mfma_f32_16x16x32_bf16 v[28:31], v[132:135], v[206:209], v[28:31]
	v_mfma_f32_16x16x32_bf16 v[24:27], v[140:143], v[206:209], v[24:27]
	v_mfma_f32_16x16x32_bf16 v[12:15], v[132:135], v[214:217], v[12:15]
	v_mfma_f32_16x16x32_bf16 v[8:11], v[140:143], v[214:217], v[8:11]
	s_setprio 0
	s_setprio 1
	v_mfma_f32_16x16x32_bf16 v[52:55], v[144:147], v[180:183], v[52:55]
	v_mfma_f32_16x16x32_bf16 v[48:51], v[172:175], v[180:183], v[48:51]
	v_mfma_f32_16x16x32_bf16 v[36:39], v[144:147], v[194:197], v[36:39]
	v_mfma_f32_16x16x32_bf16 v[32:35], v[172:175], v[194:197], v[32:35]
	v_mfma_f32_16x16x32_bf16 v[20:23], v[144:147], v[202:205], v[20:23]
	v_mfma_f32_16x16x32_bf16 v[16:19], v[172:175], v[202:205], v[16:19]
	v_mfma_f32_16x16x32_bf16 v[4:7], v[144:147], v[210:213], v[4:7]
	v_mfma_f32_16x16x32_bf16 v[0:3], v[172:175], v[210:213], v[0:3]
	v_mfma_f32_16x16x32_bf16 v[52:55], v[148:151], v[184:187], v[52:55]
	v_mfma_f32_16x16x32_bf16 v[48:51], v[176:179], v[184:187], v[48:51]
	v_mfma_f32_16x16x32_bf16 v[36:39], v[148:151], v[198:201], v[36:39]
	v_mfma_f32_16x16x32_bf16 v[32:35], v[176:179], v[198:201], v[32:35]
	v_mfma_f32_16x16x32_bf16 v[20:23], v[148:151], v[206:209], v[20:23]
	v_mfma_f32_16x16x32_bf16 v[16:19], v[176:179], v[206:209], v[16:19]
	v_mfma_f32_16x16x32_bf16 v[4:7], v[148:151], v[214:217], v[4:7]
	v_mfma_f32_16x16x32_bf16 v[0:3], v[176:179], v[214:217], v[0:3]
	s_setprio 0
	s_barrier
; #define PG8_STAGE(bufoff, gbase, voff) do { _Pragma("unroll") for (int _i = 0; _i < 2; ++_i) \
;         __builtin_amdgcn_global_load_lds((const unsigned*)((const char*)(gbase) + (voff)[_i]), (PG8_LAS unsigned*)(lds + (bufoff) + ldsw + _i * 8192), 16, 0, 0); } while (0)
; #define PG8_LDA(dst, b, h) do { _Pragma("unroll") for (int m = 0; m < 4; ++m) _Pragma("unroll") for (int k = 0; k < 2; ++k) dst[m][k] = *(const PG8_LAS bf16x8*)(lds + PG8_SA(b, h) + aoff + m * 2048 + k * 1024); } while (0)
; #define PG8_WAIT_V(n) asm volatile("s_waitcnt vmcnt(" #n ")" ::: "memory")
; #define PG8_WAIT_L(n) asm volatile("s_waitcnt lgkmcnt(" #n ")" ::: "memory")
; #define PG8_BAR __builtin_amdgcn_s_barrier()
; template <class Epi, class Sched, bool ALIGN_EPI = false, bool SP2 = false>
; __device__ __forceinline__ void gemm_phase(PG8_LAS unsigned char* lds, const Gemm g, const Sched& S, const Epi& E, const int wid) {
;     ...
;         for (int t = 0; t < nt; t += 2) {
;             const bool last = (t == nt - 2);
;             const char* a1 = cA + (size_t)(t + 1) * kstep;
;             const char* a2 = last ? nA : cA + (size_t)(t + 2) * kstep; const char* b2 = last ? nB : cB + (size_t)(t + 2) * kstep;
;             const char* a3 = a2 + kstep; const char* b3 = b2 + kstep;
;             if (last && has_next) S.a_ready(nxt);
;             if constexpr (SP2) {
;             PG8_LDB(B0, 0, 0); PG8_LDB(B1, 0, 1); PG8_SCHED; PG8_LDA(At, 0, 0); PG8_STAGE(PG8_SA(1, 1), a1 + hstepA, voffA);
;             PG8_WAIT_V(8); PG8_WAIT_L(0); PG8_BAR; PG8_MMA(0, 0, At, B0); PG8_MMA(0, 1, At, B1); PG8_BAR; PG8_SCHED;
;             PG8_LDA(At, 0, 1); PG8_STAGE(PG8_SB(0, 0), b2, voffB); PG8_STAGE(PG8_SB(0, 1), b2 + hstepB, voffB); PG8_STAGE(PG8_SA(0, 0), a2, voffA);
;             PG8_WAIT_V(8); PG8_WAIT_L(0); PG8_BAR; PG8_MMA(1, 0, At, B0); PG8_MMA(1, 1, At, B1); PG8_BAR; PG8_SCHED;
;             PG8_LDB(B0, 1, 0); PG8_LDB(B1, 1, 1); PG8_SCHED; PG8_LDA(At, 1, 0); PG8_STAGE(PG8_SA(0, 1), a2 + hstepA, voffA);
;             PG8_WAIT_V(8); PG8_WAIT_L(0); PG8_BAR; PG8_MMA(0, 0, At, B0); PG8_MMA(0, 1, At, B1); PG8_BAR; PG8_SCHED;
;             PG8_LDA(At, 1, 1); PG8_STAGE(PG8_SB(1, 0), b3, voffB); PG8_STAGE(PG8_SB(1, 1), b3 + hstepB, voffB); PG8_STAGE(PG8_SA(1, 0), a3, voffA);
;             PG8_WAIT_V(8); PG8_WAIT_L(0); PG8_BAR; PG8_MMA(1, 0, At, B0); PG8_MMA(1, 1, At, B1); PG8_BAR; PG8_SCHED;
	s_add_i32 s59, 0, 0x18000
	s_add_i32 s60, 0, 0x1c000
	v_add_u32_e32 v140, s59, v189
	v_add_u32_e32 v176, s60, v189
	ds_read_b128 v[128:131], v140
	ds_read_b128 v[132:135], v140 offset:1024
	ds_read_b128 v[136:139], v140 offset:2048
	ds_read_b128 v[140:143], v140 offset:3072
	ds_read_b128 v[144:147], v176
	ds_read_b128 v[148:151], v176 offset:1024
	ds_read_b128 v[172:175], v176 offset:2048
	ds_read_b128 v[176:179], v176 offset:3072
	s_add_u32 s22, s28, 0xb0000
	s_addc_u32 s23, s29, 0
	s_mov_b32 m0, s36
	ds_read_b128 v[180:183], v192 offset:32768
	ds_read_b128 v[184:187], v192 offset:33792
	ds_read_b128 v[194:197], v192 offset:34816
	ds_read_b128 v[198:201], v192 offset:35840
	ds_read_b128 v[202:205], v192 offset:36864
	ds_read_b128 v[206:209], v192 offset:37888
	ds_read_b128 v[210:213], v192 offset:38912
	ds_read_b128 v[214:217], v192 offset:39936
	global_load_lds_dwordx4 v152, s[22:23]
	s_mov_b32 m0, s37
	s_nop 0
	global_load_lds_dwordx4 v156, s[22:23]
	s_waitcnt vmcnt(8) lgkmcnt(0)
	s_barrier
	s_setprio 1
	v_mfma_f32_16x16x32_bf16 v[124:127], v[128:131], v[180:183], v[124:127]
	v_mfma_f32_16x16x32_bf16 v[120:123], v[136:139], v[180:183], v[120:123]
	v_mfma_f32_16x16x32_bf16 v[108:111], v[128:131], v[194:197], v[108:111]
	v_mfma_f32_16x16x32_bf16 v[104:107], v[136:139], v[194:197], v[104:107]
	v_mfma_f32_16x16x32_bf16 v[92:95], v[128:131], v[202:205], v[92:95]
	v_mfma_f32_16x16x32_bf16 v[88:91], v[136:139], v[202:205], v[88:91]
	v_mfma_f32_16x16x32_bf16 v[76:79], v[128:131], v[210:213], v[76:79]
	v_mfma_f32_16x16x32_bf16 v[72:75], v[136:139], v[210:213], v[72:75]
	v_mfma_f32_16x16x32_bf16 v[124:127], v[132:135], v[184:187], v[124:127]
	v_mfma_f32_16x16x32_bf16 v[120:123], v[140:143], v[184:187], v[120:123]
	v_mfma_f32_16x16x32_bf16 v[108:111], v[132:135], v[198:201], v[108:111]
	v_mfma_f32_16x16x32_bf16 v[104:107], v[140:143], v[198:201], v[104:107]
	v_mfma_f32_16x16x32_bf16 v[92:95], v[132:135], v[206:209], v[92:95]
	v_mfma_f32_16x16x32_bf16 v[88:91], v[140:143], v[206:209], v[88:91]
	v_mfma_f32_16x16x32_bf16 v[76:79], v[132:135], v[214:217], v[76:79]
	v_mfma_f32_16x16x32_bf16 v[72:75], v[140:143], v[214:217], v[72:75]
	s_setprio 0
	s_setprio 1
	v_mfma_f32_16x16x32_bf16 v[116:119], v[144:147], v[180:183], v[116:119]
	v_mfma_f32_16x16x32_bf16 v[112:115], v[172:175], v[180:183], v[112:115]
	v_mfma_f32_16x16x32_bf16 v[100:103], v[144:147], v[194:197], v[100:103]
	v_mfma_f32_16x16x32_bf16 v[96:99], v[172:175], v[194:197], v[96:99]
	v_mfma_f32_16x16x32_bf16 v[84:87], v[144:147], v[202:205], v[84:87]
	v_mfma_f32_16x16x32_bf16 v[80:83], v[172:175], v[202:205], v[80:83]
	v_mfma_f32_16x16x32_bf16 v[68:71], v[144:147], v[210:213], v[68:71]
	v_mfma_f32_16x16x32_bf16 v[64:67], v[172:175], v[210:213], v[64:67]
	v_mfma_f32_16x16x32_bf16 v[116:119], v[148:151], v[184:187], v[116:119]
	v_mfma_f32_16x16x32_bf16 v[112:115], v[176:179], v[184:187], v[112:115]
	v_mfma_f32_16x16x32_bf16 v[100:103], v[148:151], v[198:201], v[100:103]
	v_mfma_f32_16x16x32_bf16 v[96:99], v[176:179], v[198:201], v[96:99]
	v_mfma_f32_16x16x32_bf16 v[84:87], v[148:151], v[206:209], v[84:87]
	v_mfma_f32_16x16x32_bf16 v[80:83], v[176:179], v[206:209], v[80:83]
	v_mfma_f32_16x16x32_bf16 v[68:71], v[148:151], v[214:217], v[68:71]
	v_mfma_f32_16x16x32_bf16 v[64:67], v[176:179], v[214:217], v[64:67]
	s_setprio 0
	s_barrier
	s_add_i32 s22, s59, s33
	s_mov_b32 m0, s22
	ds_read_b128 v[180:183], v192 offset:49152
	ds_read_b128 v[184:187], v192 offset:50176
	ds_read_b128 v[194:197], v192 offset:51200
	ds_read_b128 v[198:201], v192 offset:52224
	ds_read_b128 v[202:205], v192 offset:53248
	ds_read_b128 v[206:209], v192 offset:54272
	ds_read_b128 v[210:213], v192 offset:55296
	ds_read_b128 v[214:217], v192 offset:56320
	global_load_lds_dwordx4 v154, s[98:99]
	s_add_i32 m0, s22, 0x2000
	s_add_u32 s22, s26, 0xb0080
	s_addc_u32 s23, s27, 0
	s_add_i32 s26, s60, s33
	global_load_lds_dwordx4 v158, s[98:99]
	s_mov_b32 m0, s26
	s_nop 0
	global_load_lds_dwordx4 v154, s[22:23]
	s_add_i32 m0, s26, 0x2000
	s_nop 0
	global_load_lds_dwordx4 v158, s[22:23]
	s_mov_b32 m0, s39
	s_nop 0
	global_load_lds_dwordx4 v152, s[100:101]
	s_mov_b32 m0, s40
	s_nop 0
	global_load_lds_dwordx4 v156, s[100:101]
	s_waitcnt vmcnt(8) lgkmcnt(0)
	s_barrier
	s_setprio 1
	v_mfma_f32_16x16x32_bf16 v[60:63], v[128:131], v[180:183], v[60:63]
	v_mfma_f32_16x16x32_bf16 v[56:59], v[136:139], v[180:183], v[56:59]
	v_mfma_f32_16x16x32_bf16 v[44:47], v[128:131], v[194:197], v[44:47]
	v_mfma_f32_16x16x32_bf16 v[40:43], v[136:139], v[194:197], v[40:43]
	v_mfma_f32_16x16x32_bf16 v[28:31], v[128:131], v[202:205], v[28:31]
	v_mfma_f32_16x16x32_bf16 v[24:27], v[136:139], v[202:205], v[24:27]
	v_mfma_f32_16x16x32_bf16 v[12:15], v[128:131], v[210:213], v[12:15]
	v_mfma_f32_16x16x32_bf16 v[8:11], v[136:139], v[210:213], v[8:11]
	v_mfma_f32_16x16x32_bf16 v[60:63], v[132:135], v[184:187], v[60:63]
	v_mfma_f32_16x16x32_bf16 v[56:59], v[140:143], v[184:187], v[56:59]
	v_mfma_f32_16x16x32_bf16 v[44:47], v[132:135], v[198:201], v[44:47]
	v_mfma_f32_16x16x32_bf16 v[40:43], v[140:143], v[198:201], v[40:43]
	v_mfma_f32_16x16x32_bf16 v[28:31], v[132:135], v[206:209], v[28:31]
	v_mfma_f32_16x16x32_bf16 v[24:27], v[140:143], v[206:209], v[24:27]
	v_mfma_f32_16x16x32_bf16 v[12:15], v[132:135], v[214:217], v[12:15]
	v_mfma_f32_16x16x32_bf16 v[8:11], v[140:143], v[214:217], v[8:11]
	s_setprio 0
	s_setprio 1
	v_mfma_f32_16x16x32_bf16 v[52:55], v[144:147], v[180:183], v[52:55]
	v_mfma_f32_16x16x32_bf16 v[48:51], v[172:175], v[180:183], v[48:51]
	v_mfma_f32_16x16x32_bf16 v[36:39], v[144:147], v[194:197], v[36:39]
	v_mfma_f32_16x16x32_bf16 v[32:35], v[172:175], v[194:197], v[32:35]
	v_mfma_f32_16x16x32_bf16 v[20:23], v[144:147], v[202:205], v[20:23]
	v_mfma_f32_16x16x32_bf16 v[16:19], v[172:175], v[202:205], v[16:19]
	v_mfma_f32_16x16x32_bf16 v[4:7], v[144:147], v[210:213], v[4:7]
	v_mfma_f32_16x16x32_bf16 v[0:3], v[172:175], v[210:213], v[0:3]
	v_mfma_f32_16x16x32_bf16 v[52:55], v[148:151], v[184:187], v[52:55]
	v_mfma_f32_16x16x32_bf16 v[48:51], v[176:179], v[184:187], v[48:51]
	v_mfma_f32_16x16x32_bf16 v[36:39], v[148:151], v[198:201], v[36:39]
	v_mfma_f32_16x16x32_bf16 v[32:35], v[176:179], v[198:201], v[32:35]
	v_mfma_f32_16x16x32_bf16 v[20:23], v[148:151], v[206:209], v[20:23]
	v_mfma_f32_16x16x32_bf16 v[16:19], v[176:179], v[206:209], v[16:19]
	v_mfma_f32_16x16x32_bf16 v[4:7], v[148:151], v[214:217], v[4:7]
	v_mfma_f32_16x16x32_bf16 v[0:3], v[176:179], v[214:217], v[0:3]
	s_setprio 0
	s_barrier
	s_add_i32 s58, s58, 2
	s_add_u32 s56, s56, 0x100
	s_addc_u32 s57, s57, 0
	s_cmp_gt_u32 s58, 41
	s_mov_b64 s[22:23], s[24:25]
	s_cbranch_scc0 .LBB0_2897
	s_and_b64 vcc, exec, s[18:19]
	s_cbranch_vccz .LBB0_2900
	s_barrier
